# epilogue: LDS-transpose tails software-pipelined across row blocks; store-only vmcnt waits removed
# speedup vs baseline: 1.0161x; 1.0040x over previous
.LBB2_5:
	s_mul_i32 s4, s14, 0xc000
	s_add_i32 s5, s4, 0
	s_add_i32 s16, s5, s11
	s_add_i32 s5, s5, s13
	v_add_u32_e32 v134, s5, v89
	s_waitcnt vmcnt(6)
	s_barrier
	v_add_u32_e32 v118, v134, v87
	ds_read_b128 v[102:105], v118 offset:16384
	ds_read_b128 v[110:113], v118 offset:18432
	v_add_u32_e32 v130, s16, v89
	v_add_u32_e32 v126, v130, v87
	ds_read_b128 v[106:109], v126
	s_waitcnt lgkmcnt(0)
	v_mfma_f32_16x16x32_f16 v[18:21], v[102:105], v[106:109], v[18:21]
	ds_read_b128 v[114:117], v118 offset:20480
	v_add_u32_e32 v150, v130, v85
	v_add_u32_e32 v142, v134, v85
	v_mfma_f32_16x16x32_f16 v[22:25], v[110:113], v[106:109], v[22:25]
	ds_read_b128 v[118:121], v118 offset:22528
	s_add_i32 s4, s4, 0xffff4000
	s_cmp_lg_u32 s14, 0
	s_waitcnt lgkmcnt(0)
	v_mfma_f32_16x16x32_f16 v[26:29], v[114:117], v[106:109], v[26:29]
	ds_read_b128 v[122:125], v126 offset:2048
	s_cselect_b32 s4, s4, 0x18000
	s_add_i32 s4, s4, 0
	v_mfma_f32_16x16x32_f16 v[30:33], v[118:121], v[106:109], v[30:33]
	ds_read_b128 v[106:109], v126 offset:4096
	s_add_i32 s5, s4, s9
	s_mov_b32 m0, s5
	s_waitcnt lgkmcnt(0)
	v_mfma_f32_16x16x32_f16 v[38:41], v[102:105], v[122:125], v[38:41]
	ds_read_b128 v[126:129], v126 offset:6144
	s_add_i32 s4, s4, s12
	v_mfma_f32_16x16x32_f16 v[42:45], v[110:113], v[122:125], v[42:45]
	ds_read_b128 v[130:133], v150
	v_mfma_f32_16x16x32_f16 v[50:53], v[114:117], v[122:125], v[50:53]
	ds_read_b128 v[134:137], v142 offset:16384
	v_mfma_f32_16x16x32_f16 v[46:49], v[118:121], v[122:125], v[46:49]
	ds_read_b128 v[122:125], v142 offset:18432
	v_mfma_f32_16x16x32_f16 v[54:57], v[102:105], v[106:109], v[54:57]
	ds_read_b128 v[138:141], v142 offset:20480
	v_mfma_f32_16x16x32_f16 v[58:61], v[110:113], v[106:109], v[58:61]
	ds_read_b128 v[142:145], v142 offset:22528
	v_mfma_f32_16x16x32_f16 v[62:65], v[114:117], v[106:109], v[62:65]
	ds_read_b128 v[146:149], v150 offset:2048
	v_mfma_f32_16x16x32_f16 v[66:69], v[118:121], v[106:109], v[66:69]
	ds_read_b128 v[106:109], v150 offset:4096
	s_waitcnt lgkmcnt(0)
	v_mfma_f32_16x16x32_f16 v[70:73], v[102:105], v[126:129], v[70:73]
	ds_read_b128 v[102:105], v150 offset:6144
	v_mfma_f32_16x16x32_f16 v[74:77], v[110:113], v[126:129], v[74:77]
	v_lshl_add_u64 v[110:111], v[100:101], 0, s[2:3]
	v_mfma_f32_16x16x32_f16 v[34:37], v[114:117], v[126:129], v[34:37]
	v_mfma_f32_16x16x32_f16 v[78:81], v[118:121], v[126:129], v[78:81]
	global_load_lds_dwordx4 v[110:111], off
	v_lshl_add_u64 v[110:111], v[98:99], 0, s[2:3]
	s_add_i32 m0, s5, 0x400
	v_mfma_f32_16x16x32_f16 v[18:21], v[134:137], v[130:133], v[18:21]
	v_mfma_f32_16x16x32_f16 v[22:25], v[122:125], v[130:133], v[22:25]
	v_mfma_f32_16x16x32_f16 v[26:29], v[138:141], v[130:133], v[26:29]
	global_load_lds_dwordx4 v[110:111], off
	v_lshl_add_u64 v[110:111], v[96:97], 0, s[2:3]
	s_add_i32 m0, s4, 0x4000
	v_mfma_f32_16x16x32_f16 v[30:33], v[142:145], v[130:133], v[30:33]
	v_mfma_f32_16x16x32_f16 v[38:41], v[134:137], v[146:149], v[38:41]
	v_mfma_f32_16x16x32_f16 v[42:45], v[122:125], v[146:149], v[42:45]
	global_load_lds_dwordx4 v[110:111], off
	v_lshl_add_u64 v[110:111], v[94:95], 0, s[2:3]
	s_add_i32 m0, s4, 0x4400
	v_mfma_f32_16x16x32_f16 v[50:53], v[138:141], v[146:149], v[50:53]
	v_mfma_f32_16x16x32_f16 v[46:49], v[142:145], v[146:149], v[46:49]
	v_mfma_f32_16x16x32_f16 v[54:57], v[134:137], v[106:109], v[54:57]
	global_load_lds_dwordx4 v[110:111], off
	v_lshl_add_u64 v[110:111], v[92:93], 0, s[2:3]
	s_add_i32 m0, s4, 0x4800
	v_mfma_f32_16x16x32_f16 v[58:61], v[122:125], v[106:109], v[58:61]
	v_mfma_f32_16x16x32_f16 v[62:65], v[138:141], v[106:109], v[62:65]
	v_mfma_f32_16x16x32_f16 v[66:69], v[142:145], v[106:109], v[66:69]
	global_load_lds_dwordx4 v[110:111], off
	v_lshl_add_u64 v[106:107], v[90:91], 0, s[2:3]
	s_add_i32 m0, s4, 0x4c00
	s_waitcnt lgkmcnt(0)
	v_mfma_f32_16x16x32_f16 v[70:73], v[134:137], v[102:105], v[70:73]
	s_add_i32 s4, s14, 1
	s_cmp_lg_u32 s14, 2
	s_cselect_b32 s14, s4, 0
	v_mfma_f32_16x16x32_f16 v[74:77], v[122:125], v[102:105], v[74:77]
	s_add_u32 s2, s2, 0x80
	s_addc_u32 s3, s3, 0
	s_cmp_eq_u32 s10, s2
	v_mfma_f32_16x16x32_f16 v[34:37], v[138:141], v[102:105], v[34:37]
	global_load_lds_dwordx4 v[106:107], off
	v_mfma_f32_16x16x32_f16 v[78:81], v[142:145], v[102:105], v[78:81]
	s_cbranch_scc0 .LBB2_5
	s_mul_i32 s3, s14, 0xc000
	v_or_b32_e32 v1, s8, v1
	s_add_i32 s2, s3, 0
	v_lshlrev_b32_e32 v1, 7, v1
	v_add_u32_e32 v122, s2, v1
	s_waitcnt vmcnt(6)
	s_barrier
	v_add_u32_e32 v106, v122, v87
	ds_read_b128 v[90:93], v106 offset:16384
	v_lshlrev_b32_e32 v89, 7, v83
	ds_read_b128 v[98:101], v106 offset:18432
	v_add_u32_e32 v118, s2, v89
	v_add_u32_e32 v114, v118, v87
	ds_read_b128 v[94:97], v114
	s_waitcnt lgkmcnt(0)
	v_mfma_f32_16x16x32_f16 v[18:21], v[90:93], v[94:97], v[18:21]
	ds_read_b128 v[102:105], v106 offset:20480
	v_add_u32_e32 v138, v118, v85
	v_add_u32_e32 v130, v122, v85
	v_mfma_f32_16x16x32_f16 v[22:25], v[98:101], v[94:97], v[22:25]
	ds_read_b128 v[106:109], v106 offset:22528
	s_lshr_b32 s2, s15, 8
	s_add_i32 s3, s3, 0xc000
	s_waitcnt lgkmcnt(0)
	v_mfma_f32_16x16x32_f16 v[26:29], v[102:105], v[94:97], v[26:29]
	ds_read_b128 v[110:113], v114 offset:2048
	s_cmp_lg_u32 s14, 2
	s_cselect_b32 s3, s3, 0
	v_mfma_f32_16x16x32_f16 v[30:33], v[106:109], v[94:97], v[30:33]
	ds_read_b128 v[94:97], v114 offset:4096
	s_add_i32 s3, s3, 0
	v_add_u32_e32 v1, s3, v1
	s_waitcnt lgkmcnt(0)
	v_mfma_f32_16x16x32_f16 v[38:41], v[90:93], v[110:113], v[38:41]
	ds_read_b128 v[114:117], v114 offset:6144
	v_add_u32_e32 v89, s3, v89
	s_lshl_b64 s[0:1], s[0:1], 1
	v_mfma_f32_16x16x32_f16 v[42:45], v[98:101], v[110:113], v[42:45]
	ds_read_b128 v[118:121], v138
	s_add_u32 s0, s6, s0
	s_addc_u32 s1, s7, s1
	v_mfma_f32_16x16x32_f16 v[50:53], v[102:105], v[110:113], v[50:53]
	ds_read_b128 v[122:125], v130 offset:16384
	s_lshl_b32 s3, s8, 1
	s_add_u32 s0, s0, s3
	v_mfma_f32_16x16x32_f16 v[46:49], v[106:109], v[110:113], v[46:49]
	ds_read_b128 v[110:113], v130 offset:18432
	s_addc_u32 s1, s1, 0
	v_lshlrev_b32_e32 v0, 1, v0
	v_mfma_f32_16x16x32_f16 v[54:57], v[90:93], v[94:97], v[54:57]
	ds_read_b128 v[126:129], v130 offset:20480
	v_cmp_gt_u32_e32 vcc, s2, v83
	v_mfma_f32_16x16x32_f16 v[58:61], v[98:101], v[94:97], v[58:61]
	ds_read_b128 v[130:133], v130 offset:22528
	v_mfma_f32_16x16x32_f16 v[62:65], v[102:105], v[94:97], v[62:65]
	ds_read_b128 v[134:137], v138 offset:2048
	v_mfma_f32_16x16x32_f16 v[66:69], v[106:109], v[94:97], v[66:69]
	ds_read_b128 v[94:97], v138 offset:4096
	s_waitcnt lgkmcnt(0)
	v_mfma_f32_16x16x32_f16 v[70:73], v[90:93], v[114:117], v[70:73]
	ds_read_b128 v[90:93], v138 offset:6144
	s_waitcnt vmcnt(0)
	s_barrier
	v_mfma_f32_16x16x32_f16 v[74:77], v[98:101], v[114:117], v[74:77]
	v_mfma_f32_16x16x32_f16 v[34:37], v[102:105], v[114:117], v[34:37]
	v_mfma_f32_16x16x32_f16 v[78:81], v[106:109], v[114:117], v[78:81]
	v_add_u32_e32 v106, v1, v87
	v_add_u32_e32 v87, v89, v87
	v_add_u32_e32 v1, v1, v85
	v_mfma_f32_16x16x32_f16 v[18:21], v[122:125], v[118:121], v[18:21]
	v_mfma_f32_16x16x32_f16 v[22:25], v[110:113], v[118:121], v[22:25]
	v_mfma_f32_16x16x32_f16 v[26:29], v[126:129], v[118:121], v[26:29]
	v_mfma_f32_16x16x32_f16 v[30:33], v[130:133], v[118:121], v[30:33]
	v_mfma_f32_16x16x32_f16 v[38:41], v[122:125], v[134:137], v[38:41]
	v_mfma_f32_16x16x32_f16 v[42:45], v[110:113], v[134:137], v[42:45]
	v_mfma_f32_16x16x32_f16 v[50:53], v[126:129], v[134:137], v[50:53]
	v_mfma_f32_16x16x32_f16 v[46:49], v[130:133], v[134:137], v[46:49]
	v_mfma_f32_16x16x32_f16 v[54:57], v[122:125], v[94:97], v[54:57]
	v_mfma_f32_16x16x32_f16 v[58:61], v[110:113], v[94:97], v[58:61]
	v_mfma_f32_16x16x32_f16 v[62:65], v[126:129], v[94:97], v[62:65]
	v_mfma_f32_16x16x32_f16 v[66:69], v[130:133], v[94:97], v[66:69]
	s_waitcnt lgkmcnt(0)
	v_mfma_f32_16x16x32_f16 v[70:73], v[122:125], v[90:93], v[70:73]
	v_mfma_f32_16x16x32_f16 v[74:77], v[110:113], v[90:93], v[74:77]
	v_mfma_f32_16x16x32_f16 v[34:37], v[126:129], v[90:93], v[34:37]
	v_mfma_f32_16x16x32_f16 v[78:81], v[130:133], v[90:93], v[78:81]
	ds_read_b128 v[90:93], v106 offset:16384
	ds_read_b128 v[98:101], v106 offset:18432
	ds_read_b128 v[94:97], v87
	s_waitcnt lgkmcnt(0)
	v_mfma_f32_16x16x32_f16 v[18:21], v[90:93], v[94:97], v[18:21]
	ds_read_b128 v[102:105], v106 offset:20480
	v_mfma_f32_16x16x32_f16 v[22:25], v[98:101], v[94:97], v[22:25]
	ds_read_b128 v[106:109], v106 offset:22528
	s_waitcnt lgkmcnt(0)
	v_mfma_f32_16x16x32_f16 v[26:29], v[102:105], v[94:97], v[26:29]
	ds_read_b128 v[110:113], v87 offset:2048
	v_mfma_f32_16x16x32_f16 v[30:33], v[106:109], v[94:97], v[30:33]
	ds_read_b128 v[94:97], v87 offset:4096
	s_waitcnt lgkmcnt(0)
	v_mfma_f32_16x16x32_f16 v[38:41], v[90:93], v[110:113], v[38:41]
	ds_read_b128 v[114:117], v87 offset:6144
	v_add_u32_e32 v87, v89, v85
	v_mfma_f32_16x16x32_f16 v[42:45], v[98:101], v[110:113], v[42:45]
	ds_read_b128 v[118:121], v87
	v_mfma_f32_16x16x32_f16 v[50:53], v[102:105], v[110:113], v[50:53]
	ds_read_b128 v[122:125], v1 offset:16384
	v_mfma_f32_16x16x32_f16 v[46:49], v[106:109], v[110:113], v[46:49]
	ds_read_b128 v[110:113], v1 offset:18432
	v_mfma_f32_16x16x32_f16 v[126:129], v[90:93], v[94:97], v[54:57]
	ds_read_b128 v[130:133], v1 offset:20480
	v_mfma_f32_16x16x32_f16 v[134:137], v[98:101], v[94:97], v[58:61]
	ds_read_b128 v[138:141], v1 offset:22528
	v_mov_b32_e32 v1, 0
	v_lshl_add_u64 v[0:1], s[0:1], 0, v[0:1]
	v_mfma_f32_16x16x32_f16 v[142:145], v[102:105], v[94:97], v[62:65]
	ds_read_b128 v[146:149], v87 offset:2048
	v_mfma_f32_16x16x32_f16 v[94:97], v[106:109], v[94:97], v[66:69]
	ds_read_b128 v[150:153], v87 offset:4096
	s_waitcnt lgkmcnt(0)
	v_mfma_f32_16x16x32_f16 v[90:93], v[90:93], v[114:117], v[70:73]
	ds_read_b128 v[154:157], v87 offset:6144
	v_mfma_f32_16x16x32_f16 v[98:101], v[98:101], v[114:117], v[74:77]
	v_mfma_f32_16x16x32_f16 v[102:105], v[102:105], v[114:117], v[34:37]
	v_mfma_f32_16x16x32_f16 v[106:109], v[106:109], v[114:117], v[78:81]
	v_mfma_f32_16x16x32_f16 v[78:81], v[122:125], v[118:121], v[18:21]
	v_mfma_f32_16x16x32_f16 v[74:77], v[110:113], v[118:121], v[22:25]
	v_mfma_f32_16x16x32_f16 v[70:73], v[130:133], v[118:121], v[26:29]
	v_mfma_f32_16x16x32_f16 v[66:69], v[138:141], v[118:121], v[30:33]
	v_mfma_f32_16x16x32_f16 v[62:65], v[122:125], v[146:149], v[38:41]
	v_mfma_f32_16x16x32_f16 v[58:61], v[110:113], v[146:149], v[42:45]
	v_mfma_f32_16x16x32_f16 v[54:57], v[130:133], v[146:149], v[50:53]
	v_mfma_f32_16x16x32_f16 v[50:53], v[138:141], v[146:149], v[46:49]
	v_mfma_f32_16x16x32_f16 v[46:49], v[122:125], v[150:153], v[126:129]
	v_mfma_f32_16x16x32_f16 v[42:45], v[110:113], v[150:153], v[134:137]
	v_mfma_f32_16x16x32_f16 v[38:41], v[130:133], v[150:153], v[142:145]
	v_mfma_f32_16x16x32_f16 v[34:37], v[138:141], v[150:153], v[94:97]
	s_waitcnt lgkmcnt(0)
	v_mfma_f32_16x16x32_f16 v[26:29], v[122:125], v[154:157], v[90:93]
	v_mfma_f32_16x16x32_f16 v[22:25], v[110:113], v[154:157], v[98:101]
	v_mfma_f32_16x16x32_f16 v[18:21], v[130:133], v[154:157], v[102:105]
	v_mfma_f32_16x16x32_f16 v[30:33], v[138:141], v[154:157], v[106:109]
	v_mbcnt_lo_u32_b32 v158, -1, 0
	v_mbcnt_hi_u32_b32 v158, -1, v158
	v_and_b32_e32 v159, 15, v158
	v_lshrrev_b32_e32 v160, 4, v158
	s_lshl_b32 s36, s23, 2
	s_add_u32 s36, s36, s22
	s_mulk_i32 s36, 0x900
	s_add_u32 s36, s36, 0x18000
	v_mul_u32_u24_e32 v161, 0x90, v159
	v_lshl_add_u32 v161, v160, 3, v161
	v_add_u32_e32 v161, s36, v161
	v_lshrrev_b32_e32 v162, 3, v158
	v_and_b32_e32 v163, 7, v158
	v_mul_u32_u24_e32 v164, 0x90, v162
	v_lshl_add_u32 v164, v163, 4, v164
	v_add_u32_e32 v164, s36, v164
	v_lshlrev_b32_e32 v165, 2, v162
	v_add_u32_e32 v166, 32, v165
	v_lshlrev_b32_e32 v182, 4, v163
	v_mov_b32_e32 v183, 0
	s_lshl_b32 s37, s23, 6
	v_add_u32_e32 v167, s37, v162
	s_mov_b64 s[0:1], exec
	s_cbranch_execz .LBB2_8
	s_waitcnt vmcnt(0)
	v_add_f32_e32 v79, v15, v79
	v_ashrrev_i32_e32 v89, 31, v88
	v_add_f32_e32 v78, v14, v78
	v_max_f32_e32 v85, 0, v79
	v_add_f32_e32 v79, v16, v80
	v_add_f32_e32 v80, v17, v81
	v_lshlrev_b64 v[88:89], 11, v[88:89]
	v_max_f32_e32 v78, 0, v78
	v_max_f32_e32 v79, 0, v79
	v_max_f32_e32 v80, 0, v80
	v_lshl_add_u64 v[88:89], v[0:1], 0, v[88:89]
	v_cvt_pk_f16_f32 v79, v79, v80
	v_cvt_pk_f16_f32 v78, v78, v85
	v_add_f32_e32 v75, v11, v75
	ds_write_b64 v161, v[78:79]
	v_add_f32_e32 v74, v10, v74
	v_max_f32_e32 v78, 0, v75
	v_add_f32_e32 v75, v12, v76
	v_add_f32_e32 v76, v13, v77
	v_max_f32_e32 v74, 0, v74
	v_max_f32_e32 v75, 0, v75
	v_max_f32_e32 v76, 0, v76
	v_cvt_pk_f16_f32 v75, v75, v76
	v_cvt_pk_f16_f32 v74, v74, v78
	v_add_f32_e32 v71, v7, v71
	ds_write_b64 v161, v[74:75] offset:32
	v_add_f32_e32 v70, v6, v70
	v_max_f32_e32 v74, 0, v71
	v_add_f32_e32 v71, v8, v72
	v_add_f32_e32 v72, v9, v73
	v_max_f32_e32 v70, 0, v70
	v_max_f32_e32 v71, 0, v71
	v_max_f32_e32 v72, 0, v72
	v_cvt_pk_f16_f32 v71, v71, v72
	v_cvt_pk_f16_f32 v70, v70, v74
	v_add_f32_e32 v67, v3, v67
	ds_write_b64 v161, v[70:71] offset:64
	v_add_f32_e32 v66, v2, v66
	v_max_f32_e32 v70, 0, v67
	v_add_f32_e32 v67, v4, v68
	v_add_f32_e32 v68, v5, v69
	v_max_f32_e32 v66, 0, v66
	v_max_f32_e32 v67, 0, v67
	v_max_f32_e32 v68, 0, v68
	v_cvt_pk_f16_f32 v67, v67, v68
	v_cvt_pk_f16_f32 v66, v66, v70
	ds_write_b64 v161, v[66:67] offset:96
	ds_read_b128 v[170:173], v164
	ds_read_b128 v[174:177], v164 offset:1152
	ds_bpermute_b32 v178, v165, v88
	ds_bpermute_b32 v179, v165, v89
	ds_bpermute_b32 v180, v166, v88
	ds_bpermute_b32 v181, v166, v89
	v_add_u32_e32 v184, 0, v167
	v_cmp_gt_u32_e64 s[38:39], s2, v184
	v_add_u32_e32 v184, 8, v184
	v_cmp_gt_u32_e64 s[40:41], s2, v184
.LBB2_8:
	s_or_b64 exec, exec, s[0:1]
	v_or_b32_e32 v66, 16, v83
	v_cmp_gt_u32_e32 vcc, s2, v66
	s_mov_b64 s[0:1], exec
	s_cbranch_execz .LBB2_10
	v_add_f32_e32 v63, v15, v63
	v_ashrrev_i32_e32 v87, 31, v86
	v_add_f32_e32 v62, v14, v62
	v_max_f32_e32 v68, 0, v63
	v_add_f32_e32 v63, v16, v64
	v_add_f32_e32 v64, v17, v65
	v_lshlrev_b64 v[66:67], 11, v[86:87]
	v_max_f32_e32 v62, 0, v62
	v_max_f32_e32 v63, 0, v63
	v_max_f32_e32 v64, 0, v64
	v_lshl_add_u64 v[66:67], v[0:1], 0, v[66:67]
	v_cvt_pk_f16_f32 v63, v63, v64
	v_cvt_pk_f16_f32 v62, v62, v68
	v_add_f32_e32 v59, v11, v59
	ds_write_b64 v161, v[62:63]
	v_add_f32_e32 v58, v10, v58
	v_max_f32_e32 v62, 0, v59
	v_add_f32_e32 v59, v12, v60
	v_add_f32_e32 v60, v13, v61
	v_max_f32_e32 v58, 0, v58
	v_max_f32_e32 v59, 0, v59
	v_max_f32_e32 v60, 0, v60
	v_cvt_pk_f16_f32 v59, v59, v60
	v_cvt_pk_f16_f32 v58, v58, v62
	v_add_f32_e32 v55, v7, v55
	ds_write_b64 v161, v[58:59] offset:32
	v_add_f32_e32 v54, v6, v54
	v_max_f32_e32 v58, 0, v55
	v_add_f32_e32 v55, v8, v56
	v_add_f32_e32 v56, v9, v57
	v_max_f32_e32 v54, 0, v54
	v_max_f32_e32 v55, 0, v55
	v_max_f32_e32 v56, 0, v56
	v_cvt_pk_f16_f32 v55, v55, v56
	v_cvt_pk_f16_f32 v54, v54, v58
	v_add_f32_e32 v51, v3, v51
	ds_write_b64 v161, v[54:55] offset:64
	v_add_f32_e32 v50, v2, v50
	v_max_f32_e32 v54, 0, v51
	v_add_f32_e32 v51, v4, v52
	v_add_f32_e32 v52, v5, v53
	v_max_f32_e32 v50, 0, v50
	v_max_f32_e32 v51, 0, v51
	v_max_f32_e32 v52, 0, v52
	v_cvt_pk_f16_f32 v51, v51, v52
	v_cvt_pk_f16_f32 v50, v50, v54
	ds_write_b64 v161, v[50:51] offset:96
	s_waitcnt lgkmcnt(4)
	v_lshl_add_u64 v[178:179], v[178:179], 0, v[182:183]
	v_lshl_add_u64 v[180:181], v[180:181], 0, v[182:183]
	s_mov_b64 s[42:43], exec
	s_and_b64 exec, s[42:43], s[38:39]
	global_store_dwordx4 v[178:179], v[170:173], off sc1
	s_and_b64 exec, s[42:43], s[40:41]
	global_store_dwordx4 v[180:181], v[174:177], off sc1
	s_mov_b64 exec, s[42:43]
	ds_read_b128 v[170:173], v164
	ds_read_b128 v[174:177], v164 offset:1152
	ds_bpermute_b32 v178, v165, v66
	ds_bpermute_b32 v179, v165, v67
	ds_bpermute_b32 v180, v166, v66
	ds_bpermute_b32 v181, v166, v67
	v_add_u32_e32 v184, 16, v167
	v_cmp_gt_u32_e64 s[38:39], s2, v184
	v_add_u32_e32 v184, 8, v184
	v_cmp_gt_u32_e64 s[40:41], s2, v184
.LBB2_10:
	s_or_b64 exec, exec, s[0:1]
	v_or_b32_e32 v50, 32, v83
	v_cmp_gt_u32_e32 vcc, s2, v50
	s_mov_b64 s[0:1], exec
	s_cbranch_execz .LBB2_12
	v_add_f32_e32 v47, v15, v47
	v_ashrrev_i32_e32 v85, 31, v84
	v_add_f32_e32 v46, v14, v46
	v_max_f32_e32 v52, 0, v47
	v_add_f32_e32 v47, v16, v48
	v_add_f32_e32 v48, v17, v49
	v_lshlrev_b64 v[50:51], 11, v[84:85]
	v_max_f32_e32 v46, 0, v46
	v_max_f32_e32 v47, 0, v47
	v_max_f32_e32 v48, 0, v48
	v_lshl_add_u64 v[50:51], v[0:1], 0, v[50:51]
	v_cvt_pk_f16_f32 v47, v47, v48
	v_cvt_pk_f16_f32 v46, v46, v52
	v_add_f32_e32 v43, v11, v43
	ds_write_b64 v161, v[46:47]
	v_add_f32_e32 v42, v10, v42
	v_max_f32_e32 v46, 0, v43
	v_add_f32_e32 v43, v12, v44
	v_add_f32_e32 v44, v13, v45
	v_max_f32_e32 v42, 0, v42
	v_max_f32_e32 v43, 0, v43
	v_max_f32_e32 v44, 0, v44
	v_cvt_pk_f16_f32 v43, v43, v44
	v_cvt_pk_f16_f32 v42, v42, v46
	v_add_f32_e32 v39, v7, v39
	ds_write_b64 v161, v[42:43] offset:32
	v_add_f32_e32 v38, v6, v38
	v_max_f32_e32 v42, 0, v39
	v_add_f32_e32 v39, v8, v40
	v_add_f32_e32 v40, v9, v41
	v_max_f32_e32 v38, 0, v38
	v_max_f32_e32 v39, 0, v39
	v_max_f32_e32 v40, 0, v40
	v_cvt_pk_f16_f32 v39, v39, v40
	v_cvt_pk_f16_f32 v38, v38, v42
	v_add_f32_e32 v35, v3, v35
	ds_write_b64 v161, v[38:39] offset:64
	v_add_f32_e32 v34, v2, v34
	v_max_f32_e32 v38, 0, v35
	v_add_f32_e32 v35, v4, v36
	v_add_f32_e32 v36, v5, v37
	v_max_f32_e32 v34, 0, v34
	v_max_f32_e32 v35, 0, v35
	v_max_f32_e32 v36, 0, v36
	v_cvt_pk_f16_f32 v35, v35, v36
	v_cvt_pk_f16_f32 v34, v34, v38
	ds_write_b64 v161, v[34:35] offset:96
	s_waitcnt lgkmcnt(4)
	v_lshl_add_u64 v[178:179], v[178:179], 0, v[182:183]
	v_lshl_add_u64 v[180:181], v[180:181], 0, v[182:183]
	s_mov_b64 s[42:43], exec
	s_and_b64 exec, s[42:43], s[38:39]
	global_store_dwordx4 v[178:179], v[170:173], off sc1
	s_and_b64 exec, s[42:43], s[40:41]
	global_store_dwordx4 v[180:181], v[174:177], off sc1
	s_mov_b64 exec, s[42:43]
	ds_read_b128 v[170:173], v164
	ds_read_b128 v[174:177], v164 offset:1152
	ds_bpermute_b32 v178, v165, v50
	ds_bpermute_b32 v179, v165, v51
	ds_bpermute_b32 v180, v166, v50
	ds_bpermute_b32 v181, v166, v51
	v_add_u32_e32 v184, 32, v167
	v_cmp_gt_u32_e64 s[38:39], s2, v184
	v_add_u32_e32 v184, 8, v184
	v_cmp_gt_u32_e64 s[40:41], s2, v184
.LBB2_12:
	s_or_b64 exec, exec, s[0:1]
	v_or_b32_e32 v34, 48, v83
	v_cmp_gt_u32_e32 vcc, s2, v34
	s_mov_b64 s[0:1], exec
	s_cbranch_execz .LBB2_14
	v_add_f32_e32 v15, v15, v27
	v_ashrrev_i32_e32 v83, 31, v82
	v_add_f32_e32 v14, v14, v26
	v_max_f32_e32 v26, 0, v15
	v_add_f32_e32 v15, v16, v28
	v_add_f32_e32 v16, v17, v29
	v_lshlrev_b64 v[34:35], 11, v[82:83]
	v_max_f32_e32 v14, 0, v14
	v_max_f32_e32 v15, 0, v15
	v_max_f32_e32 v16, 0, v16
	v_lshl_add_u64 v[0:1], v[0:1], 0, v[34:35]
	v_cvt_pk_f16_f32 v15, v15, v16
	v_cvt_pk_f16_f32 v14, v14, v26
	v_add_f32_e32 v11, v11, v23
	ds_write_b64 v161, v[14:15]
	v_add_f32_e32 v10, v10, v22
	v_max_f32_e32 v14, 0, v11
	v_add_f32_e32 v11, v12, v24
	v_add_f32_e32 v12, v13, v25
	v_max_f32_e32 v10, 0, v10
	v_max_f32_e32 v11, 0, v11
	v_max_f32_e32 v12, 0, v12
	v_cvt_pk_f16_f32 v11, v11, v12
	v_cvt_pk_f16_f32 v10, v10, v14
	v_add_f32_e32 v7, v7, v19
	ds_write_b64 v161, v[10:11] offset:32
	v_add_f32_e32 v6, v6, v18
	v_max_f32_e32 v10, 0, v7
	v_add_f32_e32 v7, v8, v20
	v_add_f32_e32 v8, v9, v21
	v_max_f32_e32 v6, 0, v6
	v_max_f32_e32 v7, 0, v7
	v_max_f32_e32 v8, 0, v8
	v_cvt_pk_f16_f32 v7, v7, v8
	v_cvt_pk_f16_f32 v6, v6, v10
	v_add_f32_e32 v3, v3, v31
	ds_write_b64 v161, v[6:7] offset:64
	v_add_f32_e32 v2, v2, v30
	v_max_f32_e32 v6, 0, v3
	v_add_f32_e32 v3, v4, v32
	v_add_f32_e32 v4, v5, v33
	v_max_f32_e32 v2, 0, v2
	v_max_f32_e32 v3, 0, v3
	v_max_f32_e32 v4, 0, v4
	v_cvt_pk_f16_f32 v3, v3, v4
	v_cvt_pk_f16_f32 v2, v2, v6
	ds_write_b64 v161, v[2:3] offset:96
	s_waitcnt lgkmcnt(4)
	v_lshl_add_u64 v[178:179], v[178:179], 0, v[182:183]
	v_lshl_add_u64 v[180:181], v[180:181], 0, v[182:183]
	s_mov_b64 s[42:43], exec
	s_and_b64 exec, s[42:43], s[38:39]
	global_store_dwordx4 v[178:179], v[170:173], off sc1
	s_and_b64 exec, s[42:43], s[40:41]
	global_store_dwordx4 v[180:181], v[174:177], off sc1
	s_mov_b64 exec, s[42:43]
	ds_read_b128 v[170:173], v164
	ds_read_b128 v[174:177], v164 offset:1152
	ds_bpermute_b32 v178, v165, v0
	ds_bpermute_b32 v179, v165, v1
	ds_bpermute_b32 v180, v166, v0
	ds_bpermute_b32 v181, v166, v1
	v_add_u32_e32 v184, 48, v167
	v_cmp_gt_u32_e64 s[38:39], s2, v184
	v_add_u32_e32 v184, 8, v184
	v_cmp_gt_u32_e64 s[40:41], s2, v184
	s_waitcnt lgkmcnt(0)
	v_lshl_add_u64 v[178:179], v[178:179], 0, v[182:183]
	v_lshl_add_u64 v[180:181], v[180:181], 0, v[182:183]
	s_mov_b64 s[42:43], exec
	s_and_b64 exec, s[42:43], s[38:39]
	global_store_dwordx4 v[178:179], v[170:173], off sc1
	s_and_b64 exec, s[42:43], s[40:41]
	global_store_dwordx4 v[180:181], v[174:177], off sc1
	s_mov_b64 exec, s[42:43]

.LBB3_38:
	ds_read_b128 v[6:9], v196 offset:49152
	ds_read_b128 v[18:21], v196 offset:51200
	ds_read_b128 v[34:37], v194
	ds_read_b128 v[150:153], v194 offset:2048
	ds_read_b128 v[154:157], v196 offset:53248
	ds_read_b128 v[158:161], v196 offset:55296
	s_waitcnt vmcnt(6)
	v_pk_add_f16 v2, v30, v2
	s_waitcnt lgkmcnt(3)
	v_mfma_f32_16x16x32_f16 v[106:109], v[6:9], v[34:37], v[106:109]
	v_pk_add_f16 v3, v31, v3
	v_pk_add_f16 v4, v32, v4
	v_pk_add_f16 v5, v33, v5
	v_mfma_f32_16x16x32_f16 v[102:105], v[18:21], v[34:37], v[102:105]
	v_cndmask_b32_e64 v5, v33, v5, s[2:3]
	v_cndmask_b32_e64 v4, v32, v4, s[2:3]
	v_cndmask_b32_e64 v3, v31, v3, s[2:3]
	s_waitcnt lgkmcnt(1)
	v_mfma_f32_16x16x32_f16 v[98:101], v[154:157], v[34:37], v[98:101]
	v_cndmask_b32_e64 v2, v30, v2, s[2:3]
	v_cmp_gt_u32_e32 vcc, s18, v184
	s_waitcnt lgkmcnt(0)
	v_mfma_f32_16x16x32_f16 v[34:37], v[158:161], v[34:37], v[94:97]
	v_mfma_f32_16x16x32_f16 v[90:93], v[6:9], v[150:153], v[90:93]
	v_mfma_f32_16x16x32_f16 v[86:89], v[18:21], v[150:153], v[86:89]
	v_mfma_f32_16x16x32_f16 v[82:85], v[154:157], v[150:153], v[82:85]
	v_mfma_f32_16x16x32_f16 v[78:81], v[158:161], v[150:153], v[78:81]
	ds_read_b128 v[94:97], v194 offset:4096
	ds_read_b128 v[150:153], v194 offset:6144
	s_waitcnt lgkmcnt(1)
	v_mfma_f32_16x16x32_f16 v[62:65], v[6:9], v[94:97], v[62:65]
	v_mfma_f32_16x16x32_f16 v[58:61], v[18:21], v[94:97], v[58:61]
	v_mfma_f32_16x16x32_f16 v[54:57], v[154:157], v[94:97], v[54:57]
	v_mfma_f32_16x16x32_f16 v[74:77], v[158:161], v[94:97], v[74:77]
	s_waitcnt lgkmcnt(0)
	v_mfma_f32_16x16x32_f16 v[66:69], v[6:9], v[150:153], v[66:69]
	v_mfma_f32_16x16x32_f16 v[70:73], v[18:21], v[150:153], v[70:73]
	v_mfma_f32_16x16x32_f16 v[94:97], v[154:157], v[150:153], v[110:113]
	v_mfma_f32_16x16x32_f16 v[110:113], v[158:161], v[150:153], v[114:117]
	s_nop 2
	ds_read_b128 v[114:117], v194 offset:8192
	ds_read_b128 v[150:153], v194 offset:10240
	s_waitcnt lgkmcnt(1)
	v_mfma_f32_16x16x32_f16 v[118:121], v[6:9], v[114:117], v[118:121]
	v_mfma_f32_16x16x32_f16 v[122:125], v[18:21], v[114:117], v[122:125]
	v_mfma_f32_16x16x32_f16 v[126:129], v[154:157], v[114:117], v[126:129]
	v_mfma_f32_16x16x32_f16 v[114:117], v[158:161], v[114:117], v[130:133]
	s_waitcnt lgkmcnt(0)
	v_mfma_f32_16x16x32_f16 v[6:9], v[6:9], v[150:153], v[134:137]
	v_mfma_f32_16x16x32_f16 v[18:21], v[18:21], v[150:153], v[138:141]
	s_nop 1
	ds_read_b128 v[134:137], v197 offset:49152
	v_mfma_f32_16x16x32_f16 v[130:133], v[154:157], v[150:153], v[146:149]
	v_mfma_f32_16x16x32_f16 v[138:141], v[158:161], v[150:153], v[142:145]
	s_nop 2
	ds_read_b128 v[142:145], v197 offset:51200
	ds_read_b128 v[146:149], v195
	ds_read_b128 v[150:153], v195 offset:2048
	ds_read_b128 v[154:157], v197 offset:53248
	ds_read_b128 v[158:161], v197 offset:55296
	s_waitcnt lgkmcnt(3)
	v_mfma_f32_16x16x32_f16 v[106:109], v[134:137], v[146:149], v[106:109]
	v_mfma_f32_16x16x32_f16 v[102:105], v[142:145], v[146:149], v[102:105]
	s_waitcnt lgkmcnt(1)
	v_mfma_f32_16x16x32_f16 v[98:101], v[154:157], v[146:149], v[98:101]
	s_waitcnt lgkmcnt(0)
	v_mfma_f32_16x16x32_f16 v[34:37], v[158:161], v[146:149], v[34:37]
	v_mfma_f32_16x16x32_f16 v[90:93], v[134:137], v[150:153], v[90:93]
	v_mfma_f32_16x16x32_f16 v[86:89], v[142:145], v[150:153], v[86:89]
	v_mfma_f32_16x16x32_f16 v[82:85], v[154:157], v[150:153], v[82:85]
	v_mfma_f32_16x16x32_f16 v[78:81], v[158:161], v[150:153], v[78:81]
	ds_read_b128 v[146:149], v195 offset:4096
	ds_read_b128 v[150:153], v195 offset:6144
	s_waitcnt lgkmcnt(1)
	v_mfma_f32_16x16x32_f16 v[62:65], v[134:137], v[146:149], v[62:65]
	v_mfma_f32_16x16x32_f16 v[58:61], v[142:145], v[146:149], v[58:61]
	v_mfma_f32_16x16x32_f16 v[54:57], v[154:157], v[146:149], v[54:57]
	v_mfma_f32_16x16x32_f16 v[74:77], v[158:161], v[146:149], v[74:77]
	s_waitcnt lgkmcnt(0)
	v_mfma_f32_16x16x32_f16 v[66:69], v[134:137], v[150:153], v[66:69]
	v_mfma_f32_16x16x32_f16 v[70:73], v[142:145], v[150:153], v[70:73]
	v_mfma_f32_16x16x32_f16 v[94:97], v[154:157], v[150:153], v[94:97]
	v_mfma_f32_16x16x32_f16 v[110:113], v[158:161], v[150:153], v[110:113]
	ds_read_b128 v[146:149], v195 offset:8192
	ds_read_b128 v[150:153], v195 offset:10240
	ds_write_b128 v187, v[2:5] offset:24576
	s_waitcnt vmcnt(5)
	v_pk_add_f16 v2, v26, v10
	v_pk_add_f16 v3, v27, v11
	v_pk_add_f16 v4, v28, v12
	v_pk_add_f16 v5, v29, v13
	v_cndmask_b32_e64 v4, v28, v4, s[2:3]
	v_cndmask_b32_e64 v5, v29, v5, s[2:3]
	v_cndmask_b32_e64 v3, v27, v3, s[2:3]
	v_cndmask_b32_e64 v2, v26, v2, s[2:3]
	ds_write_b128 v187, v[2:5] offset:32768
	s_waitcnt vmcnt(4)
	v_pk_add_f16 v2, v22, v14
	v_pk_add_f16 v3, v23, v15
	v_pk_add_f16 v4, v24, v16
	v_pk_add_f16 v5, v25, v17
	v_cndmask_b32_e64 v4, v24, v4, s[2:3]
	v_cndmask_b32_e64 v5, v25, v5, s[2:3]
	v_cndmask_b32_e64 v3, v23, v3, s[2:3]
	v_cndmask_b32_e64 v2, v22, v2, s[2:3]
	s_waitcnt lgkmcnt(3)
	v_mfma_f32_16x16x32_f16 v[118:121], v[134:137], v[146:149], v[118:121]
	s_lshl_b32 s2, s15, 12
	s_add_u32 s4, s12, s2
	s_addc_u32 s5, s13, 0
	s_waitcnt lgkmcnt(2)
	v_mfma_f32_16x16x32_f16 v[6:9], v[134:137], v[150:153], v[6:9]
	v_add_u32_e32 v134, 0x14000, v187
	ds_write_b128 v187, v[2:5] offset:40960
	s_waitcnt vmcnt(3)
	ds_write_b128 v134, v[38:41]
	s_waitcnt vmcnt(2)
	ds_write_b128 v134, v[42:45] offset:8192
	s_waitcnt vmcnt(1)
	ds_write_b128 v134, v[46:49] offset:16384
	s_waitcnt vmcnt(0)
	ds_write_b128 v134, v[50:53] offset:24576
	s_waitcnt lgkmcnt(0)
	s_barrier
	ds_read_b128 v[2:5], v176 offset:32768
	ds_read_b128 v[14:17], v176 offset:34816
	ds_read_b128 v[22:25], v194 offset:24576
	ds_read_b128 v[26:29], v194 offset:26624
	ds_read_b128 v[38:41], v176 offset:36864
	ds_read_b128 v[46:49], v176 offset:38912
	s_waitcnt lgkmcnt(3)
	v_mfma_f32_16x16x32_f16 v[30:33], v[2:5], v[22:25], v[106:109]
	s_ashr_i32 s15, s14, 31
	s_lshl_b64 s[2:3], s[14:15], 2
	s_add_u32 s2, s4, s2
	v_mfma_f32_16x16x32_f16 v[42:45], v[14:17], v[22:25], v[102:105]
	s_addc_u32 s3, s5, s3
	s_waitcnt lgkmcnt(1)
	v_mfma_f32_16x16x32_f16 v[50:53], v[38:41], v[22:25], v[98:101]
	s_waitcnt lgkmcnt(0)
	v_mfma_f32_16x16x32_f16 v[22:25], v[46:49], v[22:25], v[34:37]
	v_mfma_f32_16x16x32_f16 v[34:37], v[2:5], v[26:29], v[90:93]
	v_mfma_f32_16x16x32_f16 v[86:89], v[14:17], v[26:29], v[86:89]
	v_mfma_f32_16x16x32_f16 v[82:85], v[38:41], v[26:29], v[82:85]
	v_mfma_f32_16x16x32_f16 v[26:29], v[46:49], v[26:29], v[78:81]
	s_nop 2
	ds_read_b128 v[78:81], v194 offset:28672
	ds_read_b128 v[90:93], v194 offset:30720
	v_mfma_f32_16x16x32_f16 v[122:125], v[142:145], v[146:149], v[122:125]
	v_mfma_f32_16x16x32_f16 v[18:21], v[142:145], v[150:153], v[18:21]
	v_mfma_f32_16x16x32_f16 v[10:13], v[158:161], v[150:153], v[138:141]
	s_waitcnt lgkmcnt(0)
	v_mfma_f32_16x16x32_f16 v[138:141], v[2:5], v[90:93], v[66:69]
	v_mfma_f32_16x16x32_f16 v[142:145], v[14:17], v[90:93], v[70:73]
	s_nop 1
	ds_read_b128 v[66:69], v194 offset:32768
	ds_read_b128 v[70:73], v194 offset:34816
	v_mfma_f32_16x16x32_f16 v[126:129], v[154:157], v[146:149], v[126:129]
	v_mfma_f32_16x16x32_f16 v[130:133], v[154:157], v[150:153], v[130:133]
	v_mfma_f32_16x16x32_f16 v[114:117], v[158:161], v[146:149], v[114:117]
	v_mfma_f32_16x16x32_f16 v[62:65], v[2:5], v[78:81], v[62:65]
	v_mfma_f32_16x16x32_f16 v[58:61], v[14:17], v[78:81], v[58:61]
	v_mfma_f32_16x16x32_f16 v[54:57], v[38:41], v[78:81], v[54:57]
	v_mfma_f32_16x16x32_f16 v[146:149], v[38:41], v[90:93], v[94:97]
	s_waitcnt lgkmcnt(1)
	v_mfma_f32_16x16x32_f16 v[118:121], v[2:5], v[66:69], v[118:121]
	v_mfma_f32_16x16x32_f16 v[154:157], v[14:17], v[66:69], v[122:125]
	v_mfma_f32_16x16x32_f16 v[158:161], v[38:41], v[66:69], v[126:129]
	s_waitcnt lgkmcnt(0)
	v_mfma_f32_16x16x32_f16 v[2:5], v[2:5], v[70:73], v[6:9]
	s_nop 0
	v_lshlrev_b32_e32 v126, 2, v184
	v_mov_b32_e32 v129, 0
	v_lshlrev_b32_e32 v128, 8, v186
	v_mfma_f32_16x16x32_f16 v[14:17], v[14:17], v[70:73], v[18:21]
	ds_read_b128 v[6:9], v162 offset:32768
	v_mfma_f32_16x16x32_f16 v[130:133], v[38:41], v[70:73], v[130:133]
	ds_read_b128 v[168:171], v162 offset:34816
	ds_read_b128 v[18:21], v195 offset:24576
	ds_read_b128 v[38:41], v195 offset:26624
	ds_read_b128 v[172:175], v162 offset:36864
	ds_read_b128 v[176:179], v162 offset:38912
	v_mfma_f32_16x16x32_f16 v[134:137], v[46:49], v[78:81], v[74:77]
	v_mfma_f32_16x16x32_f16 v[150:153], v[46:49], v[90:93], v[110:113]
	s_waitcnt lgkmcnt(3)
	v_mfma_f32_16x16x32_f16 v[110:113], v[6:9], v[18:21], v[30:33]
	v_mfma_f32_16x16x32_f16 v[106:109], v[168:171], v[18:21], v[42:45]
	s_waitcnt lgkmcnt(1)
	v_mfma_f32_16x16x32_f16 v[102:105], v[172:175], v[18:21], v[50:53]
	s_waitcnt lgkmcnt(0)
	v_mfma_f32_16x16x32_f16 v[98:101], v[176:179], v[18:21], v[22:25]
	ds_read_b128 v[18:21], v195 offset:28672
	s_nop 1
	ds_read_b128 v[22:25], v195 offset:30720
	v_mfma_f32_16x16x32_f16 v[164:167], v[46:49], v[66:69], v[114:117]
	v_mfma_f32_16x16x32_f16 v[10:13], v[46:49], v[70:73], v[10:13]
	s_waitcnt lgkmcnt(1)
	v_mfma_f32_16x16x32_f16 v[78:81], v[6:9], v[18:21], v[62:65]
	v_mfma_f32_16x16x32_f16 v[74:77], v[168:171], v[18:21], v[58:61]
	v_mfma_f32_16x16x32_f16 v[70:73], v[172:175], v[18:21], v[54:57]
	v_mfma_f32_16x16x32_f16 v[66:69], v[176:179], v[18:21], v[134:137]
	ds_read_b128 v[18:21], v195 offset:32768
	s_nop 1
	ds_read_b128 v[134:137], v195 offset:34816
	s_waitcnt lgkmcnt(1)
	v_mfma_f32_16x16x32_f16 v[46:49], v[6:9], v[18:21], v[118:121]
	global_load_dword v124, v126, s[6:7] offset:64
	global_load_dword v122, v126, s[6:7] offset:128
	s_nop 0
	global_load_dword v120, v126, s[6:7] offset:192
	global_load_dword v118, v126, s[6:7] offset:256
	global_load_dword v114, v126, s[6:7] offset:320
	v_mfma_f32_16x16x32_f16 v[62:65], v[6:9], v[22:25], v[138:141]
	v_mfma_f32_16x16x32_f16 v[58:61], v[168:171], v[22:25], v[142:145]
	v_mfma_f32_16x16x32_f16 v[54:57], v[172:175], v[22:25], v[146:149]
	v_mfma_f32_16x16x32_f16 v[50:53], v[176:179], v[22:25], v[150:153]
	v_lshl_add_u64 v[22:23], s[2:3], 0, v[128:129]
	v_lshlrev_b32_e32 v128, 4, v185
	v_lshl_add_u64 v[22:23], v[22:23], 0, v[128:129]
	v_mfma_f32_16x16x32_f16 v[94:97], v[6:9], v[38:41], v[34:37]
	s_lshl_b64 s[2:3], s[14:15], 1
	s_add_u32 s2, s10, s2
	s_addc_u32 s3, s11, s3
	v_mfma_f32_16x16x32_f16 v[90:93], v[168:171], v[38:41], v[86:89]
	v_lshlrev_b32_e32 v128, 7, v186
	v_lshl_add_u64 v[116:117], s[2:3], 0, v[128:129]
	v_lshlrev_b32_e32 v128, 3, v185
	v_mfma_f32_16x16x32_f16 v[86:89], v[172:175], v[38:41], v[82:85]
	v_lshl_add_u64 v[116:117], v[116:117], 0, v[128:129]
	v_mfma_f32_16x16x32_f16 v[82:85], v[176:179], v[38:41], v[26:29]
	v_mfma_f32_16x16x32_f16 v[42:45], v[168:171], v[18:21], v[154:157]
	v_mfma_f32_16x16x32_f16 v[38:41], v[172:175], v[18:21], v[158:161]
	v_mfma_f32_16x16x32_f16 v[34:37], v[176:179], v[18:21], v[164:167]
	global_load_dwordx4 v[26:29], v[22:23], off
	global_load_dwordx4 v[18:21], v[22:23], off offset:64
	s_waitcnt lgkmcnt(0)
	v_mfma_f32_16x16x32_f16 v[30:33], v[6:9], v[134:137], v[2:5]
	global_load_dwordx4 v[6:9], v[22:23], off offset:128
	s_nop 1
	global_load_dwordx4 v[2:5], v[22:23], off offset:192
	v_mfma_f32_16x16x32_f16 v[22:25], v[168:171], v[134:137], v[14:17]
	v_mfma_f32_16x16x32_f16 v[14:17], v[172:175], v[134:137], v[130:133]
	v_mfma_f32_16x16x32_f16 v[10:13], v[176:179], v[134:137], v[10:13]
	v_mbcnt_lo_u32_b32 v196, -1, 0
	v_mbcnt_hi_u32_b32 v196, -1, v196
	v_and_b32_e32 v197, 15, v196
	v_lshrrev_b32_e32 v198, 4, v196
	v_lshrrev_b32_e32 v222, 10, v187
	s_nop 0
	v_readfirstlane_b32 s36, v222
	s_nop 3
	s_and_b32 s36, s36, 7
	s_mulk_i32 s36, 0x900
	v_mul_u32_u24_e32 v199, 0x90, v197
	v_lshl_add_u32 v199, v198, 3, v199
	v_add_u32_e32 v199, s36, v199
	v_lshrrev_b32_e32 v200, 3, v196
	v_and_b32_e32 v201, 7, v196
	v_mul_u32_u24_e32 v202, 0x90, v200
	v_lshl_add_u32 v202, v201, 4, v202
	v_add_u32_e32 v202, s36, v202
	v_lshlrev_b32_e32 v203, 2, v200
	v_add_u32_e32 v204, 32, v203
	v_lshlrev_b32_e32 v220, 4, v201
	v_mov_b32_e32 v221, 0
	v_sub_u32_e32 v205, v184, v197
	v_add_u32_e32 v205, v205, v200
	s_mov_b64 s[2:3], exec
	s_cbranch_execz .LBB3_40
	v_mov_b32_e32 v127, v129
	v_lshl_add_u64 v[126:127], s[6:7], 0, v[126:127]
	global_load_dword v126, v[126:127], off
	s_waitcnt vmcnt(3)
	v_add_f32_e32 v106, v106, v18
	v_add_f32_e32 v107, v107, v19
	v_add_f32_e32 v110, v110, v26
	v_add_f32_e32 v111, v111, v27
	v_add_f32_e32 v112, v112, v28
	v_add_f32_e32 v113, v113, v29
	s_waitcnt vmcnt(2)
	v_add_f32_e32 v103, v103, v7
	v_add_f32_e32 v104, v104, v8
	v_add_f32_e32 v105, v105, v9
	s_waitcnt vmcnt(1)
	v_add_f32_e32 v100, v100, v4
	v_max_f32_e32 v106, 0, v106
	v_max_f32_e32 v107, 0, v107
	v_add_f32_e32 v108, v108, v20
	v_add_f32_e32 v109, v109, v21
	v_add_f32_e32 v102, v102, v6
	v_add_f32_e32 v98, v98, v2
	v_add_f32_e32 v99, v99, v3
	v_add_f32_e32 v101, v101, v5
	v_max_f32_e32 v110, 0, v110
	v_max_f32_e32 v111, 0, v111
	v_max_f32_e32 v112, 0, v112
	v_max_f32_e32 v113, 0, v113
	v_max_f32_e32 v115, 0, v103
	v_max_f32_e32 v103, 0, v104
	v_max_f32_e32 v104, 0, v105
	v_max_f32_e32 v105, 0, v100
	v_cvt_pk_f16_f32 v100, v106, v107
	v_max_f32_e32 v108, 0, v108
	v_max_f32_e32 v109, 0, v109
	v_max_f32_e32 v102, 0, v102
	v_max_f32_e32 v119, 0, v98
	v_max_f32_e32 v121, 0, v99
	v_max_f32_e32 v123, 0, v101
	v_cvt_pk_f16_f32 v99, v112, v113
	v_cvt_pk_f16_f32 v98, v110, v111
	v_cvt_pk_f16_f32 v101, v108, v109
	v_cvt_pk_f16_f32 v103, v103, v104
	v_cvt_pk_f16_f32 v102, v102, v115
	v_cvt_pk_f16_f32 v105, v105, v123
	v_cvt_pk_f16_f32 v104, v119, v121
	s_waitcnt vmcnt(0)
	v_ashrrev_i32_e32 v127, 31, v126
	v_lshlrev_b64 v[106:107], 11, v[126:127]
	v_lshl_add_u64 v[106:107], v[116:117], 0, v[106:107]
	ds_write_b64 v199, v[98:99]
	ds_write_b64 v199, v[100:101] offset:32
	ds_write_b64 v199, v[102:103] offset:64
	ds_write_b64 v199, v[104:105] offset:96
	ds_read_b128 v[208:211], v202
	ds_read_b128 v[212:215], v202 offset:1152
	ds_bpermute_b32 v216, v203, v106
	ds_bpermute_b32 v217, v203, v107
	ds_bpermute_b32 v218, v204, v106
	ds_bpermute_b32 v219, v204, v107
	v_add_u32_e32 v222, 0, v205
	v_cmp_gt_u32_e64 s[38:39], s18, v222
	v_add_u32_e32 v222, 8, v222
	v_cmp_gt_u32_e64 s[40:41], s18, v222
.LBB3_40:
	s_or_b64 exec, exec, s[2:3]
	v_or_b32_e32 v98, 16, v184
	v_cmp_gt_u32_e32 vcc, s18, v98
	s_mov_b64 s[2:3], exec
	s_cbranch_execz .LBB3_42
	v_add_f32_e32 v95, v95, v27
	v_ashrrev_i32_e32 v125, 31, v124
	v_add_f32_e32 v94, v94, v26
	v_max_f32_e32 v100, 0, v95
	v_add_f32_e32 v95, v96, v28
	v_add_f32_e32 v96, v97, v29
	v_lshlrev_b64 v[98:99], 11, v[124:125]
	v_max_f32_e32 v94, 0, v94
	v_max_f32_e32 v95, 0, v95
	v_max_f32_e32 v96, 0, v96
	v_lshl_add_u64 v[98:99], v[116:117], 0, v[98:99]
	v_cvt_pk_f16_f32 v95, v95, v96
	v_cvt_pk_f16_f32 v94, v94, v100
	v_add_f32_e32 v91, v91, v19
	ds_write_b64 v199, v[94:95]
	v_add_f32_e32 v90, v90, v18
	v_max_f32_e32 v94, 0, v91
	v_add_f32_e32 v91, v92, v20
	v_add_f32_e32 v92, v93, v21
	v_max_f32_e32 v90, 0, v90
	v_max_f32_e32 v91, 0, v91
	v_max_f32_e32 v92, 0, v92
	v_cvt_pk_f16_f32 v91, v91, v92
	v_cvt_pk_f16_f32 v90, v90, v94
	v_add_f32_e32 v87, v87, v7
	ds_write_b64 v199, v[90:91] offset:32
	v_add_f32_e32 v86, v86, v6
	v_max_f32_e32 v90, 0, v87
	v_add_f32_e32 v87, v88, v8
	v_add_f32_e32 v88, v89, v9
	v_max_f32_e32 v86, 0, v86
	v_max_f32_e32 v87, 0, v87
	v_max_f32_e32 v88, 0, v88
	v_cvt_pk_f16_f32 v87, v87, v88
	v_cvt_pk_f16_f32 v86, v86, v90
	v_add_f32_e32 v83, v83, v3
	ds_write_b64 v199, v[86:87] offset:64
	v_add_f32_e32 v82, v82, v2
	v_max_f32_e32 v86, 0, v83
	v_add_f32_e32 v83, v84, v4
	v_add_f32_e32 v84, v85, v5
	v_max_f32_e32 v82, 0, v82
	v_max_f32_e32 v83, 0, v83
	v_max_f32_e32 v84, 0, v84
	v_cvt_pk_f16_f32 v83, v83, v84
	v_cvt_pk_f16_f32 v82, v82, v86
	ds_write_b64 v199, v[82:83] offset:96
	s_waitcnt lgkmcnt(4)
	v_lshl_add_u64 v[216:217], v[216:217], 0, v[220:221]
	v_lshl_add_u64 v[218:219], v[218:219], 0, v[220:221]
	s_mov_b64 s[42:43], exec
	s_and_b64 exec, s[42:43], s[38:39]
	global_store_dwordx4 v[216:217], v[208:211], off sc1
	s_and_b64 exec, s[42:43], s[40:41]
	global_store_dwordx4 v[218:219], v[212:215], off sc1
	s_mov_b64 exec, s[42:43]
	ds_read_b128 v[208:211], v202
	ds_read_b128 v[212:215], v202 offset:1152
	ds_bpermute_b32 v216, v203, v98
	ds_bpermute_b32 v217, v203, v99
	ds_bpermute_b32 v218, v204, v98
	ds_bpermute_b32 v219, v204, v99
	v_add_u32_e32 v222, 16, v205
	v_cmp_gt_u32_e64 s[38:39], s18, v222
	v_add_u32_e32 v222, 8, v222
	v_cmp_gt_u32_e64 s[40:41], s18, v222
.LBB3_42:
	s_or_b64 exec, exec, s[2:3]
	v_add_u32_e32 v82, 32, v184
	v_cmp_gt_u32_e32 vcc, s18, v82
	s_mov_b64 s[2:3], exec
	s_cbranch_execz .LBB3_44
	v_add_f32_e32 v79, v79, v27
	v_ashrrev_i32_e32 v123, 31, v122
	v_add_f32_e32 v78, v78, v26
	v_max_f32_e32 v84, 0, v79
	v_add_f32_e32 v79, v80, v28
	v_add_f32_e32 v80, v81, v29
	v_lshlrev_b64 v[82:83], 11, v[122:123]
	v_max_f32_e32 v78, 0, v78
	v_max_f32_e32 v79, 0, v79
	v_max_f32_e32 v80, 0, v80
	v_lshl_add_u64 v[82:83], v[116:117], 0, v[82:83]
	v_cvt_pk_f16_f32 v79, v79, v80
	v_cvt_pk_f16_f32 v78, v78, v84
	v_add_f32_e32 v75, v75, v19
	ds_write_b64 v199, v[78:79]
	v_add_f32_e32 v74, v74, v18
	v_max_f32_e32 v78, 0, v75
	v_add_f32_e32 v75, v76, v20
	v_add_f32_e32 v76, v77, v21
	v_max_f32_e32 v74, 0, v74
	v_max_f32_e32 v75, 0, v75
	v_max_f32_e32 v76, 0, v76
	v_cvt_pk_f16_f32 v75, v75, v76
	v_cvt_pk_f16_f32 v74, v74, v78
	v_add_f32_e32 v71, v71, v7
	ds_write_b64 v199, v[74:75] offset:32
	v_add_f32_e32 v70, v70, v6
	v_max_f32_e32 v74, 0, v71
	v_add_f32_e32 v71, v72, v8
	v_add_f32_e32 v72, v73, v9
	v_max_f32_e32 v70, 0, v70
	v_max_f32_e32 v71, 0, v71
	v_max_f32_e32 v72, 0, v72
	v_cvt_pk_f16_f32 v71, v71, v72
	v_cvt_pk_f16_f32 v70, v70, v74
	v_add_f32_e32 v67, v67, v3
	ds_write_b64 v199, v[70:71] offset:64
	v_add_f32_e32 v66, v66, v2
	v_max_f32_e32 v70, 0, v67
	v_add_f32_e32 v67, v68, v4
	v_add_f32_e32 v68, v69, v5
	v_max_f32_e32 v66, 0, v66
	v_max_f32_e32 v67, 0, v67
	v_max_f32_e32 v68, 0, v68
	v_cvt_pk_f16_f32 v67, v67, v68
	v_cvt_pk_f16_f32 v66, v66, v70
	ds_write_b64 v199, v[66:67] offset:96
	s_waitcnt lgkmcnt(4)
	v_lshl_add_u64 v[216:217], v[216:217], 0, v[220:221]
	v_lshl_add_u64 v[218:219], v[218:219], 0, v[220:221]
	s_mov_b64 s[42:43], exec
	s_and_b64 exec, s[42:43], s[38:39]
	global_store_dwordx4 v[216:217], v[208:211], off sc1
	s_and_b64 exec, s[42:43], s[40:41]
	global_store_dwordx4 v[218:219], v[212:215], off sc1
	s_mov_b64 exec, s[42:43]
	ds_read_b128 v[208:211], v202
	ds_read_b128 v[212:215], v202 offset:1152
	ds_bpermute_b32 v216, v203, v82
	ds_bpermute_b32 v217, v203, v83
	ds_bpermute_b32 v218, v204, v82
	ds_bpermute_b32 v219, v204, v83
	v_add_u32_e32 v222, 32, v205
	v_cmp_gt_u32_e64 s[38:39], s18, v222
	v_add_u32_e32 v222, 8, v222
	v_cmp_gt_u32_e64 s[40:41], s18, v222
.LBB3_44:
	s_or_b64 exec, exec, s[2:3]
	v_add_u32_e32 v66, 48, v184
	v_cmp_gt_u32_e32 vcc, s18, v66
	s_mov_b64 s[2:3], exec
	s_cbranch_execz .LBB3_46
	v_add_f32_e32 v63, v63, v27
	v_ashrrev_i32_e32 v121, 31, v120
	v_add_f32_e32 v62, v62, v26
	v_max_f32_e32 v68, 0, v63
	v_add_f32_e32 v63, v64, v28
	v_add_f32_e32 v64, v65, v29
	v_lshlrev_b64 v[66:67], 11, v[120:121]
	v_max_f32_e32 v62, 0, v62
	v_max_f32_e32 v63, 0, v63
	v_max_f32_e32 v64, 0, v64
	v_lshl_add_u64 v[66:67], v[116:117], 0, v[66:67]
	v_cvt_pk_f16_f32 v63, v63, v64
	v_cvt_pk_f16_f32 v62, v62, v68
	v_add_f32_e32 v59, v59, v19
	ds_write_b64 v199, v[62:63]
	v_add_f32_e32 v58, v58, v18
	v_max_f32_e32 v62, 0, v59
	v_add_f32_e32 v59, v60, v20
	v_add_f32_e32 v60, v61, v21
	v_max_f32_e32 v58, 0, v58
	v_max_f32_e32 v59, 0, v59
	v_max_f32_e32 v60, 0, v60
	v_cvt_pk_f16_f32 v59, v59, v60
	v_cvt_pk_f16_f32 v58, v58, v62
	v_add_f32_e32 v55, v55, v7
	ds_write_b64 v199, v[58:59] offset:32
	v_add_f32_e32 v54, v54, v6
	v_max_f32_e32 v58, 0, v55
	v_add_f32_e32 v55, v56, v8
	v_add_f32_e32 v56, v57, v9
	v_max_f32_e32 v54, 0, v54
	v_max_f32_e32 v55, 0, v55
	v_max_f32_e32 v56, 0, v56
	v_cvt_pk_f16_f32 v55, v55, v56
	v_cvt_pk_f16_f32 v54, v54, v58
	v_add_f32_e32 v51, v51, v3
	ds_write_b64 v199, v[54:55] offset:64
	v_add_f32_e32 v50, v50, v2
	v_max_f32_e32 v54, 0, v51
	v_add_f32_e32 v51, v52, v4
	v_add_f32_e32 v52, v53, v5
	v_max_f32_e32 v50, 0, v50
	v_max_f32_e32 v51, 0, v51
	v_max_f32_e32 v52, 0, v52
	v_cvt_pk_f16_f32 v51, v51, v52
	v_cvt_pk_f16_f32 v50, v50, v54
	ds_write_b64 v199, v[50:51] offset:96
	s_waitcnt lgkmcnt(4)
	v_lshl_add_u64 v[216:217], v[216:217], 0, v[220:221]
	v_lshl_add_u64 v[218:219], v[218:219], 0, v[220:221]
	s_mov_b64 s[42:43], exec
	s_and_b64 exec, s[42:43], s[38:39]
	global_store_dwordx4 v[216:217], v[208:211], off sc1
	s_and_b64 exec, s[42:43], s[40:41]
	global_store_dwordx4 v[218:219], v[212:215], off sc1
	s_mov_b64 exec, s[42:43]
	ds_read_b128 v[208:211], v202
	ds_read_b128 v[212:215], v202 offset:1152
	ds_bpermute_b32 v216, v203, v66
	ds_bpermute_b32 v217, v203, v67
	ds_bpermute_b32 v218, v204, v66
	ds_bpermute_b32 v219, v204, v67
	v_add_u32_e32 v222, 48, v205
	v_cmp_gt_u32_e64 s[38:39], s18, v222
	v_add_u32_e32 v222, 8, v222
	v_cmp_gt_u32_e64 s[40:41], s18, v222
.LBB3_46:
	s_or_b64 exec, exec, s[2:3]
	v_add_u32_e32 v50, 64, v184
	v_cmp_gt_u32_e32 vcc, s18, v50
	s_mov_b64 s[2:3], exec
	s_cbranch_execz .LBB3_48
	v_add_f32_e32 v47, v47, v27
	v_ashrrev_i32_e32 v119, 31, v118
	v_add_f32_e32 v46, v46, v26
	v_max_f32_e32 v52, 0, v47
	v_add_f32_e32 v47, v48, v28
	v_add_f32_e32 v48, v49, v29
	v_lshlrev_b64 v[50:51], 11, v[118:119]
	v_max_f32_e32 v46, 0, v46
	v_max_f32_e32 v47, 0, v47
	v_max_f32_e32 v48, 0, v48
	v_lshl_add_u64 v[50:51], v[116:117], 0, v[50:51]
	v_cvt_pk_f16_f32 v47, v47, v48
	v_cvt_pk_f16_f32 v46, v46, v52
	v_add_f32_e32 v43, v43, v19
	ds_write_b64 v199, v[46:47]
	v_add_f32_e32 v42, v42, v18
	v_max_f32_e32 v46, 0, v43
	v_add_f32_e32 v43, v44, v20
	v_add_f32_e32 v44, v45, v21
	v_max_f32_e32 v42, 0, v42
	v_max_f32_e32 v43, 0, v43
	v_max_f32_e32 v44, 0, v44
	v_cvt_pk_f16_f32 v43, v43, v44
	v_cvt_pk_f16_f32 v42, v42, v46
	v_add_f32_e32 v39, v39, v7
	ds_write_b64 v199, v[42:43] offset:32
	v_add_f32_e32 v38, v38, v6
	v_max_f32_e32 v42, 0, v39
	v_add_f32_e32 v39, v40, v8
	v_add_f32_e32 v40, v41, v9
	v_max_f32_e32 v38, 0, v38
	v_max_f32_e32 v39, 0, v39
	v_max_f32_e32 v40, 0, v40
	v_cvt_pk_f16_f32 v39, v39, v40
	v_cvt_pk_f16_f32 v38, v38, v42
	v_add_f32_e32 v35, v35, v3
	ds_write_b64 v199, v[38:39] offset:64
	v_add_f32_e32 v34, v34, v2
	v_max_f32_e32 v38, 0, v35
	v_add_f32_e32 v35, v36, v4
	v_add_f32_e32 v36, v37, v5
	v_max_f32_e32 v34, 0, v34
	v_max_f32_e32 v35, 0, v35
	v_max_f32_e32 v36, 0, v36
	v_cvt_pk_f16_f32 v35, v35, v36
	v_cvt_pk_f16_f32 v34, v34, v38
	ds_write_b64 v199, v[34:35] offset:96
	s_waitcnt lgkmcnt(4)
	v_lshl_add_u64 v[216:217], v[216:217], 0, v[220:221]
	v_lshl_add_u64 v[218:219], v[218:219], 0, v[220:221]
	s_mov_b64 s[42:43], exec
	s_and_b64 exec, s[42:43], s[38:39]
	global_store_dwordx4 v[216:217], v[208:211], off sc1
	s_and_b64 exec, s[42:43], s[40:41]
	global_store_dwordx4 v[218:219], v[212:215], off sc1
	s_mov_b64 exec, s[42:43]
	ds_read_b128 v[208:211], v202
	ds_read_b128 v[212:215], v202 offset:1152
	ds_bpermute_b32 v216, v203, v50
	ds_bpermute_b32 v217, v203, v51
	ds_bpermute_b32 v218, v204, v50
	ds_bpermute_b32 v219, v204, v51
	v_add_u32_e32 v222, 64, v205
	v_cmp_gt_u32_e64 s[38:39], s18, v222
	v_add_u32_e32 v222, 8, v222
	v_cmp_gt_u32_e64 s[40:41], s18, v222
.LBB3_48:
	s_or_b64 exec, exec, s[2:3]
	v_add_u32_e32 v34, 0x50, v184
	v_cmp_gt_u32_e32 vcc, s18, v34
	s_mov_b64 s[2:3], exec
	s_cbranch_execz .LBB3_50
	v_add_f32_e32 v7, v15, v7
	v_ashrrev_i32_e32 v115, 31, v114
	v_add_f32_e32 v6, v14, v6
	v_max_f32_e32 v14, 0, v7
	v_add_f32_e32 v7, v16, v8
	v_add_f32_e32 v8, v17, v9
	v_lshlrev_b64 v[34:35], 11, v[114:115]
	v_max_f32_e32 v6, 0, v6
	v_max_f32_e32 v7, 0, v7
	v_max_f32_e32 v8, 0, v8
	v_lshl_add_u64 v[34:35], v[116:117], 0, v[34:35]
	v_add_f32_e32 v27, v31, v27
	v_add_f32_e32 v19, v23, v19
	v_cvt_pk_f16_f32 v7, v7, v8
	v_cvt_pk_f16_f32 v6, v6, v14
	v_add_f32_e32 v3, v11, v3
	v_add_f32_e32 v26, v30, v26
	v_max_f32_e32 v30, 0, v27
	v_add_f32_e32 v27, v32, v28
	v_add_f32_e32 v28, v33, v29
	v_add_f32_e32 v18, v22, v18
	v_max_f32_e32 v22, 0, v19
	v_add_f32_e32 v19, v24, v20
	v_add_f32_e32 v20, v25, v21
	ds_write_b64 v199, v[6:7] offset:64
	v_add_f32_e32 v2, v10, v2
	v_max_f32_e32 v6, 0, v3
	v_add_f32_e32 v3, v12, v4
	v_add_f32_e32 v4, v13, v5
	v_max_f32_e32 v26, 0, v26
	v_max_f32_e32 v27, 0, v27
	v_max_f32_e32 v28, 0, v28
	v_max_f32_e32 v18, 0, v18
	v_max_f32_e32 v19, 0, v19
	v_max_f32_e32 v20, 0, v20
	v_max_f32_e32 v2, 0, v2
	v_max_f32_e32 v3, 0, v3
	v_max_f32_e32 v4, 0, v4
	v_cvt_pk_f16_f32 v27, v27, v28
	v_cvt_pk_f16_f32 v26, v26, v30
	v_cvt_pk_f16_f32 v19, v19, v20
	v_cvt_pk_f16_f32 v18, v18, v22
	v_cvt_pk_f16_f32 v3, v3, v4
	v_cvt_pk_f16_f32 v2, v2, v6
	ds_write_b64 v199, v[26:27]
	ds_write_b64 v199, v[18:19] offset:32
	ds_write_b64 v199, v[2:3] offset:96
	s_waitcnt lgkmcnt(4)
	v_lshl_add_u64 v[216:217], v[216:217], 0, v[220:221]
	v_lshl_add_u64 v[218:219], v[218:219], 0, v[220:221]
	s_mov_b64 s[42:43], exec
	s_and_b64 exec, s[42:43], s[38:39]
	global_store_dwordx4 v[216:217], v[208:211], off sc1
	s_and_b64 exec, s[42:43], s[40:41]
	global_store_dwordx4 v[218:219], v[212:215], off sc1
	s_mov_b64 exec, s[42:43]
	ds_read_b128 v[208:211], v202
	ds_read_b128 v[212:215], v202 offset:1152
	ds_bpermute_b32 v216, v203, v34
	ds_bpermute_b32 v217, v203, v35
	ds_bpermute_b32 v218, v204, v34
	ds_bpermute_b32 v219, v204, v35
	v_add_u32_e32 v222, 80, v205
	v_cmp_gt_u32_e64 s[38:39], s18, v222
	v_add_u32_e32 v222, 8, v222
	v_cmp_gt_u32_e64 s[40:41], s18, v222
	s_waitcnt lgkmcnt(0)
	v_lshl_add_u64 v[216:217], v[216:217], 0, v[220:221]
	v_lshl_add_u64 v[218:219], v[218:219], 0, v[220:221]
	s_mov_b64 s[42:43], exec
	s_and_b64 exec, s[42:43], s[38:39]
	global_store_dwordx4 v[216:217], v[208:211], off sc1
	s_and_b64 exec, s[42:43], s[40:41]
	global_store_dwordx4 v[218:219], v[212:215], off sc1
	s_mov_b64 exec, s[42:43]

.LBB3_53:
	v_add_u32_e32 v104, v81, v83
	v_add_u32_e32 v102, v89, v83
	ds_read_b128 v[106:109], v104 offset:49152
	ds_read_b128 v[110:113], v104 offset:51200
	ds_read_b128 v[114:117], v102
	ds_read_b128 v[118:121], v102 offset:2048
	v_add_u32_e32 v103, v89, v87
	v_add_u32_e32 v105, v81, v87
	s_waitcnt lgkmcnt(1)
	v_mfma_f32_16x16x32_f16 v[46:49], v[106:109], v[114:117], v[46:49]
	v_lshl_add_u64 v[154:155], v[96:97], 0, v[84:85]
	v_lshl_add_u64 v[156:157], v[98:99], 0, v[84:85]
	v_lshl_add_u64 v[160:161], v[94:95], 0, v[84:85]
	v_mfma_f32_16x16x32_f16 v[38:41], v[110:113], v[114:117], v[38:41]
	v_lshl_add_u64 v[158:159], v[100:101], 0, v[84:85]
	v_add_co_u32_e32 v162, vcc, s14, v160
	s_waitcnt lgkmcnt(0)
	v_mfma_f32_16x16x32_f16 v[34:37], v[106:109], v[118:121], v[34:37]
	v_addc_co_u32_e32 v163, vcc, 0, v161, vcc
	s_add_i32 s4, s4, 2
	v_mfma_f32_16x16x32_f16 v[30:33], v[110:113], v[118:121], v[30:33]
	ds_read_b128 v[114:117], v102 offset:4096
	ds_read_b128 v[118:121], v102 offset:6144
	v_lshl_add_u64 v[96:97], v[96:97], 0, s[2:3]
	v_lshl_add_u64 v[98:99], v[98:99], 0, s[2:3]
	s_waitcnt lgkmcnt(1)
	v_mfma_f32_16x16x32_f16 v[42:45], v[106:109], v[114:117], v[42:45]
	v_lshl_add_u64 v[100:101], v[100:101], 0, s[2:3]
	v_lshl_add_u64 v[94:95], v[94:95], 0, s[2:3]
	s_cmp_lt_u32 s4, 27
	v_mfma_f32_16x16x32_f16 v[50:53], v[110:113], v[114:117], v[50:53]
	s_waitcnt lgkmcnt(0)
	v_mfma_f32_16x16x32_f16 v[54:57], v[106:109], v[118:121], v[54:57]
	v_mfma_f32_16x16x32_f16 v[58:61], v[110:113], v[118:121], v[58:61]
	ds_read_b128 v[114:117], v102 offset:8192
	ds_read_b128 v[118:121], v102 offset:10240
	s_waitcnt lgkmcnt(1)
	v_mfma_f32_16x16x32_f16 v[62:65], v[106:109], v[114:117], v[62:65]
	v_mfma_f32_16x16x32_f16 v[66:69], v[110:113], v[114:117], v[66:69]
	ds_read_b128 v[114:117], v105 offset:49152
	ds_read_b128 v[122:125], v105 offset:51200
	s_waitcnt lgkmcnt(2)
	v_mfma_f32_16x16x32_f16 v[74:77], v[106:109], v[118:121], v[74:77]
	v_mfma_f32_16x16x32_f16 v[70:73], v[110:113], v[118:121], v[70:73]
	ds_read_b128 v[106:109], v103
	ds_read_b128 v[110:113], v103 offset:2048
	s_waitcnt lgkmcnt(1)
	v_mfma_f32_16x16x32_f16 v[46:49], v[114:117], v[106:109], v[46:49]
	v_mfma_f32_16x16x32_f16 v[38:41], v[122:125], v[106:109], v[38:41]
	v_add_u32_e32 v106, v93, v83
	v_add_u32_e32 v107, v93, v87
	s_waitcnt lgkmcnt(0)
	v_mfma_f32_16x16x32_f16 v[34:37], v[114:117], v[110:113], v[34:37]
	v_mfma_f32_16x16x32_f16 v[30:33], v[122:125], v[110:113], v[30:33]
	ds_read_b128 v[108:111], v103 offset:4096
	ds_read_b128 v[118:121], v103 offset:6144
	global_load_dwordx4 v[126:129], v[154:155], off offset:256
	ds_read_b128 v[130:133], v103 offset:8192
	ds_read_b128 v[134:137], v103 offset:10240
	s_waitcnt vmcnt(3)
	ds_write_b128 v1, v[26:29] offset:24576
	s_waitcnt lgkmcnt(4)
	v_mfma_f32_16x16x32_f16 v[42:45], v[114:117], v[108:111], v[42:45]
	v_mfma_f32_16x16x32_f16 v[50:53], v[122:125], v[108:111], v[50:53]
	global_load_dwordx4 v[108:111], v[156:157], off offset:256
	global_load_dwordx4 v[138:141], v[158:159], off offset:256
	s_waitcnt vmcnt(4)
	ds_write_b128 v1, v[22:25] offset:32768
	s_waitcnt vmcnt(3)
	ds_write_b128 v1, v[18:21] offset:40960
	ds_write_b128 v91, v[10:13] offset:16384
	ds_write_b128 v91, v[14:17] offset:24576
	s_waitcnt lgkmcnt(7)
	v_mfma_f32_16x16x32_f16 v[26:29], v[114:117], v[118:121], v[54:57]
	v_mfma_f32_16x16x32_f16 v[54:57], v[122:125], v[118:121], v[58:61]
	global_load_dwordx4 v[118:121], v[160:161], off offset:256
	global_load_dwordx4 v[142:145], v[162:163], off offset:256
	s_waitcnt lgkmcnt(0)
	s_barrier
	v_mfma_f32_16x16x32_f16 v[10:13], v[114:117], v[130:133], v[62:65]
	ds_read_b128 v[22:25], v106 offset:16384
	ds_read_b128 v[58:61], v106 offset:18432
	v_mfma_f32_16x16x32_f16 v[14:17], v[122:125], v[130:133], v[66:69]
	v_mfma_f32_16x16x32_f16 v[62:65], v[122:125], v[134:137], v[70:73]
	s_nop 1
	ds_read_b128 v[66:69], v102 offset:24576
	ds_read_b128 v[70:73], v102 offset:26624
	s_waitcnt lgkmcnt(1)
	v_mfma_f32_16x16x32_f16 v[46:49], v[22:25], v[66:69], v[46:49]
	v_mfma_f32_16x16x32_f16 v[38:41], v[58:61], v[66:69], v[38:41]
	s_waitcnt lgkmcnt(0)
	v_mfma_f32_16x16x32_f16 v[34:37], v[22:25], v[70:73], v[34:37]
	v_mfma_f32_16x16x32_f16 v[30:33], v[58:61], v[70:73], v[30:33]
	ds_read_b128 v[66:69], v102 offset:28672
	ds_read_b128 v[70:73], v102 offset:30720
	s_waitcnt lgkmcnt(1)
	v_mfma_f32_16x16x32_f16 v[42:45], v[22:25], v[66:69], v[42:45]
	v_mfma_f32_16x16x32_f16 v[50:53], v[58:61], v[66:69], v[50:53]
	s_waitcnt lgkmcnt(0)
	v_mfma_f32_16x16x32_f16 v[26:29], v[22:25], v[70:73], v[26:29]
	v_mfma_f32_16x16x32_f16 v[66:69], v[58:61], v[70:73], v[54:57]
	s_nop 2
	ds_read_b128 v[54:57], v102 offset:32768
	ds_read_b128 v[70:73], v102 offset:34816
	v_mfma_f32_16x16x32_f16 v[18:21], v[114:117], v[134:137], v[74:77]
	ds_read_b128 v[130:133], v107 offset:16384
	ds_read_b128 v[134:137], v107 offset:18432
	s_waitcnt lgkmcnt(3)
	v_mfma_f32_16x16x32_f16 v[74:77], v[22:25], v[54:57], v[10:13]
	v_mfma_f32_16x16x32_f16 v[112:115], v[58:61], v[54:57], v[14:17]
	s_nop 1
	ds_read_b128 v[10:13], v103 offset:24576
	ds_read_b128 v[14:17], v103 offset:26624
	s_waitcnt lgkmcnt(1)
	v_mfma_f32_16x16x32_f16 v[46:49], v[130:133], v[10:13], v[46:49]
	v_mfma_f32_16x16x32_f16 v[38:41], v[134:137], v[10:13], v[38:41]
	s_waitcnt lgkmcnt(0)
	v_mfma_f32_16x16x32_f16 v[34:37], v[130:133], v[14:17], v[34:37]
	v_mfma_f32_16x16x32_f16 v[30:33], v[134:137], v[14:17], v[30:33]
	ds_read_b128 v[10:13], v103 offset:28672
	ds_read_b128 v[14:17], v103 offset:30720
	ds_read_b128 v[146:149], v103 offset:32768
	ds_read_b128 v[150:153], v103 offset:34816
	v_mfma_f32_16x16x32_f16 v[122:125], v[22:25], v[70:73], v[18:21]
	s_waitcnt lgkmcnt(3)
	v_mfma_f32_16x16x32_f16 v[42:45], v[130:133], v[10:13], v[42:45]
	v_mfma_f32_16x16x32_f16 v[50:53], v[134:137], v[10:13], v[50:53]
	s_waitcnt lgkmcnt(2)
	v_mfma_f32_16x16x32_f16 v[54:57], v[130:133], v[14:17], v[26:29]
	s_nop 2
	global_load_dwordx4 v[26:29], v[154:155], off offset:384
	global_load_dwordx4 v[22:25], v[156:157], off offset:384
	global_load_dwordx4 v[18:21], v[158:159], off offset:384
	global_load_dwordx4 v[10:13], v[160:161], off offset:384
	v_mfma_f32_16x16x32_f16 v[70:73], v[58:61], v[70:73], v[62:65]
	v_mfma_f32_16x16x32_f16 v[58:61], v[134:137], v[14:17], v[66:69]
	global_load_dwordx4 v[14:17], v[162:163], off offset:384
	s_waitcnt vmcnt(9)
	ds_write_b128 v1, v[126:129]
	s_waitcnt vmcnt(8)
	ds_write_b128 v1, v[108:111] offset:8192
	s_waitcnt vmcnt(7)
	ds_write_b128 v1, v[138:141] offset:16384
	s_waitcnt vmcnt(6)
	ds_write_b128 v1, v[118:121] offset:49152
	s_waitcnt vmcnt(5)
	ds_write_b128 v1, v[142:145] offset:57344
	s_waitcnt lgkmcnt(0)
	v_mfma_f32_16x16x32_f16 v[62:65], v[130:133], v[146:149], v[74:77]
	s_barrier
	v_mfma_f32_16x16x32_f16 v[66:69], v[134:137], v[146:149], v[112:115]
	v_mfma_f32_16x16x32_f16 v[74:77], v[130:133], v[150:153], v[122:125]
	v_mfma_f32_16x16x32_f16 v[70:73], v[134:137], v[150:153], v[70:73]
	s_cbranch_scc1 .LBB3_53
	ds_read_b128 v[94:97], v104 offset:49152
	ds_read_b128 v[98:101], v104 offset:51200
	ds_read_b128 v[108:111], v102
	ds_read_b128 v[112:115], v102 offset:2048
	v_add_u32_e32 v81, 0x10000, v1
	s_lshl_b64 s[0:1], s[0:1], 1
	s_add_u32 s0, s10, s0
	s_waitcnt lgkmcnt(1)
	v_mfma_f32_16x16x32_f16 v[46:49], v[94:97], v[108:111], v[46:49]
	s_addc_u32 s1, s11, s1
	v_cmp_gt_u32_e32 vcc, s18, v79
	v_mfma_f32_16x16x32_f16 v[38:41], v[98:101], v[108:111], v[38:41]
	s_waitcnt lgkmcnt(0)
	v_mfma_f32_16x16x32_f16 v[34:37], v[94:97], v[112:115], v[34:37]
	v_mfma_f32_16x16x32_f16 v[30:33], v[98:101], v[112:115], v[30:33]
	ds_read_b128 v[108:111], v102 offset:4096
	ds_read_b128 v[112:115], v102 offset:6144
	s_waitcnt lgkmcnt(1)
	v_mfma_f32_16x16x32_f16 v[42:45], v[94:97], v[108:111], v[42:45]
	v_mfma_f32_16x16x32_f16 v[50:53], v[98:101], v[108:111], v[50:53]
	s_waitcnt lgkmcnt(0)
	v_mfma_f32_16x16x32_f16 v[54:57], v[94:97], v[112:115], v[54:57]
	v_mfma_f32_16x16x32_f16 v[58:61], v[98:101], v[112:115], v[58:61]
	ds_read_b128 v[108:111], v102 offset:8192
	ds_read_b128 v[112:115], v102 offset:10240
	s_waitcnt lgkmcnt(1)
	v_mfma_f32_16x16x32_f16 v[62:65], v[94:97], v[108:111], v[62:65]
	s_waitcnt lgkmcnt(0)
	v_mfma_f32_16x16x32_f16 v[74:77], v[94:97], v[112:115], v[74:77]
	ds_read_b128 v[94:97], v105 offset:49152
	v_mfma_f32_16x16x32_f16 v[66:69], v[98:101], v[108:111], v[66:69]
	v_mfma_f32_16x16x32_f16 v[70:73], v[98:101], v[112:115], v[70:73]
	ds_read_b128 v[98:101], v105 offset:51200
	ds_read_b128 v[108:111], v103
	ds_read_b128 v[112:115], v103 offset:2048
	s_waitcnt lgkmcnt(1)
	v_mfma_f32_16x16x32_f16 v[46:49], v[94:97], v[108:111], v[46:49]
	v_mfma_f32_16x16x32_f16 v[38:41], v[98:101], v[108:111], v[38:41]
	s_waitcnt lgkmcnt(0)
	v_mfma_f32_16x16x32_f16 v[34:37], v[94:97], v[112:115], v[34:37]
	v_mfma_f32_16x16x32_f16 v[30:33], v[98:101], v[112:115], v[30:33]
	ds_read_b128 v[108:111], v103 offset:4096
	ds_read_b128 v[112:115], v103 offset:6144
	s_waitcnt lgkmcnt(1)
	v_mfma_f32_16x16x32_f16 v[42:45], v[94:97], v[108:111], v[42:45]
	v_mfma_f32_16x16x32_f16 v[50:53], v[98:101], v[108:111], v[50:53]
	s_waitcnt lgkmcnt(0)
	v_mfma_f32_16x16x32_f16 v[54:57], v[94:97], v[112:115], v[54:57]
	v_mfma_f32_16x16x32_f16 v[58:61], v[98:101], v[112:115], v[58:61]
	ds_read_b128 v[108:111], v103 offset:8192
	ds_read_b128 v[112:115], v103 offset:10240
	s_waitcnt vmcnt(4)
	ds_write_b128 v1, v[26:29] offset:24576
	s_waitcnt vmcnt(3)
	ds_write_b128 v1, v[22:25] offset:32768
	s_waitcnt vmcnt(2)
	ds_write_b128 v1, v[18:21] offset:40960
	s_waitcnt vmcnt(1)
	ds_write_b128 v81, v[10:13]
	s_waitcnt vmcnt(0)
	ds_write_b128 v81, v[14:17] offset:8192
	s_waitcnt lgkmcnt(0)
	s_barrier
	ds_read_b128 v[10:13], v106 offset:16384
	ds_read_b128 v[18:21], v106 offset:18432
	ds_read_b128 v[22:25], v102 offset:24576
	ds_read_b128 v[26:29], v102 offset:26624
	s_waitcnt lgkmcnt(1)
	v_mfma_f32_16x16x32_f16 v[46:49], v[10:13], v[22:25], v[46:49]
	v_mfma_f32_16x16x32_f16 v[22:25], v[18:21], v[22:25], v[38:41]
	s_waitcnt lgkmcnt(0)
	v_mfma_f32_16x16x32_f16 v[34:37], v[10:13], v[26:29], v[34:37]
	v_mfma_f32_16x16x32_f16 v[26:29], v[18:21], v[26:29], v[30:33]
	s_nop 2
	ds_read_b128 v[30:33], v102 offset:28672
	ds_read_b128 v[38:41], v102 offset:30720
	v_mfma_f32_16x16x32_f16 v[62:65], v[94:97], v[108:111], v[62:65]
	v_mfma_f32_16x16x32_f16 v[74:77], v[94:97], v[112:115], v[74:77]
	v_mfma_f32_16x16x32_f16 v[14:17], v[98:101], v[112:115], v[70:73]
	s_waitcnt lgkmcnt(1)
	v_mfma_f32_16x16x32_f16 v[70:73], v[10:13], v[30:33], v[42:45]
	s_waitcnt lgkmcnt(0)
	v_mfma_f32_16x16x32_f16 v[94:97], v[10:13], v[38:41], v[54:57]
	v_mfma_f32_16x16x32_f16 v[58:61], v[18:21], v[38:41], v[58:61]
	ds_read_b128 v[38:41], v102 offset:32768
	ds_read_b128 v[42:45], v102 offset:34816
	v_mfma_f32_16x16x32_f16 v[66:69], v[98:101], v[108:111], v[66:69]
	s_waitcnt lgkmcnt(1)
	v_mfma_f32_16x16x32_f16 v[62:65], v[10:13], v[38:41], v[62:65]
	s_waitcnt lgkmcnt(0)
	v_mfma_f32_16x16x32_f16 v[10:13], v[10:13], v[42:45], v[74:77]
	s_nop 2
	ds_read_b128 v[74:77], v107 offset:16384
	v_mfma_f32_16x16x32_f16 v[30:33], v[18:21], v[30:33], v[50:53]
	v_mfma_f32_16x16x32_f16 v[66:69], v[18:21], v[38:41], v[66:69]
	v_mfma_f32_16x16x32_f16 v[98:101], v[18:21], v[42:45], v[14:17]
	ds_read_b128 v[104:107], v107 offset:18432
	s_nop 1
	ds_read_b128 v[14:17], v103 offset:24576
	ds_read_b128 v[18:21], v103 offset:26624
	s_waitcnt lgkmcnt(1)
	v_mfma_f32_16x16x32_f16 v[54:57], v[74:77], v[14:17], v[46:49]
	v_mfma_f32_16x16x32_f16 v[50:53], v[104:107], v[14:17], v[22:25]
	s_waitcnt lgkmcnt(0)
	v_mfma_f32_16x16x32_f16 v[46:49], v[74:77], v[18:21], v[34:37]
	v_mfma_f32_16x16x32_f16 v[42:45], v[104:107], v[18:21], v[26:29]
	ds_read_b128 v[14:17], v103 offset:28672
	ds_read_b128 v[18:21], v103 offset:30720
	s_waitcnt lgkmcnt(1)
	v_mfma_f32_16x16x32_f16 v[38:41], v[74:77], v[14:17], v[70:73]
	v_mfma_f32_16x16x32_f16 v[34:37], v[104:107], v[14:17], v[30:33]
	s_waitcnt lgkmcnt(0)
	v_mfma_f32_16x16x32_f16 v[26:29], v[104:107], v[18:21], v[58:61]
	ds_read_b128 v[14:17], v103 offset:32768
	s_nop 1
	ds_read_b128 v[58:61], v103 offset:34816
	s_waitcnt lgkmcnt(1)
	v_mfma_f32_16x16x32_f16 v[22:25], v[74:77], v[14:17], v[62:65]
	s_nop 2
	v_lshlrev_b32_e32 v62, 1, v92
	v_mov_b32_e32 v63, 0
	v_mfma_f32_16x16x32_f16 v[30:33], v[74:77], v[18:21], v[94:97]
	v_mfma_f32_16x16x32_f16 v[18:21], v[104:107], v[14:17], v[66:69]
	s_waitcnt lgkmcnt(0)
	v_mfma_f32_16x16x32_f16 v[14:17], v[74:77], v[58:61], v[10:13]
	s_nop 2
	v_lshl_add_u64 v[10:11], s[0:1], 0, v[62:63]
	v_lshlrev_b32_e32 v62, 1, v0
	v_lshl_add_u64 v[0:1], v[10:11], 0, v[62:63]
	v_mfma_f32_16x16x32_f16 v[10:13], v[104:107], v[58:61], v[98:101]
	v_mbcnt_lo_u32_b32 v196, -1, 0
	v_mbcnt_hi_u32_b32 v196, -1, v196
	v_and_b32_e32 v197, 15, v196
	v_lshrrev_b32_e32 v198, 4, v196
	v_lshrrev_b32_e32 v222, 10, v81
	s_nop 0
	v_readfirstlane_b32 s36, v222
	s_nop 3
	s_and_b32 s36, s36, 7
	s_mulk_i32 s36, 0x500
	v_mul_u32_u24_e32 v199, 0x50, v197
	v_lshl_add_u32 v199, v198, 3, v199
	v_add_u32_e32 v199, s36, v199
	v_lshrrev_b32_e32 v200, 2, v196
	v_and_b32_e32 v201, 3, v196
	v_mul_u32_u24_e32 v202, 0x50, v200
	v_lshl_add_u32 v202, v201, 4, v202
	v_add_u32_e32 v202, s36, v202
	v_lshlrev_b32_e32 v203, 2, v200
	v_add_u32_e32 v204, 32, v203
	v_lshlrev_b32_e32 v220, 4, v201
	v_mov_b32_e32 v221, 0
	v_sub_u32_e32 v205, v79, v197
	v_add_u32_e32 v205, v205, v200
	s_mov_b64 s[0:1], exec
	s_cbranch_execz .LBB3_56
	v_add_f32_e32 v55, v7, v55
	v_ashrrev_i32_e32 v91, 31, v90
	v_add_f32_e32 v54, v6, v54
	v_max_f32_e32 v60, 0, v55
	v_add_f32_e32 v55, v8, v56
	v_add_f32_e32 v56, v9, v57
	v_lshlrev_b64 v[58:59], 11, v[90:91]
	v_max_f32_e32 v54, 0, v54
	v_max_f32_e32 v55, 0, v55
	v_max_f32_e32 v56, 0, v56
	v_lshl_add_u64 v[58:59], v[0:1], 0, v[58:59]
	v_cvt_pk_f16_f32 v55, v55, v56
	v_cvt_pk_f16_f32 v54, v54, v60
	v_add_f32_e32 v51, v3, v51
	ds_write_b64 v199, v[54:55]
	v_add_f32_e32 v50, v2, v50
	v_max_f32_e32 v54, 0, v51
	v_add_f32_e32 v51, v4, v52
	v_add_f32_e32 v52, v5, v53
	v_max_f32_e32 v50, 0, v50
	v_max_f32_e32 v51, 0, v51
	v_max_f32_e32 v52, 0, v52
	v_cvt_pk_f16_f32 v51, v51, v52
	v_cvt_pk_f16_f32 v50, v50, v54
	ds_write_b64 v199, v[50:51] offset:32
	ds_read_b128 v[208:211], v202
	ds_bpermute_b32 v216, v203, v58
	ds_bpermute_b32 v217, v203, v59
	v_add_u32_e32 v222, 0, v205
	v_cmp_gt_u32_e64 s[38:39], s18, v222
.LBB3_56:
	s_or_b64 exec, exec, s[0:1]
	v_or_b32_e32 v50, 16, v79
	v_cmp_gt_u32_e32 vcc, s18, v50
	s_mov_b64 s[0:1], exec
	s_cbranch_execz .LBB3_58
	v_add_f32_e32 v47, v7, v47
	v_ashrrev_i32_e32 v89, 31, v88
	v_add_f32_e32 v46, v6, v46
	v_max_f32_e32 v52, 0, v47
	v_add_f32_e32 v47, v8, v48
	v_add_f32_e32 v48, v9, v49
	v_lshlrev_b64 v[50:51], 11, v[88:89]
	v_max_f32_e32 v46, 0, v46
	v_max_f32_e32 v47, 0, v47
	v_max_f32_e32 v48, 0, v48
	v_lshl_add_u64 v[50:51], v[0:1], 0, v[50:51]
	v_cvt_pk_f16_f32 v47, v47, v48
	v_cvt_pk_f16_f32 v46, v46, v52
	v_add_f32_e32 v43, v3, v43
	ds_write_b64 v199, v[46:47]
	v_add_f32_e32 v42, v2, v42
	v_max_f32_e32 v46, 0, v43
	v_add_f32_e32 v43, v4, v44
	v_add_f32_e32 v44, v5, v45
	v_max_f32_e32 v42, 0, v42
	v_max_f32_e32 v43, 0, v43
	v_max_f32_e32 v44, 0, v44
	v_cvt_pk_f16_f32 v43, v43, v44
	v_cvt_pk_f16_f32 v42, v42, v46
	ds_write_b64 v199, v[42:43] offset:32
	s_waitcnt lgkmcnt(2)
	v_lshl_add_u64 v[216:217], v[216:217], 0, v[220:221]
	s_mov_b64 s[42:43], exec
	s_and_b64 exec, s[42:43], s[38:39]
	global_store_dwordx4 v[216:217], v[208:211], off sc1
	s_mov_b64 exec, s[42:43]
	ds_read_b128 v[208:211], v202
	ds_bpermute_b32 v216, v203, v50
	ds_bpermute_b32 v217, v203, v51
	v_add_u32_e32 v222, 16, v205
	v_cmp_gt_u32_e64 s[38:39], s18, v222
.LBB3_58:
	s_or_b64 exec, exec, s[0:1]
	v_add_u32_e32 v42, 32, v79
	v_cmp_gt_u32_e32 vcc, s18, v42
	s_mov_b64 s[0:1], exec
	s_cbranch_execz .LBB3_60
	v_add_f32_e32 v39, v7, v39
	v_ashrrev_i32_e32 v87, 31, v86
	v_add_f32_e32 v38, v6, v38
	v_max_f32_e32 v44, 0, v39
	v_add_f32_e32 v39, v8, v40
	v_add_f32_e32 v40, v9, v41
	v_lshlrev_b64 v[42:43], 11, v[86:87]
	v_max_f32_e32 v38, 0, v38
	v_max_f32_e32 v39, 0, v39
	v_max_f32_e32 v40, 0, v40
	v_lshl_add_u64 v[42:43], v[0:1], 0, v[42:43]
	v_cvt_pk_f16_f32 v39, v39, v40
	v_cvt_pk_f16_f32 v38, v38, v44
	v_add_f32_e32 v35, v3, v35
	ds_write_b64 v199, v[38:39]
	v_add_f32_e32 v34, v2, v34
	v_max_f32_e32 v38, 0, v35
	v_add_f32_e32 v35, v4, v36
	v_add_f32_e32 v36, v5, v37
	v_max_f32_e32 v34, 0, v34
	v_max_f32_e32 v35, 0, v35
	v_max_f32_e32 v36, 0, v36
	v_cvt_pk_f16_f32 v35, v35, v36
	v_cvt_pk_f16_f32 v34, v34, v38
	ds_write_b64 v199, v[34:35] offset:32
	s_waitcnt lgkmcnt(2)
	v_lshl_add_u64 v[216:217], v[216:217], 0, v[220:221]
	s_mov_b64 s[42:43], exec
	s_and_b64 exec, s[42:43], s[38:39]
	global_store_dwordx4 v[216:217], v[208:211], off sc1
	s_mov_b64 exec, s[42:43]
	ds_read_b128 v[208:211], v202
	ds_bpermute_b32 v216, v203, v42
	ds_bpermute_b32 v217, v203, v43
	v_add_u32_e32 v222, 32, v205
	v_cmp_gt_u32_e64 s[38:39], s18, v222
.LBB3_60:
	s_or_b64 exec, exec, s[0:1]
	v_add_u32_e32 v34, 48, v79
	v_cmp_gt_u32_e32 vcc, s18, v34
	s_mov_b64 s[0:1], exec
	s_cbranch_execz .LBB3_62
	v_add_f32_e32 v31, v7, v31
	v_ashrrev_i32_e32 v83, 31, v82
	v_add_f32_e32 v30, v6, v30
	v_max_f32_e32 v36, 0, v31
	v_add_f32_e32 v31, v8, v32
	v_add_f32_e32 v32, v9, v33
	v_lshlrev_b64 v[34:35], 11, v[82:83]
	v_max_f32_e32 v30, 0, v30
	v_max_f32_e32 v31, 0, v31
	v_max_f32_e32 v32, 0, v32
	v_lshl_add_u64 v[34:35], v[0:1], 0, v[34:35]
	v_cvt_pk_f16_f32 v31, v31, v32
	v_cvt_pk_f16_f32 v30, v30, v36
	v_add_f32_e32 v27, v3, v27
	ds_write_b64 v199, v[30:31]
	v_add_f32_e32 v26, v2, v26
	v_max_f32_e32 v30, 0, v27
	v_add_f32_e32 v27, v4, v28
	v_add_f32_e32 v28, v5, v29
	v_max_f32_e32 v26, 0, v26
	v_max_f32_e32 v27, 0, v27
	v_max_f32_e32 v28, 0, v28
	v_cvt_pk_f16_f32 v27, v27, v28
	v_cvt_pk_f16_f32 v26, v26, v30
	ds_write_b64 v199, v[26:27] offset:32
	s_waitcnt lgkmcnt(2)
	v_lshl_add_u64 v[216:217], v[216:217], 0, v[220:221]
	s_mov_b64 s[42:43], exec
	s_and_b64 exec, s[42:43], s[38:39]
	global_store_dwordx4 v[216:217], v[208:211], off sc1
	s_mov_b64 exec, s[42:43]
	ds_read_b128 v[208:211], v202
	ds_bpermute_b32 v216, v203, v34
	ds_bpermute_b32 v217, v203, v35
	v_add_u32_e32 v222, 48, v205
	v_cmp_gt_u32_e64 s[38:39], s18, v222
.LBB3_62:
	s_or_b64 exec, exec, s[0:1]
	v_add_u32_e32 v26, 64, v79
	v_cmp_gt_u32_e32 vcc, s18, v26
	s_mov_b64 s[0:1], exec
	s_cbranch_execz .LBB3_64
	v_add_f32_e32 v23, v7, v23
	v_ashrrev_i32_e32 v81, 31, v80
	v_add_f32_e32 v22, v6, v22
	v_max_f32_e32 v28, 0, v23
	v_add_f32_e32 v23, v8, v24
	v_add_f32_e32 v24, v9, v25
	v_lshlrev_b64 v[26:27], 11, v[80:81]
	v_max_f32_e32 v22, 0, v22
	v_max_f32_e32 v23, 0, v23
	v_max_f32_e32 v24, 0, v24
	v_lshl_add_u64 v[26:27], v[0:1], 0, v[26:27]
	v_cvt_pk_f16_f32 v23, v23, v24
	v_cvt_pk_f16_f32 v22, v22, v28
	v_add_f32_e32 v19, v3, v19
	ds_write_b64 v199, v[22:23]
	v_add_f32_e32 v18, v2, v18
	v_max_f32_e32 v22, 0, v19
	v_add_f32_e32 v19, v4, v20
	v_add_f32_e32 v20, v5, v21
	v_max_f32_e32 v18, 0, v18
	v_max_f32_e32 v19, 0, v19
	v_max_f32_e32 v20, 0, v20
	v_cvt_pk_f16_f32 v19, v19, v20
	v_cvt_pk_f16_f32 v18, v18, v22
	ds_write_b64 v199, v[18:19] offset:32
	s_waitcnt lgkmcnt(2)
	v_lshl_add_u64 v[216:217], v[216:217], 0, v[220:221]
	s_mov_b64 s[42:43], exec
	s_and_b64 exec, s[42:43], s[38:39]
	global_store_dwordx4 v[216:217], v[208:211], off sc1
	s_mov_b64 exec, s[42:43]
	ds_read_b128 v[208:211], v202
	ds_bpermute_b32 v216, v203, v26
	ds_bpermute_b32 v217, v203, v27
	v_add_u32_e32 v222, 64, v205
	v_cmp_gt_u32_e64 s[38:39], s18, v222
.LBB3_64:
	s_or_b64 exec, exec, s[0:1]
	v_add_u32_e32 v18, 0x50, v79
	v_cmp_gt_u32_e32 vcc, s18, v18
	s_mov_b64 s[0:1], exec
	s_cbranch_execz .LBB3_66
	v_add_f32_e32 v7, v7, v15
	v_ashrrev_i32_e32 v79, 31, v78
	v_add_f32_e32 v6, v6, v14
	v_max_f32_e32 v14, 0, v7
	v_add_f32_e32 v7, v8, v16
	v_add_f32_e32 v8, v9, v17
	v_lshlrev_b64 v[18:19], 11, v[78:79]
	v_max_f32_e32 v6, 0, v6
	v_max_f32_e32 v7, 0, v7
	v_max_f32_e32 v8, 0, v8
	v_lshl_add_u64 v[0:1], v[0:1], 0, v[18:19]
	v_cvt_pk_f16_f32 v7, v7, v8
	v_cvt_pk_f16_f32 v6, v6, v14
	v_add_f32_e32 v3, v3, v11
	ds_write_b64 v199, v[6:7]
	v_add_f32_e32 v2, v2, v10
	v_max_f32_e32 v6, 0, v3
	v_add_f32_e32 v3, v4, v12
	v_add_f32_e32 v4, v5, v13
	v_max_f32_e32 v2, 0, v2
	v_max_f32_e32 v3, 0, v3
	v_max_f32_e32 v4, 0, v4
	v_cvt_pk_f16_f32 v3, v3, v4
	v_cvt_pk_f16_f32 v2, v2, v6
	ds_write_b64 v199, v[2:3] offset:32
	s_waitcnt lgkmcnt(2)
	v_lshl_add_u64 v[216:217], v[216:217], 0, v[220:221]
	s_mov_b64 s[42:43], exec
	s_and_b64 exec, s[42:43], s[38:39]
	global_store_dwordx4 v[216:217], v[208:211], off sc1
	s_mov_b64 exec, s[42:43]
	ds_read_b128 v[208:211], v202
	ds_bpermute_b32 v216, v203, v0
	ds_bpermute_b32 v217, v203, v1
	v_add_u32_e32 v222, 80, v205
	v_cmp_gt_u32_e64 s[38:39], s18, v222
	s_waitcnt lgkmcnt(0)
	v_lshl_add_u64 v[216:217], v[216:217], 0, v[220:221]
	s_mov_b64 s[42:43], exec
	s_and_b64 exec, s[42:43], s[38:39]
	global_store_dwordx4 v[216:217], v[208:211], off sc1
	s_mov_b64 exec, s[42:43]

.LBB4_37:
	s_or_b64 exec, exec, s[6:7]
	s_waitcnt vmcnt(3)
	ds_write_b128 v154, v[42:45]
	s_waitcnt vmcnt(2)
	ds_write_b128 v154, v[46:49] offset:8192
	s_waitcnt vmcnt(1)
	ds_write_b128 v154, v[50:53] offset:16384
	s_waitcnt vmcnt(0)
	ds_write_b128 v154, v[54:57] offset:24576
	s_waitcnt lgkmcnt(0)
	s_barrier
	ds_read_b128 v[26:29], v162 offset:57344
	ds_read_b128 v[34:37], v161 offset:12288
	ds_read_b128 v[42:45], v162 offset:59392
	ds_read_b128 v[46:49], v161 offset:14336
	ds_read_b128 v[54:57], v162 offset:61440
	s_waitcnt lgkmcnt(3)
	v_mfma_f32_16x16x32_f16 v[50:53], v[26:29], v[34:37], v[78:81]
	s_lshl_b64 s[2:3], s[16:17], 1
	s_add_u32 s2, s10, s2
	s_addc_u32 s3, s11, s3
	s_waitcnt lgkmcnt(2)
	v_mfma_f32_16x16x32_f16 v[78:81], v[42:45], v[34:37], v[82:85]
	v_cmp_gt_u32_e32 vcc, s24, v133
	s_waitcnt lgkmcnt(0)
	v_mfma_f32_16x16x32_f16 v[82:85], v[54:57], v[34:37], v[86:89]
	s_nop 2
	ds_read_b128 v[86:89], v162 offset:63488
	ds_read_b128 v[90:93], v160 offset:12288
	ds_read_b128 v[98:101], v163 offset:59392
	ds_read_b128 v[102:105], v163 offset:61440
	s_waitcnt lgkmcnt(3)
	v_mfma_f32_16x16x32_f16 v[22:25], v[86:89], v[34:37], v[22:25]
	v_mfma_f32_16x16x32_f16 v[34:37], v[26:29], v[46:49], v[58:61]
	v_mfma_f32_16x16x32_f16 v[94:97], v[42:45], v[46:49], v[62:65]
	v_mfma_f32_16x16x32_f16 v[66:69], v[54:57], v[46:49], v[66:69]
	v_mfma_f32_16x16x32_f16 v[70:73], v[86:89], v[46:49], v[70:73]
	ds_read_b128 v[46:49], v161 offset:16384
	s_waitcnt lgkmcnt(0)
	v_mfma_f32_16x16x32_f16 v[26:29], v[26:29], v[46:49], v[30:33]
	s_nop 2
	ds_read_b128 v[30:33], v163 offset:57344
	v_mfma_f32_16x16x32_f16 v[58:61], v[98:101], v[90:93], v[78:81]
	s_nop 2
	ds_read_b128 v[78:81], v163 offset:63488
	v_mfma_f32_16x16x32_f16 v[18:21], v[54:57], v[46:49], v[18:21]
	s_waitcnt lgkmcnt(1)
	v_mfma_f32_16x16x32_f16 v[62:65], v[30:33], v[90:93], v[50:53]
	v_mfma_f32_16x16x32_f16 v[54:57], v[102:105], v[90:93], v[82:85]
	s_waitcnt lgkmcnt(0)
	v_mfma_f32_16x16x32_f16 v[50:53], v[78:81], v[90:93], v[22:25]
	s_nop 2
	ds_read_b128 v[22:25], v160 offset:14336
	ds_read_b128 v[82:85], v160 offset:16384
	v_mfma_f32_16x16x32_f16 v[74:77], v[42:45], v[46:49], v[74:77]
	v_mfma_f32_16x16x32_f16 v[86:89], v[86:89], v[46:49], v[38:41]
	s_waitcnt lgkmcnt(1)
	v_mfma_f32_16x16x32_f16 v[38:41], v[102:105], v[22:25], v[66:69]
	s_nop 2
	v_lshlrev_b32_e32 v66, 1, v135
	v_mov_b32_e32 v67, 0
	v_mfma_f32_16x16x32_f16 v[46:49], v[30:33], v[22:25], v[34:37]
	v_mfma_f32_16x16x32_f16 v[42:45], v[98:101], v[22:25], v[94:97]
	v_mfma_f32_16x16x32_f16 v[34:37], v[78:81], v[22:25], v[70:73]
	s_waitcnt lgkmcnt(0)
	v_mfma_f32_16x16x32_f16 v[22:25], v[102:105], v[82:85], v[18:21]
	s_nop 2
	v_lshl_add_u64 v[18:19], s[2:3], 0, v[66:67]
	v_lshlrev_b32_e32 v66, 1, v131
	v_mfma_f32_16x16x32_f16 v[30:33], v[30:33], v[82:85], v[26:29]
	v_lshl_add_u64 v[66:67], v[18:19], 0, v[66:67]
	v_mfma_f32_16x16x32_f16 v[26:29], v[98:101], v[82:85], v[74:77]
	v_mfma_f32_16x16x32_f16 v[18:21], v[78:81], v[82:85], v[86:89]
	v_mbcnt_lo_u32_b32 v196, -1, 0
	v_mbcnt_hi_u32_b32 v196, -1, v196
	v_and_b32_e32 v197, 15, v196
	v_lshrrev_b32_e32 v198, 4, v196
	v_lshrrev_b32_e32 v222, 10, v137
	s_nop 0
	v_readfirstlane_b32 s36, v222
	s_nop 3
	s_and_b32 s36, s36, 7
	s_mulk_i32 s36, 0x900
	s_add_u32 s36, s36, 0x6000
	v_mul_u32_u24_e32 v199, 0x90, v197
	v_lshl_add_u32 v199, v198, 3, v199
	v_add_u32_e32 v199, s36, v199
	v_lshrrev_b32_e32 v200, 3, v196
	v_and_b32_e32 v201, 7, v196
	v_mul_u32_u24_e32 v202, 0x90, v200
	v_lshl_add_u32 v202, v201, 4, v202
	v_add_u32_e32 v202, s36, v202
	v_lshlrev_b32_e32 v203, 2, v200
	v_add_u32_e32 v204, 32, v203
	v_lshlrev_b32_e32 v220, 4, v201
	v_mov_b32_e32 v221, 0
	v_sub_u32_e32 v205, v133, v197
	v_add_u32_e32 v205, v205, v200
	s_mov_b64 s[2:3], exec
	s_cbranch_execz .LBB4_39
	v_add_f32_e32 v63, v15, v63
	v_ashrrev_i32_e32 v137, 31, v136
	v_add_f32_e32 v62, v14, v62
	v_max_f32_e32 v70, 0, v63
	v_add_f32_e32 v63, v16, v64
	v_add_f32_e32 v64, v17, v65
	v_lshlrev_b64 v[68:69], 11, v[136:137]
	v_max_f32_e32 v62, 0, v62
	v_max_f32_e32 v63, 0, v63
	v_max_f32_e32 v64, 0, v64
	v_lshl_add_u64 v[68:69], v[66:67], 0, v[68:69]
	v_cvt_pk_f16_f32 v63, v63, v64
	v_cvt_pk_f16_f32 v62, v62, v70
	v_add_f32_e32 v59, v11, v59
	ds_write_b64 v199, v[62:63]
	v_add_f32_e32 v58, v10, v58
	v_max_f32_e32 v62, 0, v59
	v_add_f32_e32 v59, v12, v60
	v_add_f32_e32 v60, v13, v61
	v_max_f32_e32 v58, 0, v58
	v_max_f32_e32 v59, 0, v59
	v_max_f32_e32 v60, 0, v60
	v_cvt_pk_f16_f32 v59, v59, v60
	v_cvt_pk_f16_f32 v58, v58, v62
	v_add_f32_e32 v55, v7, v55
	ds_write_b64 v199, v[58:59] offset:32
	v_add_f32_e32 v54, v6, v54
	v_max_f32_e32 v58, 0, v55
	v_add_f32_e32 v55, v8, v56
	v_add_f32_e32 v56, v9, v57
	v_max_f32_e32 v54, 0, v54
	v_max_f32_e32 v55, 0, v55
	v_max_f32_e32 v56, 0, v56
	v_cvt_pk_f16_f32 v55, v55, v56
	v_cvt_pk_f16_f32 v54, v54, v58
	v_add_f32_e32 v51, v3, v51
	ds_write_b64 v199, v[54:55] offset:64
	v_add_f32_e32 v50, v2, v50
	v_max_f32_e32 v54, 0, v51
	v_add_f32_e32 v51, v4, v52
	v_add_f32_e32 v52, v5, v53
	v_max_f32_e32 v50, 0, v50
	v_max_f32_e32 v51, 0, v51
	v_max_f32_e32 v52, 0, v52
	v_cvt_pk_f16_f32 v51, v51, v52
	v_cvt_pk_f16_f32 v50, v50, v54
	ds_write_b64 v199, v[50:51] offset:96
	ds_read_b128 v[208:211], v202
	ds_read_b128 v[212:215], v202 offset:1152
	ds_bpermute_b32 v216, v203, v68
	ds_bpermute_b32 v217, v203, v69
	ds_bpermute_b32 v218, v204, v68
	ds_bpermute_b32 v219, v204, v69
	v_add_u32_e32 v222, 0, v205
	v_cmp_gt_u32_e64 s[38:39], s24, v222
	v_add_u32_e32 v222, 8, v222
	v_cmp_gt_u32_e64 s[40:41], s24, v222
.LBB4_39:
	s_or_b64 exec, exec, s[2:3]
	v_add_u32_e32 v50, 16, v133
	v_cmp_gt_u32_e32 vcc, s24, v50
	s_mov_b64 s[2:3], exec
	s_cbranch_execz .LBB4_41
	v_add_f32_e32 v47, v15, v47
	v_ashrrev_i32_e32 v135, 31, v134
	v_add_f32_e32 v46, v14, v46
	v_max_f32_e32 v52, 0, v47
	v_add_f32_e32 v47, v16, v48
	v_add_f32_e32 v48, v17, v49
	v_lshlrev_b64 v[50:51], 11, v[134:135]
	v_max_f32_e32 v46, 0, v46
	v_max_f32_e32 v47, 0, v47
	v_max_f32_e32 v48, 0, v48
	v_lshl_add_u64 v[50:51], v[66:67], 0, v[50:51]
	v_cvt_pk_f16_f32 v47, v47, v48
	v_cvt_pk_f16_f32 v46, v46, v52
	v_add_f32_e32 v43, v11, v43
	ds_write_b64 v199, v[46:47]
	v_add_f32_e32 v42, v10, v42
	v_max_f32_e32 v46, 0, v43
	v_add_f32_e32 v43, v12, v44
	v_add_f32_e32 v44, v13, v45
	v_max_f32_e32 v42, 0, v42
	v_max_f32_e32 v43, 0, v43
	v_max_f32_e32 v44, 0, v44
	v_cvt_pk_f16_f32 v43, v43, v44
	v_cvt_pk_f16_f32 v42, v42, v46
	v_add_f32_e32 v39, v7, v39
	ds_write_b64 v199, v[42:43] offset:32
	v_add_f32_e32 v38, v6, v38
	v_max_f32_e32 v42, 0, v39
	v_add_f32_e32 v39, v8, v40
	v_add_f32_e32 v40, v9, v41
	v_max_f32_e32 v38, 0, v38
	v_max_f32_e32 v39, 0, v39
	v_max_f32_e32 v40, 0, v40
	v_cvt_pk_f16_f32 v39, v39, v40
	v_cvt_pk_f16_f32 v38, v38, v42
	v_add_f32_e32 v35, v3, v35
	ds_write_b64 v199, v[38:39] offset:64
	v_add_f32_e32 v34, v2, v34
	v_max_f32_e32 v38, 0, v35
	v_add_f32_e32 v35, v4, v36
	v_add_f32_e32 v36, v5, v37
	v_max_f32_e32 v34, 0, v34
	v_max_f32_e32 v35, 0, v35
	v_max_f32_e32 v36, 0, v36
	v_cvt_pk_f16_f32 v35, v35, v36
	v_cvt_pk_f16_f32 v34, v34, v38
	ds_write_b64 v199, v[34:35] offset:96
	s_waitcnt lgkmcnt(4)
	v_lshl_add_u64 v[216:217], v[216:217], 0, v[220:221]
	v_lshl_add_u64 v[218:219], v[218:219], 0, v[220:221]
	s_mov_b64 s[42:43], exec
	s_and_b64 exec, s[42:43], s[38:39]
	global_store_dwordx4 v[216:217], v[208:211], off sc1
	s_and_b64 exec, s[42:43], s[40:41]
	global_store_dwordx4 v[218:219], v[212:215], off sc1
	s_mov_b64 exec, s[42:43]
	ds_read_b128 v[208:211], v202
	ds_read_b128 v[212:215], v202 offset:1152
	ds_bpermute_b32 v216, v203, v50
	ds_bpermute_b32 v217, v203, v51
	ds_bpermute_b32 v218, v204, v50
	ds_bpermute_b32 v219, v204, v51
	v_add_u32_e32 v222, 16, v205
	v_cmp_gt_u32_e64 s[38:39], s24, v222
	v_add_u32_e32 v222, 8, v222
	v_cmp_gt_u32_e64 s[40:41], s24, v222
.LBB4_41:
	s_or_b64 exec, exec, s[2:3]
	v_add_u32_e32 v34, 32, v133
	v_cmp_gt_u32_e32 vcc, s24, v34
	s_mov_b64 s[2:3], exec
	s_cbranch_execz .LBB4_43
	v_add_f32_e32 v15, v15, v31
	v_ashrrev_i32_e32 v133, 31, v132
	v_add_f32_e32 v14, v14, v30
	v_max_f32_e32 v30, 0, v15
	v_add_f32_e32 v15, v16, v32
	v_add_f32_e32 v16, v17, v33
	v_lshlrev_b64 v[34:35], 11, v[132:133]
	v_max_f32_e32 v14, 0, v14
	v_max_f32_e32 v15, 0, v15
	v_max_f32_e32 v16, 0, v16
	v_lshl_add_u64 v[34:35], v[66:67], 0, v[34:35]
	v_cvt_pk_f16_f32 v15, v15, v16
	v_cvt_pk_f16_f32 v14, v14, v30
	v_add_f32_e32 v11, v11, v27
	ds_write_b64 v199, v[14:15]
	v_add_f32_e32 v10, v10, v26
	v_max_f32_e32 v14, 0, v11
	v_add_f32_e32 v11, v12, v28
	v_add_f32_e32 v12, v13, v29
	v_max_f32_e32 v10, 0, v10
	v_max_f32_e32 v11, 0, v11
	v_max_f32_e32 v12, 0, v12
	v_cvt_pk_f16_f32 v11, v11, v12
	v_cvt_pk_f16_f32 v10, v10, v14
	v_add_f32_e32 v7, v7, v23
	ds_write_b64 v199, v[10:11] offset:32
	v_add_f32_e32 v6, v6, v22
	v_max_f32_e32 v10, 0, v7
	v_add_f32_e32 v7, v8, v24
	v_add_f32_e32 v8, v9, v25
	v_max_f32_e32 v6, 0, v6
	v_max_f32_e32 v7, 0, v7
	v_max_f32_e32 v8, 0, v8
	v_cvt_pk_f16_f32 v7, v7, v8
	v_cvt_pk_f16_f32 v6, v6, v10
	v_add_f32_e32 v3, v3, v19
	ds_write_b64 v199, v[6:7] offset:64
	v_add_f32_e32 v2, v2, v18
	v_max_f32_e32 v6, 0, v3
	v_add_f32_e32 v3, v4, v20
	v_add_f32_e32 v4, v5, v21
	v_max_f32_e32 v2, 0, v2
	v_max_f32_e32 v3, 0, v3
	v_max_f32_e32 v4, 0, v4
	v_cvt_pk_f16_f32 v3, v3, v4
	v_cvt_pk_f16_f32 v2, v2, v6
	ds_write_b64 v199, v[2:3] offset:96
	s_waitcnt lgkmcnt(4)
	v_lshl_add_u64 v[216:217], v[216:217], 0, v[220:221]
	v_lshl_add_u64 v[218:219], v[218:219], 0, v[220:221]
	s_mov_b64 s[42:43], exec
	s_and_b64 exec, s[42:43], s[38:39]
	global_store_dwordx4 v[216:217], v[208:211], off sc1
	s_and_b64 exec, s[42:43], s[40:41]
	global_store_dwordx4 v[218:219], v[212:215], off sc1
	s_mov_b64 exec, s[42:43]
	ds_read_b128 v[208:211], v202
	ds_read_b128 v[212:215], v202 offset:1152
	ds_bpermute_b32 v216, v203, v34
	ds_bpermute_b32 v217, v203, v35
	ds_bpermute_b32 v218, v204, v34
	ds_bpermute_b32 v219, v204, v35
	v_add_u32_e32 v222, 32, v205
	v_cmp_gt_u32_e64 s[38:39], s24, v222
	v_add_u32_e32 v222, 8, v222
	v_cmp_gt_u32_e64 s[40:41], s24, v222
	s_waitcnt lgkmcnt(0)
	v_lshl_add_u64 v[216:217], v[216:217], 0, v[220:221]
	v_lshl_add_u64 v[218:219], v[218:219], 0, v[220:221]
	s_mov_b64 s[42:43], exec
	s_and_b64 exec, s[42:43], s[38:39]
	global_store_dwordx4 v[216:217], v[208:211], off sc1
	s_and_b64 exec, s[42:43], s[40:41]
	global_store_dwordx4 v[218:219], v[212:215], off sc1
	s_mov_b64 exec, s[42:43]

.LBB4_55:
	s_or_b64 exec, exec, s[4:5]
	s_waitcnt vmcnt(1)
	ds_write_b128 v78, v[14:17] offset:40960
	s_waitcnt vmcnt(0)
	ds_write_b128 v78, v[22:25] offset:49152
	s_waitcnt lgkmcnt(0)
	s_barrier
	ds_read_b128 v[14:17], v82 offset:40960
	ds_read_b128 v[18:21], v81 offset:12288
	ds_read_b128 v[22:25], v81 offset:14336
	ds_read_b128 v[46:49], v82 offset:43008
	ds_read_b128 v[50:53], v79 offset:12288
	s_waitcnt lgkmcnt(3)
	v_mfma_f32_16x16x32_f16 v[42:45], v[14:17], v[18:21], v[42:45]
	ds_read_b128 v[54:57], v80 offset:43008
	s_lshl_b64 s[0:1], s[0:1], 1
	s_add_u32 s0, s10, s0
	s_waitcnt lgkmcnt(2)
	v_mfma_f32_16x16x32_f16 v[10:13], v[46:49], v[18:21], v[10:13]
	s_addc_u32 s1, s11, s1
	v_lshlrev_b32_e32 v0, 1, v67
	v_mov_b32_e32 v1, 0
	v_mfma_f32_16x16x32_f16 v[18:21], v[14:17], v[22:25], v[34:37]
	v_cmp_gt_u32_e32 vcc, s24, v63
	v_mfma_f32_16x16x32_f16 v[34:37], v[46:49], v[22:25], v[38:41]
	ds_read_b128 v[22:25], v81 offset:16384
	s_nop 1
	ds_read_b128 v[38:41], v80 offset:40960
	s_waitcnt lgkmcnt(1)
	v_mfma_f32_16x16x32_f16 v[14:17], v[14:17], v[22:25], v[30:33]
	v_mfma_f32_16x16x32_f16 v[46:49], v[46:49], v[22:25], v[26:29]
	s_waitcnt lgkmcnt(0)
	v_mfma_f32_16x16x32_f16 v[30:33], v[38:41], v[50:53], v[42:45]
	v_mfma_f32_16x16x32_f16 v[26:29], v[54:57], v[50:53], v[10:13]
	s_nop 2
	ds_read_b128 v[10:13], v79 offset:14336
	ds_read_b128 v[42:45], v79 offset:16384
	s_waitcnt lgkmcnt(1)
	v_mfma_f32_16x16x32_f16 v[22:25], v[38:41], v[10:13], v[18:21]
	v_mfma_f32_16x16x32_f16 v[18:21], v[54:57], v[10:13], v[34:37]
	v_lshl_add_u64 v[10:11], s[0:1], 0, v[0:1]
	v_lshlrev_b32_e32 v0, 1, v65
	v_lshl_add_u64 v[0:1], v[10:11], 0, v[0:1]
	s_waitcnt lgkmcnt(0)
	v_mfma_f32_16x16x32_f16 v[14:17], v[38:41], v[42:45], v[14:17]
	v_mfma_f32_16x16x32_f16 v[10:13], v[54:57], v[42:45], v[46:49]
	v_mbcnt_lo_u32_b32 v196, -1, 0
	v_mbcnt_hi_u32_b32 v196, -1, v196
	v_and_b32_e32 v197, 15, v196
	v_lshrrev_b32_e32 v198, 4, v196
	v_lshrrev_b32_e32 v222, 10, v78
	s_nop 0
	v_readfirstlane_b32 s36, v222
	s_nop 3
	s_and_b32 s36, s36, 7
	s_mulk_i32 s36, 0x500
	s_add_u32 s36, s36, 0x6000
	v_mul_u32_u24_e32 v199, 0x50, v197
	v_lshl_add_u32 v199, v198, 3, v199
	v_add_u32_e32 v199, s36, v199
	v_lshrrev_b32_e32 v200, 2, v196
	v_and_b32_e32 v201, 3, v196
	v_mul_u32_u24_e32 v202, 0x50, v200
	v_lshl_add_u32 v202, v201, 4, v202
	v_add_u32_e32 v202, s36, v202
	v_lshlrev_b32_e32 v203, 2, v200
	v_add_u32_e32 v204, 32, v203
	v_lshlrev_b32_e32 v220, 4, v201
	v_mov_b32_e32 v221, 0
	v_sub_u32_e32 v205, v63, v197
	v_add_u32_e32 v205, v205, v200
	s_mov_b64 s[0:1], exec
	s_cbranch_execz .LBB4_57
	v_add_f32_e32 v31, v7, v31
	v_ashrrev_i32_e32 v67, 31, v66
	v_add_f32_e32 v30, v6, v30
	v_max_f32_e32 v36, 0, v31
	v_add_f32_e32 v31, v8, v32
	v_add_f32_e32 v32, v9, v33
	v_lshlrev_b64 v[34:35], 11, v[66:67]
	v_max_f32_e32 v30, 0, v30
	v_max_f32_e32 v31, 0, v31
	v_max_f32_e32 v32, 0, v32
	v_lshl_add_u64 v[34:35], v[0:1], 0, v[34:35]
	v_cvt_pk_f16_f32 v31, v31, v32
	v_cvt_pk_f16_f32 v30, v30, v36
	v_add_f32_e32 v27, v3, v27
	ds_write_b64 v199, v[30:31]
	v_add_f32_e32 v26, v2, v26
	v_max_f32_e32 v30, 0, v27
	v_add_f32_e32 v27, v4, v28
	v_add_f32_e32 v28, v5, v29
	v_max_f32_e32 v26, 0, v26
	v_max_f32_e32 v27, 0, v27
	v_max_f32_e32 v28, 0, v28
	v_cvt_pk_f16_f32 v27, v27, v28
	v_cvt_pk_f16_f32 v26, v26, v30
	ds_write_b64 v199, v[26:27] offset:32
	ds_read_b128 v[208:211], v202
	ds_bpermute_b32 v216, v203, v34
	ds_bpermute_b32 v217, v203, v35
	v_add_u32_e32 v222, 0, v205
	v_cmp_gt_u32_e64 s[38:39], s24, v222
.LBB4_57:
	s_or_b64 exec, exec, s[0:1]
	v_add_u32_e32 v26, 16, v63
	v_cmp_gt_u32_e32 vcc, s24, v26
	s_mov_b64 s[0:1], exec
	s_cbranch_execz .LBB4_59
	v_add_f32_e32 v23, v7, v23
	v_ashrrev_i32_e32 v65, 31, v64
	v_add_f32_e32 v22, v6, v22
	v_max_f32_e32 v28, 0, v23
	v_add_f32_e32 v23, v8, v24
	v_add_f32_e32 v24, v9, v25
	v_lshlrev_b64 v[26:27], 11, v[64:65]
	v_max_f32_e32 v22, 0, v22
	v_max_f32_e32 v23, 0, v23
	v_max_f32_e32 v24, 0, v24
	v_lshl_add_u64 v[26:27], v[0:1], 0, v[26:27]
	v_cvt_pk_f16_f32 v23, v23, v24
	v_cvt_pk_f16_f32 v22, v22, v28
	v_add_f32_e32 v19, v3, v19
	ds_write_b64 v199, v[22:23]
	v_add_f32_e32 v18, v2, v18
	v_max_f32_e32 v22, 0, v19
	v_add_f32_e32 v19, v4, v20
	v_add_f32_e32 v20, v5, v21
	v_max_f32_e32 v18, 0, v18
	v_max_f32_e32 v19, 0, v19
	v_max_f32_e32 v20, 0, v20
	v_cvt_pk_f16_f32 v19, v19, v20
	v_cvt_pk_f16_f32 v18, v18, v22
	ds_write_b64 v199, v[18:19] offset:32
	s_waitcnt lgkmcnt(2)
	v_lshl_add_u64 v[216:217], v[216:217], 0, v[220:221]
	s_mov_b64 s[42:43], exec
	s_and_b64 exec, s[42:43], s[38:39]
	global_store_dwordx4 v[216:217], v[208:211], off sc1
	s_mov_b64 exec, s[42:43]
	ds_read_b128 v[208:211], v202
	ds_bpermute_b32 v216, v203, v26
	ds_bpermute_b32 v217, v203, v27
	v_add_u32_e32 v222, 16, v205
	v_cmp_gt_u32_e64 s[38:39], s24, v222
.LBB4_59:
	s_or_b64 exec, exec, s[0:1]
	v_add_u32_e32 v18, 32, v63
	v_cmp_gt_u32_e32 vcc, s24, v18
	s_mov_b64 s[0:1], exec
	s_cbranch_execz .LBB4_61
	v_add_f32_e32 v7, v7, v15
	v_ashrrev_i32_e32 v63, 31, v62
	v_add_f32_e32 v6, v6, v14
	v_max_f32_e32 v14, 0, v7
	v_add_f32_e32 v7, v8, v16
	v_add_f32_e32 v8, v9, v17
	v_lshlrev_b64 v[18:19], 11, v[62:63]
	v_max_f32_e32 v6, 0, v6
	v_max_f32_e32 v7, 0, v7
	v_max_f32_e32 v8, 0, v8
	v_lshl_add_u64 v[0:1], v[0:1], 0, v[18:19]
	v_cvt_pk_f16_f32 v7, v7, v8
	v_cvt_pk_f16_f32 v6, v6, v14
	v_add_f32_e32 v3, v3, v11
	ds_write_b64 v199, v[6:7]
	v_add_f32_e32 v2, v2, v10
	v_max_f32_e32 v6, 0, v3
	v_add_f32_e32 v3, v4, v12
	v_add_f32_e32 v4, v5, v13
	v_max_f32_e32 v2, 0, v2
	v_max_f32_e32 v3, 0, v3
	v_max_f32_e32 v4, 0, v4
	v_cvt_pk_f16_f32 v3, v3, v4
	v_cvt_pk_f16_f32 v2, v2, v6
	ds_write_b64 v199, v[2:3] offset:32
	s_waitcnt lgkmcnt(2)
	v_lshl_add_u64 v[216:217], v[216:217], 0, v[220:221]
	s_mov_b64 s[42:43], exec
	s_and_b64 exec, s[42:43], s[38:39]
	global_store_dwordx4 v[216:217], v[208:211], off sc1
	s_mov_b64 exec, s[42:43]
	ds_read_b128 v[208:211], v202
	ds_bpermute_b32 v216, v203, v0
	ds_bpermute_b32 v217, v203, v1
	v_add_u32_e32 v222, 32, v205
	v_cmp_gt_u32_e64 s[38:39], s24, v222
	s_waitcnt lgkmcnt(0)
	v_lshl_add_u64 v[216:217], v[216:217], 0, v[220:221]
	s_mov_b64 s[42:43], exec
	s_and_b64 exec, s[42:43], s[38:39]
	global_store_dwordx4 v[216:217], v[208:211], off sc1
	s_mov_b64 exec, s[42:43]

.LBB5_17:
	s_lshl_b64 s[10:11], s[10:11], 1
	s_add_u32 s10, s6, s10
	s_addc_u32 s11, s7, s11
	s_lshl_b32 s12, s23, 1
	s_add_u32 s10, s10, s12
	s_addc_u32 s11, s11, 0
	v_lshlrev_b32_e32 v76, 1, v75
	v_mov_b32_e32 v77, 0
	v_lshl_add_u64 v[76:77], s[10:11], 0, v[76:77]
	v_cmp_gt_u32_e32 vcc, s20, v68
	v_mbcnt_lo_u32_b32 v196, -1, 0
	v_mbcnt_hi_u32_b32 v196, -1, v196
	v_and_b32_e32 v197, 15, v196
	v_lshrrev_b32_e32 v198, 4, v196
	v_readfirstlane_b32 s36, v68
	s_nop 3
	s_cmp_ge_u32 s36, 48
	s_cselect_b32 s36, 2, 0
	s_lshr_b32 s37, s23, 6
	s_add_u32 s36, s36, s37
	s_mulk_i32 s36, 0x900
	s_add_u32 s36, s36, 0xa000
	v_mul_u32_u24_e32 v199, 0x90, v197
	v_lshl_add_u32 v199, v198, 3, v199
	v_add_u32_e32 v199, s36, v199
	v_lshrrev_b32_e32 v200, 3, v196
	v_and_b32_e32 v201, 7, v196
	v_mul_u32_u24_e32 v202, 0x90, v200
	v_lshl_add_u32 v202, v201, 4, v202
	v_add_u32_e32 v202, s36, v202
	v_lshlrev_b32_e32 v203, 2, v200
	v_add_u32_e32 v204, 32, v203
	v_lshlrev_b32_e32 v220, 4, v201
	v_mov_b32_e32 v221, 0
	v_sub_u32_e32 v205, v68, v197
	v_add_u32_e32 v205, v205, v200
	s_mov_b64 s[10:11], exec
	s_cbranch_execz .LBB5_19
	v_add_f32_e32 v63, v15, v63
	v_ashrrev_i32_e32 v75, 31, v74
	v_add_f32_e32 v62, v14, v62
	v_max_f32_e32 v69, 0, v63
	v_add_f32_e32 v63, v16, v64
	v_add_f32_e32 v64, v17, v65
	v_lshlrev_b64 v[74:75], 11, v[74:75]
	v_max_f32_e32 v62, 0, v62
	v_max_f32_e32 v63, 0, v63
	v_max_f32_e32 v64, 0, v64
	v_lshl_add_u64 v[74:75], v[76:77], 0, v[74:75]
	v_cvt_pk_f16_f32 v63, v63, v64
	v_cvt_pk_f16_f32 v62, v62, v69
	v_add_f32_e32 v59, v11, v59
	ds_write_b64 v199, v[62:63]
	v_add_f32_e32 v58, v10, v58
	v_max_f32_e32 v62, 0, v59
	v_add_f32_e32 v59, v12, v60
	v_add_f32_e32 v60, v13, v61
	v_max_f32_e32 v58, 0, v58
	v_max_f32_e32 v59, 0, v59
	v_max_f32_e32 v60, 0, v60
	v_cvt_pk_f16_f32 v59, v59, v60
	v_cvt_pk_f16_f32 v58, v58, v62
	v_add_f32_e32 v55, v7, v55
	ds_write_b64 v199, v[58:59] offset:32
	v_add_f32_e32 v54, v6, v54
	v_max_f32_e32 v58, 0, v55
	v_add_f32_e32 v55, v8, v56
	v_add_f32_e32 v56, v9, v57
	v_max_f32_e32 v54, 0, v54
	v_max_f32_e32 v55, 0, v55
	v_max_f32_e32 v56, 0, v56
	v_cvt_pk_f16_f32 v55, v55, v56
	v_cvt_pk_f16_f32 v54, v54, v58
	v_add_f32_e32 v47, v3, v47
	ds_write_b64 v199, v[54:55] offset:64
	v_add_f32_e32 v46, v2, v46
	v_max_f32_e32 v54, 0, v47
	v_add_f32_e32 v47, v4, v48
	v_add_f32_e32 v48, v5, v49
	v_max_f32_e32 v46, 0, v46
	v_max_f32_e32 v47, 0, v47
	v_max_f32_e32 v48, 0, v48
	v_cvt_pk_f16_f32 v47, v47, v48
	v_cvt_pk_f16_f32 v46, v46, v54
	ds_write_b64 v199, v[46:47] offset:96
	ds_read_b128 v[208:211], v202
	ds_read_b128 v[212:215], v202 offset:1152
	ds_bpermute_b32 v216, v203, v74
	ds_bpermute_b32 v217, v203, v75
	ds_bpermute_b32 v218, v204, v74
	ds_bpermute_b32 v219, v204, v75
	v_add_u32_e32 v222, 0, v205
	v_cmp_gt_u32_e64 s[38:39], s20, v222
	v_add_u32_e32 v222, 8, v222
	v_cmp_gt_u32_e64 s[40:41], s20, v222
.LBB5_19:
	s_or_b64 exec, exec, s[10:11]
	v_add_u32_e32 v46, 16, v68
	v_cmp_gt_u32_e32 vcc, s20, v46
	s_mov_b64 s[10:11], exec
	s_cbranch_execz .LBB5_21
	v_add_f32_e32 v43, v15, v43
	v_ashrrev_i32_e32 v73, 31, v72
	v_add_f32_e32 v42, v14, v42
	v_max_f32_e32 v48, 0, v43
	v_add_f32_e32 v43, v16, v44
	v_add_f32_e32 v44, v17, v45
	v_lshlrev_b64 v[46:47], 11, v[72:73]
	v_max_f32_e32 v42, 0, v42
	v_max_f32_e32 v43, 0, v43
	v_max_f32_e32 v44, 0, v44
	v_lshl_add_u64 v[46:47], v[76:77], 0, v[46:47]
	v_cvt_pk_f16_f32 v43, v43, v44
	v_cvt_pk_f16_f32 v42, v42, v48
	v_add_f32_e32 v39, v11, v39
	ds_write_b64 v199, v[42:43]
	v_add_f32_e32 v38, v10, v38
	v_max_f32_e32 v42, 0, v39
	v_add_f32_e32 v39, v12, v40
	v_add_f32_e32 v40, v13, v41
	v_max_f32_e32 v38, 0, v38
	v_max_f32_e32 v39, 0, v39
	v_max_f32_e32 v40, 0, v40
	v_cvt_pk_f16_f32 v39, v39, v40
	v_cvt_pk_f16_f32 v38, v38, v42
	v_add_f32_e32 v35, v7, v35
	ds_write_b64 v199, v[38:39] offset:32
	v_add_f32_e32 v34, v6, v34
	v_max_f32_e32 v38, 0, v35
	v_add_f32_e32 v35, v8, v36
	v_add_f32_e32 v36, v9, v37
	v_max_f32_e32 v34, 0, v34
	v_max_f32_e32 v35, 0, v35
	v_max_f32_e32 v36, 0, v36
	v_cvt_pk_f16_f32 v35, v35, v36
	v_cvt_pk_f16_f32 v34, v34, v38
	v_add_f32_e32 v31, v3, v31
	ds_write_b64 v199, v[34:35] offset:64
	v_add_f32_e32 v30, v2, v30
	v_max_f32_e32 v34, 0, v31
	v_add_f32_e32 v31, v4, v32
	v_add_f32_e32 v32, v5, v33
	v_max_f32_e32 v30, 0, v30
	v_max_f32_e32 v31, 0, v31
	v_max_f32_e32 v32, 0, v32
	v_cvt_pk_f16_f32 v31, v31, v32
	v_cvt_pk_f16_f32 v30, v30, v34
	ds_write_b64 v199, v[30:31] offset:96
	s_waitcnt lgkmcnt(4)
	v_lshl_add_u64 v[216:217], v[216:217], 0, v[220:221]
	v_lshl_add_u64 v[218:219], v[218:219], 0, v[220:221]
	s_mov_b64 s[42:43], exec
	s_and_b64 exec, s[42:43], s[38:39]
	global_store_dwordx4 v[216:217], v[208:211], off sc1
	s_and_b64 exec, s[42:43], s[40:41]
	global_store_dwordx4 v[218:219], v[212:215], off sc1
	s_mov_b64 exec, s[42:43]
	ds_read_b128 v[208:211], v202
	ds_read_b128 v[212:215], v202 offset:1152
	ds_bpermute_b32 v216, v203, v46
	ds_bpermute_b32 v217, v203, v47
	ds_bpermute_b32 v218, v204, v46
	ds_bpermute_b32 v219, v204, v47
	v_add_u32_e32 v222, 16, v205
	v_cmp_gt_u32_e64 s[38:39], s20, v222
	v_add_u32_e32 v222, 8, v222
	v_cmp_gt_u32_e64 s[40:41], s20, v222
.LBB5_21:
	s_or_b64 exec, exec, s[10:11]
	v_add_u32_e32 v30, 32, v68
	v_cmp_gt_u32_e32 vcc, s20, v30
	s_mov_b64 s[10:11], exec
	s_cbranch_execz .LBB5_23
	v_add_f32_e32 v15, v15, v27
	v_ashrrev_i32_e32 v71, 31, v70
	v_add_f32_e32 v14, v14, v26
	v_max_f32_e32 v26, 0, v15
	v_add_f32_e32 v15, v16, v28
	v_add_f32_e32 v16, v17, v29
	v_lshlrev_b64 v[30:31], 11, v[70:71]
	v_max_f32_e32 v14, 0, v14
	v_max_f32_e32 v15, 0, v15
	v_max_f32_e32 v16, 0, v16
	v_lshl_add_u64 v[30:31], v[76:77], 0, v[30:31]
	v_cvt_pk_f16_f32 v15, v15, v16
	v_cvt_pk_f16_f32 v14, v14, v26
	v_add_f32_e32 v11, v11, v23
	ds_write_b64 v199, v[14:15]
	v_add_f32_e32 v10, v10, v22
	v_max_f32_e32 v14, 0, v11
	v_add_f32_e32 v11, v12, v24
	v_add_f32_e32 v12, v13, v25
	v_max_f32_e32 v10, 0, v10
	v_max_f32_e32 v11, 0, v11
	v_max_f32_e32 v12, 0, v12
	v_cvt_pk_f16_f32 v11, v11, v12
	v_cvt_pk_f16_f32 v10, v10, v14
	v_add_f32_e32 v7, v7, v19
	ds_write_b64 v199, v[10:11] offset:32
	v_add_f32_e32 v6, v6, v18
	v_max_f32_e32 v10, 0, v7
	v_add_f32_e32 v7, v8, v20
	v_add_f32_e32 v8, v9, v21
	v_max_f32_e32 v6, 0, v6
	v_max_f32_e32 v7, 0, v7
	v_max_f32_e32 v8, 0, v8
	v_cvt_pk_f16_f32 v7, v7, v8
	v_cvt_pk_f16_f32 v6, v6, v10
	v_add_f32_e32 v3, v3, v51
	ds_write_b64 v199, v[6:7] offset:64
	v_add_f32_e32 v2, v2, v50
	v_max_f32_e32 v6, 0, v3
	v_add_f32_e32 v3, v4, v52
	v_add_f32_e32 v4, v5, v53
	v_max_f32_e32 v2, 0, v2
	v_max_f32_e32 v3, 0, v3
	v_max_f32_e32 v4, 0, v4
	v_cvt_pk_f16_f32 v3, v3, v4
	v_cvt_pk_f16_f32 v2, v2, v6
	ds_write_b64 v199, v[2:3] offset:96
	s_waitcnt lgkmcnt(4)
	v_lshl_add_u64 v[216:217], v[216:217], 0, v[220:221]
	v_lshl_add_u64 v[218:219], v[218:219], 0, v[220:221]
	s_mov_b64 s[42:43], exec
	s_and_b64 exec, s[42:43], s[38:39]
	global_store_dwordx4 v[216:217], v[208:211], off sc1
	s_and_b64 exec, s[42:43], s[40:41]
	global_store_dwordx4 v[218:219], v[212:215], off sc1
	s_mov_b64 exec, s[42:43]
	ds_read_b128 v[208:211], v202
	ds_read_b128 v[212:215], v202 offset:1152
	ds_bpermute_b32 v216, v203, v30
	ds_bpermute_b32 v217, v203, v31
	ds_bpermute_b32 v218, v204, v30
	ds_bpermute_b32 v219, v204, v31
	v_add_u32_e32 v222, 32, v205
	v_cmp_gt_u32_e64 s[38:39], s20, v222
	v_add_u32_e32 v222, 8, v222
	v_cmp_gt_u32_e64 s[40:41], s20, v222
	s_waitcnt lgkmcnt(0)
	v_lshl_add_u64 v[216:217], v[216:217], 0, v[220:221]
	v_lshl_add_u64 v[218:219], v[218:219], 0, v[220:221]
	s_mov_b64 s[42:43], exec
	s_and_b64 exec, s[42:43], s[38:39]
	global_store_dwordx4 v[216:217], v[208:211], off sc1
	s_and_b64 exec, s[42:43], s[40:41]
	global_store_dwordx4 v[218:219], v[212:215], off sc1
	s_mov_b64 exec, s[42:43]

.LBB5_26:
	s_mul_i32 s4, s13, 0xa000
	s_add_i32 s4, s4, 0
	v_add_u32_e32 v35, s4, v43
	s_add_i32 s4, s4, s12
	v_add_u32_e32 v80, s4, v41
	s_waitcnt vmcnt(5)
	s_barrier
	v_add_u32_e32 v60, v80, v39
	ds_read_b128 v[56:59], v60 offset:24576
	ds_read_b128 v[60:63], v60 offset:26624
	v_add_u32_e32 v68, v35, v39
	ds_read_b128 v[52:55], v68
	v_add_u32_e32 v35, v35, v37
	s_waitcnt lgkmcnt(0)
	v_mfma_f32_16x16x32_f16 v[26:29], v[56:59], v[52:55], v[26:29]
	ds_read_b128 v[64:67], v68 offset:2048
	v_add_u32_e32 v82, v80, v37
	s_cmp_gt_i32 s13, 0
	v_mfma_f32_16x16x32_f16 v[30:33], v[60:63], v[52:55], v[30:33]
	ds_read_b128 v[52:55], v68 offset:4096
	s_cselect_b32 s4, -1, 2
	s_add_i32 s4, s4, s13
	s_waitcnt lgkmcnt(0)
	v_mfma_f32_16x16x32_f16 v[22:25], v[56:59], v[64:67], v[22:25]
	ds_read_b128 v[68:71], v35
	s_mul_i32 s4, s4, 0xa000
	s_add_i32 s4, s9, s4
	v_mfma_f32_16x16x32_f16 v[18:21], v[60:63], v[64:67], v[18:21]
	ds_read_b128 v[64:67], v82 offset:24576
	v_lshl_add_u64 v[72:73], v[44:45], 0, s[2:3]
	s_mov_b32 m0, s4
	v_mfma_f32_16x16x32_f16 v[14:17], v[56:59], v[52:55], v[14:17]
	ds_read_b128 v[56:59], v82 offset:26624
	v_lshl_add_u64 v[74:75], v[46:47], 0, s[2:3]
	v_lshl_add_u64 v[76:77], v[0:1], 0, s[2:3]
	v_mfma_f32_16x16x32_f16 v[10:13], v[60:63], v[52:55], v[10:13]
	ds_read_b128 v[52:55], v35 offset:2048
	v_lshl_add_u64 v[78:79], v[48:49], 0, s[2:3]
	v_lshl_add_u64 v[80:81], v[50:51], 0, s[2:3]
	s_waitcnt lgkmcnt(0)
	v_mfma_f32_16x16x32_f16 v[26:29], v[64:67], v[68:71], v[26:29]
	ds_read_b128 v[60:63], v35 offset:4096
	v_mfma_f32_16x16x32_f16 v[30:33], v[56:59], v[68:71], v[30:33]
	global_load_lds_dwordx4 v[72:73], off
	s_add_i32 m0, s4, 0x1000
	v_mfma_f32_16x16x32_f16 v[22:25], v[64:67], v[52:55], v[22:25]
	global_load_lds_dwordx4 v[74:75], off
	s_add_i32 m0, s4, 0x2000
	v_mfma_f32_16x16x32_f16 v[18:21], v[56:59], v[52:55], v[18:21]
	global_load_lds_dwordx4 v[76:77], off
	s_add_i32 m0, s4, 0x6000
	s_waitcnt lgkmcnt(0)
	v_mfma_f32_16x16x32_f16 v[14:17], v[64:67], v[60:63], v[14:17]
	global_load_lds_dwordx4 v[78:79], off
	s_add_i32 m0, s4, 0x7000
	v_mfma_f32_16x16x32_f16 v[10:13], v[56:59], v[60:63], v[10:13]
	global_load_lds_dwordx4 v[80:81], off
	s_add_i32 s4, s13, 1
	s_cmp_lg_u32 s13, 2
	s_cselect_b32 s13, s4, 0
	s_add_u32 s2, s2, 0x80
	s_addc_u32 s3, s3, 0
	s_cmpk_lg_i32 s2, 0xf00
	s_cbranch_scc1 .LBB5_26
	s_add_i32 s2, s12, 0
	v_add_u32_e32 v0, s2, v41
	s_waitcnt vmcnt(5)
	s_barrier
	v_add_u32_e32 v1, v0, v39
	ds_read_b128 v[44:47], v1 offset:24576
	v_add_u32_e32 v35, 0, v43
	v_add_u32_e32 v43, v35, v39
	ds_read_b128 v[48:51], v43
	ds_read_b128 v[52:55], v1 offset:26624
	v_add_u32_e32 v1, v35, v37
	s_waitcnt lgkmcnt(0)
	v_mfma_f32_16x16x32_f16 v[26:29], v[44:47], v[48:51], v[26:29]
	ds_read_b128 v[56:59], v43 offset:2048
	v_add_u32_e32 v0, v0, v37
	s_add_i32 s2, s2, 0x10000
	v_mfma_f32_16x16x32_f16 v[30:33], v[52:55], v[48:51], v[30:33]
	ds_read_b128 v[48:51], v43 offset:4096
	s_lshl_b64 s[0:1], s[0:1], 1
	s_add_u32 s0, s6, s0
	s_waitcnt lgkmcnt(0)
	v_mfma_f32_16x16x32_f16 v[22:25], v[44:47], v[56:59], v[22:25]
	ds_read_b128 v[60:63], v1
	s_addc_u32 s1, s7, s1
	v_cmp_gt_u32_e32 vcc, s20, v34
	v_mfma_f32_16x16x32_f16 v[18:21], v[52:55], v[56:59], v[18:21]
	ds_read_b128 v[56:59], v0 offset:24576
	v_mfma_f32_16x16x32_f16 v[14:17], v[44:47], v[48:51], v[14:17]
	ds_read_b128 v[44:47], v0 offset:26624
	v_add_u32_e32 v0, s2, v41
	v_add_u32_e32 v35, v0, v39
	v_mfma_f32_16x16x32_f16 v[10:13], v[52:55], v[48:51], v[10:13]
	ds_read_b128 v[48:51], v1 offset:2048
	v_add_u32_e32 v0, v0, v37
	s_lshl_b32 s2, s8, 1
	s_waitcnt lgkmcnt(0)
	v_mfma_f32_16x16x32_f16 v[26:29], v[56:59], v[60:63], v[26:29]
	ds_read_b128 v[52:55], v1 offset:4096
	s_waitcnt vmcnt(0)
	s_barrier
	v_mfma_f32_16x16x32_f16 v[30:33], v[44:47], v[60:63], v[30:33]
	s_add_u32 s0, s0, s2
	s_addc_u32 s1, s1, 0
	v_mfma_f32_16x16x32_f16 v[22:25], v[56:59], v[48:51], v[22:25]
	v_mfma_f32_16x16x32_f16 v[18:21], v[44:47], v[48:51], v[18:21]
	s_waitcnt lgkmcnt(0)
	v_mfma_f32_16x16x32_f16 v[14:17], v[56:59], v[52:55], v[14:17]
	v_mfma_f32_16x16x32_f16 v[10:13], v[44:47], v[52:55], v[10:13]
	ds_read_b128 v[44:47], v35
	ds_read_b128 v[48:51], v43 offset:40960
	ds_read_b128 v[52:55], v35 offset:2048
	s_waitcnt lgkmcnt(0)
	v_mfma_f32_16x16x32_f16 v[26:29], v[44:47], v[48:51], v[26:29]
	ds_read_b128 v[56:59], v43 offset:43008
	v_mfma_f32_16x16x32_f16 v[48:51], v[52:55], v[48:51], v[30:33]
	s_nop 2
	ds_read_b128 v[30:33], v43 offset:45056
	s_waitcnt lgkmcnt(0)
	v_mfma_f32_16x16x32_f16 v[22:25], v[44:47], v[56:59], v[22:25]
	ds_read_b128 v[60:63], v1 offset:40960
	v_mfma_f32_16x16x32_f16 v[18:21], v[52:55], v[56:59], v[18:21]
	ds_read_b128 v[56:59], v0
	v_mfma_f32_16x16x32_f16 v[14:17], v[44:47], v[30:33], v[14:17]
	ds_read_b128 v[44:47], v0 offset:2048
	v_lshlrev_b32_e32 v0, 1, v42
	v_mfma_f32_16x16x32_f16 v[52:55], v[52:55], v[30:33], v[10:13]
	s_nop 2
	ds_read_b128 v[10:13], v1 offset:43008
	s_waitcnt lgkmcnt(0)
	v_mfma_f32_16x16x32_f16 v[30:33], v[56:59], v[60:63], v[26:29]
	ds_read_b128 v[64:67], v1 offset:45056
	v_mov_b32_e32 v1, 0
	v_lshl_add_u64 v[0:1], s[0:1], 0, v[0:1]
	v_mfma_f32_16x16x32_f16 v[26:29], v[44:47], v[60:63], v[48:51]
	v_mfma_f32_16x16x32_f16 v[22:25], v[56:59], v[10:13], v[22:25]
	v_mfma_f32_16x16x32_f16 v[18:21], v[44:47], v[10:13], v[18:21]
	s_waitcnt lgkmcnt(0)
	v_mfma_f32_16x16x32_f16 v[10:13], v[56:59], v[64:67], v[14:17]
	v_mfma_f32_16x16x32_f16 v[14:17], v[44:47], v[64:67], v[52:55]
	v_mbcnt_lo_u32_b32 v196, -1, 0
	v_mbcnt_hi_u32_b32 v196, -1, v196
	v_and_b32_e32 v197, 15, v196
	v_lshrrev_b32_e32 v198, 4, v196
	v_readfirstlane_b32 s36, v34
	s_nop 3
	s_cmp_ge_u32 s36, 48
	s_cselect_b32 s36, 2, 0
	s_add_u32 s36, s36, s18
	s_mulk_i32 s36, 0x500
	s_add_u32 s36, s36, 0x14000
	v_mul_u32_u24_e32 v199, 0x50, v197
	v_lshl_add_u32 v199, v198, 3, v199
	v_add_u32_e32 v199, s36, v199
	v_lshrrev_b32_e32 v200, 2, v196
	v_and_b32_e32 v201, 3, v196
	v_mul_u32_u24_e32 v202, 0x50, v200
	v_lshl_add_u32 v202, v201, 4, v202
	v_add_u32_e32 v202, s36, v202
	v_lshlrev_b32_e32 v203, 2, v200
	v_add_u32_e32 v204, 32, v203
	v_lshlrev_b32_e32 v220, 4, v201
	v_mov_b32_e32 v221, 0
	v_sub_u32_e32 v205, v34, v197
	v_add_u32_e32 v205, v205, v200
	s_mov_b64 s[0:1], exec
	s_cbranch_execz .LBB5_29
	v_add_f32_e32 v31, v7, v31
	s_waitcnt vmcnt(0)
	v_ashrrev_i32_e32 v41, 31, v40
	v_add_f32_e32 v30, v6, v30
	v_max_f32_e32 v35, 0, v31
	v_add_f32_e32 v31, v8, v32
	v_add_f32_e32 v32, v9, v33
	v_lshlrev_b64 v[40:41], 11, v[40:41]
	v_max_f32_e32 v30, 0, v30
	v_max_f32_e32 v31, 0, v31
	v_max_f32_e32 v32, 0, v32
	v_lshl_add_u64 v[40:41], v[0:1], 0, v[40:41]
	v_cvt_pk_f16_f32 v31, v31, v32
	v_cvt_pk_f16_f32 v30, v30, v35
	v_add_f32_e32 v27, v3, v27
	ds_write_b64 v199, v[30:31]
	v_add_f32_e32 v26, v2, v26
	v_max_f32_e32 v30, 0, v27
	v_add_f32_e32 v27, v4, v28
	v_add_f32_e32 v28, v5, v29
	v_max_f32_e32 v26, 0, v26
	v_max_f32_e32 v27, 0, v27
	v_max_f32_e32 v28, 0, v28
	v_cvt_pk_f16_f32 v27, v27, v28
	v_cvt_pk_f16_f32 v26, v26, v30
	ds_write_b64 v199, v[26:27] offset:32
	ds_read_b128 v[208:211], v202
	ds_bpermute_b32 v216, v203, v40
	ds_bpermute_b32 v217, v203, v41
	v_add_u32_e32 v222, 0, v205
	v_cmp_gt_u32_e64 s[38:39], s20, v222
.LBB5_29:
	s_or_b64 exec, exec, s[0:1]
	v_add_u32_e32 v26, 16, v34
	v_cmp_gt_u32_e32 vcc, s20, v26
	s_mov_b64 s[0:1], exec
	s_cbranch_execz .LBB5_31
	v_add_f32_e32 v23, v7, v23
	v_ashrrev_i32_e32 v39, 31, v38
	v_add_f32_e32 v22, v6, v22
	v_max_f32_e32 v28, 0, v23
	v_add_f32_e32 v23, v8, v24
	v_add_f32_e32 v24, v9, v25
	v_lshlrev_b64 v[26:27], 11, v[38:39]
	v_max_f32_e32 v22, 0, v22
	v_max_f32_e32 v23, 0, v23
	v_max_f32_e32 v24, 0, v24
	v_lshl_add_u64 v[26:27], v[0:1], 0, v[26:27]
	v_cvt_pk_f16_f32 v23, v23, v24
	v_cvt_pk_f16_f32 v22, v22, v28
	v_add_f32_e32 v19, v3, v19
	ds_write_b64 v199, v[22:23]
	v_add_f32_e32 v18, v2, v18
	v_max_f32_e32 v22, 0, v19
	v_add_f32_e32 v19, v4, v20
	v_add_f32_e32 v20, v5, v21
	v_max_f32_e32 v18, 0, v18
	v_max_f32_e32 v19, 0, v19
	v_max_f32_e32 v20, 0, v20
	v_cvt_pk_f16_f32 v19, v19, v20
	v_cvt_pk_f16_f32 v18, v18, v22
	ds_write_b64 v199, v[18:19] offset:32
	s_waitcnt lgkmcnt(2)
	v_lshl_add_u64 v[216:217], v[216:217], 0, v[220:221]
	s_mov_b64 s[42:43], exec
	s_and_b64 exec, s[42:43], s[38:39]
	global_store_dwordx4 v[216:217], v[208:211], off sc1
	s_mov_b64 exec, s[42:43]
	ds_read_b128 v[208:211], v202
	ds_bpermute_b32 v216, v203, v26
	ds_bpermute_b32 v217, v203, v27
	v_add_u32_e32 v222, 16, v205
	v_cmp_gt_u32_e64 s[38:39], s20, v222
.LBB5_31:
	s_or_b64 exec, exec, s[0:1]
	v_add_u32_e32 v18, 32, v34
	v_cmp_gt_u32_e32 vcc, s20, v18
	s_mov_b64 s[0:1], exec
	s_cbranch_execz .LBB5_33
	v_add_f32_e32 v7, v7, v11
	v_ashrrev_i32_e32 v37, 31, v36
	v_add_f32_e32 v6, v6, v10
	v_max_f32_e32 v10, 0, v7
	v_add_f32_e32 v7, v8, v12
	v_add_f32_e32 v8, v9, v13
	v_lshlrev_b64 v[18:19], 11, v[36:37]
	v_max_f32_e32 v6, 0, v6
	v_max_f32_e32 v7, 0, v7
	v_max_f32_e32 v8, 0, v8
	v_lshl_add_u64 v[0:1], v[0:1], 0, v[18:19]
	v_cvt_pk_f16_f32 v7, v7, v8
	v_cvt_pk_f16_f32 v6, v6, v10
	v_add_f32_e32 v3, v3, v15
	ds_write_b64 v199, v[6:7]
	v_add_f32_e32 v2, v2, v14
	v_max_f32_e32 v6, 0, v3
	v_add_f32_e32 v3, v4, v16
	v_add_f32_e32 v4, v5, v17
	v_max_f32_e32 v2, 0, v2
	v_max_f32_e32 v3, 0, v3
	v_max_f32_e32 v4, 0, v4
	v_cvt_pk_f16_f32 v3, v3, v4
	v_cvt_pk_f16_f32 v2, v2, v6
	ds_write_b64 v199, v[2:3] offset:32
	s_waitcnt lgkmcnt(2)
	v_lshl_add_u64 v[216:217], v[216:217], 0, v[220:221]
	s_mov_b64 s[42:43], exec
	s_and_b64 exec, s[42:43], s[38:39]
	global_store_dwordx4 v[216:217], v[208:211], off sc1
	s_mov_b64 exec, s[42:43]
	ds_read_b128 v[208:211], v202
	ds_bpermute_b32 v216, v203, v0
	ds_bpermute_b32 v217, v203, v1
	v_add_u32_e32 v222, 32, v205
	v_cmp_gt_u32_e64 s[38:39], s20, v222
	s_waitcnt lgkmcnt(0)
	v_lshl_add_u64 v[216:217], v[216:217], 0, v[220:221]
	s_mov_b64 s[42:43], exec
	s_and_b64 exec, s[42:43], s[38:39]
	global_store_dwordx4 v[216:217], v[208:211], off sc1
	s_mov_b64 exec, s[42:43]

.LBB6_39:
	ds_read_b128 v[14:17], v180 offset:24576
	ds_read_b128 v[18:21], v179
	ds_read_b128 v[22:25], v179 offset:4096
	ds_read_b128 v[82:85], v180 offset:28672
	ds_read_b128 v[86:89], v181
	s_waitcnt vmcnt(10)
	v_pk_add_f16 v10, v34, v10
	v_pk_add_f16 v11, v35, v11
	s_waitcnt lgkmcnt(3)
	v_mfma_f32_16x16x32_f16 v[78:81], v[14:17], v[18:21], v[98:101]
	v_pk_add_f16 v12, v36, v12
	v_pk_add_f16 v13, v37, v13
	v_cndmask_b32_e64 v12, v36, v12, s[2:3]
	s_waitcnt lgkmcnt(1)
	v_mfma_f32_16x16x32_f16 v[18:21], v[82:85], v[18:21], v[90:93]
	ds_read_b128 v[98:101], v183 offset:24576
	v_cndmask_b32_e64 v13, v37, v13, s[2:3]
	v_cndmask_b32_e64 v11, v35, v11, s[2:3]
	v_mfma_f32_16x16x32_f16 v[90:93], v[14:17], v[22:25], v[94:97]
	v_cndmask_b32_e64 v10, v34, v10, s[2:3]
	v_cmp_gt_u32_e32 vcc, s18, v170
	s_nop 0
	ds_read_b128 v[94:97], v179 offset:8192
	v_mfma_f32_16x16x32_f16 v[22:25], v[82:85], v[22:25], v[110:113]
	s_waitcnt lgkmcnt(0)
	v_mfma_f32_16x16x32_f16 v[14:17], v[14:17], v[94:97], v[114:117]
	v_mfma_f32_16x16x32_f16 v[82:85], v[82:85], v[94:97], v[118:121]
	ds_read_b128 v[94:97], v183 offset:28672
	v_mfma_f32_16x16x32_f16 v[78:81], v[98:101], v[86:89], v[78:81]
	s_waitcnt lgkmcnt(0)
	v_mfma_f32_16x16x32_f16 v[18:21], v[94:97], v[86:89], v[18:21]
	ds_read_b128 v[86:89], v181 offset:4096
	ds_read_b128 v[102:105], v181 offset:8192
	s_waitcnt lgkmcnt(1)
	v_mfma_f32_16x16x32_f16 v[90:93], v[98:101], v[86:89], v[90:93]
	v_mfma_f32_16x16x32_f16 v[22:25], v[94:97], v[86:89], v[22:25]
	ds_read_b128 v[86:89], v184 offset:24576
	s_waitcnt lgkmcnt(1)
	v_mfma_f32_16x16x32_f16 v[14:17], v[98:101], v[102:105], v[14:17]
	v_mfma_f32_16x16x32_f16 v[82:85], v[94:97], v[102:105], v[82:85]
	ds_read_b128 v[94:97], v182
	ds_read_b128 v[98:101], v182 offset:4096
	ds_read_b128 v[102:105], v184 offset:28672
	ds_read_b128 v[106:109], v185
	s_waitcnt lgkmcnt(3)
	v_mfma_f32_16x16x32_f16 v[78:81], v[86:89], v[94:97], v[78:81]
	s_waitcnt lgkmcnt(1)
	v_mfma_f32_16x16x32_f16 v[18:21], v[102:105], v[94:97], v[18:21]
	ds_read_b128 v[94:97], v182 offset:8192
	v_mfma_f32_16x16x32_f16 v[90:93], v[86:89], v[98:101], v[90:93]
	s_waitcnt lgkmcnt(0)
	v_mfma_f32_16x16x32_f16 v[14:17], v[86:89], v[94:97], v[14:17]
	ds_read_b128 v[86:89], v186 offset:24576
	v_mfma_f32_16x16x32_f16 v[82:85], v[102:105], v[94:97], v[82:85]
	ds_read_b128 v[94:97], v186 offset:28672
	v_mfma_f32_16x16x32_f16 v[22:25], v[102:105], v[98:101], v[22:25]
	ds_read_b128 v[98:101], v185 offset:4096
	ds_read_b128 v[102:105], v185 offset:8192
	ds_write_b128 v151, v[10:13] offset:12288
	s_waitcnt vmcnt(9)
	v_pk_add_f16 v10, v38, v26
	v_pk_add_f16 v11, v39, v27
	v_pk_add_f16 v12, v40, v28
	v_pk_add_f16 v13, v41, v29
	v_cndmask_b32_e64 v12, v40, v12, s[2:3]
	v_cndmask_b32_e64 v13, v41, v13, s[2:3]
	v_cndmask_b32_e64 v11, v39, v11, s[2:3]
	v_cndmask_b32_e64 v10, v38, v10, s[2:3]
	ds_write_b128 v151, v[10:13] offset:16384
	s_waitcnt vmcnt(8)
	v_pk_add_f16 v10, v42, v30
	v_pk_add_f16 v11, v43, v31
	v_pk_add_f16 v12, v44, v32
	v_pk_add_f16 v13, v45, v33
	v_cndmask_b32_e64 v12, v44, v12, s[2:3]
	v_cndmask_b32_e64 v13, v45, v13, s[2:3]
	v_cndmask_b32_e64 v11, v43, v11, s[2:3]
	v_cndmask_b32_e64 v10, v42, v10, s[2:3]
	s_waitcnt lgkmcnt(3)
	v_mfma_f32_16x16x32_f16 v[90:93], v[86:89], v[98:101], v[90:93]
	s_lshl_b64 s[2:3], s[14:15], 1
	s_add_u32 s2, s10, s2
	s_addc_u32 s3, s11, s3
	v_mfma_f32_16x16x32_f16 v[22:25], v[94:97], v[98:101], v[22:25]
	v_add_u32_e32 v98, 0xe000, v151
	ds_write_b128 v151, v[10:13] offset:20480
	s_waitcnt vmcnt(7)
	ds_write_b128 v151, v[46:49] offset:57344
	s_waitcnt vmcnt(6)
	ds_write_b128 v151, v[50:53] offset:61440
	s_waitcnt vmcnt(5)
	ds_write_b128 v98, v[54:57] offset:8192
	s_waitcnt vmcnt(4)
	ds_write_b128 v98, v[58:61] offset:12288
	s_waitcnt vmcnt(3)
	ds_write_b128 v98, v[62:65] offset:16384
	s_waitcnt vmcnt(2)
	ds_write_b128 v98, v[66:69] offset:20480
	s_waitcnt vmcnt(1)
	ds_write_b128 v98, v[70:73] offset:24576
	s_waitcnt vmcnt(0)
	ds_write_b128 v98, v[74:77] offset:28672
	s_waitcnt lgkmcnt(0)
	s_barrier
	ds_read_b128 v[10:13], v180 offset:57344
	ds_read_b128 v[30:33], v179 offset:12288
	ds_read_b128 v[34:37], v179 offset:16384
	v_mfma_f32_16x16x32_f16 v[78:81], v[86:89], v[106:109], v[78:81]
	ds_read_b128 v[42:45], v180 offset:61440
	ds_read_b128 v[46:49], v181 offset:12288
	v_mfma_f32_16x16x32_f16 v[18:21], v[94:97], v[106:109], v[18:21]
	s_waitcnt lgkmcnt(3)
	v_mfma_f32_16x16x32_f16 v[38:41], v[10:13], v[30:33], v[78:81]
	s_waitcnt lgkmcnt(1)
	v_mfma_f32_16x16x32_f16 v[18:21], v[42:45], v[30:33], v[18:21]
	v_mfma_f32_16x16x32_f16 v[30:33], v[10:13], v[34:37], v[90:93]
	v_mfma_f32_16x16x32_f16 v[22:25], v[42:45], v[34:37], v[22:25]
	ds_read_b128 v[34:37], v179 offset:20480
	v_mfma_f32_16x16x32_f16 v[14:17], v[86:89], v[102:105], v[14:17]
	v_mfma_f32_16x16x32_f16 v[26:29], v[94:97], v[102:105], v[82:85]
	s_waitcnt lgkmcnt(0)
	v_mfma_f32_16x16x32_f16 v[10:13], v[10:13], v[34:37], v[14:17]
	s_nop 4
	ds_read_b128 v[14:17], v183 offset:57344
	v_mfma_f32_16x16x32_f16 v[26:29], v[42:45], v[34:37], v[26:29]
	ds_read_b128 v[34:37], v183 offset:61440
	s_waitcnt lgkmcnt(1)
	v_mfma_f32_16x16x32_f16 v[38:41], v[14:17], v[46:49], v[38:41]
	s_waitcnt lgkmcnt(0)
	v_mfma_f32_16x16x32_f16 v[18:21], v[34:37], v[46:49], v[18:21]
	ds_read_b128 v[42:45], v181 offset:16384
	ds_read_b128 v[46:49], v181 offset:20480
	s_waitcnt lgkmcnt(1)
	v_mfma_f32_16x16x32_f16 v[30:33], v[14:17], v[42:45], v[30:33]
	s_waitcnt lgkmcnt(0)
	v_mfma_f32_16x16x32_f16 v[10:13], v[14:17], v[46:49], v[10:13]
	ds_read_b128 v[14:17], v184 offset:57344
	v_mfma_f32_16x16x32_f16 v[22:25], v[34:37], v[42:45], v[22:25]
	v_mfma_f32_16x16x32_f16 v[26:29], v[34:37], v[46:49], v[26:29]
	ds_read_b128 v[34:37], v182 offset:12288
	ds_read_b128 v[42:45], v182 offset:16384
	ds_read_b128 v[46:49], v184 offset:61440
	ds_read_b128 v[50:53], v185 offset:12288
	ds_read_b128 v[54:57], v186 offset:61440
	s_waitcnt lgkmcnt(4)
	v_mfma_f32_16x16x32_f16 v[38:41], v[14:17], v[34:37], v[38:41]
	s_waitcnt lgkmcnt(2)
	v_mfma_f32_16x16x32_f16 v[18:21], v[46:49], v[34:37], v[18:21]
	v_mfma_f32_16x16x32_f16 v[34:37], v[14:17], v[42:45], v[30:33]
	v_mfma_f32_16x16x32_f16 v[42:45], v[46:49], v[42:45], v[22:25]
	s_nop 2
	ds_read_b128 v[22:25], v182 offset:20480
	s_waitcnt lgkmcnt(0)
	v_mfma_f32_16x16x32_f16 v[10:13], v[14:17], v[22:25], v[10:13]
	ds_read_b128 v[14:17], v186 offset:57344
	v_mfma_f32_16x16x32_f16 v[46:49], v[46:49], v[22:25], v[26:29]
	s_waitcnt lgkmcnt(0)
	v_mfma_f32_16x16x32_f16 v[30:33], v[14:17], v[50:53], v[38:41]
	v_mfma_f32_16x16x32_f16 v[26:29], v[54:57], v[50:53], v[18:21]
	s_nop 2
	ds_read_b128 v[18:21], v185 offset:16384
	ds_read_b128 v[38:41], v185 offset:20480
	s_waitcnt lgkmcnt(1)
	v_mfma_f32_16x16x32_f16 v[22:25], v[14:17], v[18:21], v[34:37]
	s_nop 2
	v_lshlrev_b32_e32 v34, 1, v149
	v_mov_b32_e32 v35, 0
	s_waitcnt lgkmcnt(0)
	v_mfma_f32_16x16x32_f16 v[14:17], v[14:17], v[38:41], v[10:13]
	s_nop 2
	v_lshl_add_u64 v[10:11], s[2:3], 0, v[34:35]
	v_lshlrev_b32_e32 v34, 1, v147
	v_mfma_f32_16x16x32_f16 v[18:21], v[54:57], v[18:21], v[42:45]
	v_lshl_add_u64 v[34:35], v[10:11], 0, v[34:35]
	v_mfma_f32_16x16x32_f16 v[10:13], v[54:57], v[38:41], v[46:49]
	v_mbcnt_lo_u32_b32 v196, -1, 0
	v_mbcnt_hi_u32_b32 v196, -1, v196
	v_and_b32_e32 v197, 15, v196
	v_lshrrev_b32_e32 v198, 4, v196
	v_lshrrev_b32_e32 v222, 10, v151
	s_nop 0
	v_readfirstlane_b32 s36, v222
	s_nop 3
	s_and_b32 s36, s36, 7
	s_mulk_i32 s36, 0x500
	s_add_u32 s36, s36, 0x6000
	v_mul_u32_u24_e32 v199, 0x50, v197
	v_lshl_add_u32 v199, v198, 3, v199
	v_add_u32_e32 v199, s36, v199
	v_lshrrev_b32_e32 v200, 2, v196
	v_and_b32_e32 v201, 3, v196
	v_mul_u32_u24_e32 v202, 0x50, v200
	v_lshl_add_u32 v202, v201, 4, v202
	v_add_u32_e32 v202, s36, v202
	v_lshlrev_b32_e32 v203, 2, v200
	v_add_u32_e32 v204, 32, v203
	v_lshlrev_b32_e32 v220, 4, v201
	v_mov_b32_e32 v221, 0
	v_sub_u32_e32 v205, v170, v197
	v_add_u32_e32 v205, v205, v200
	s_mov_b64 s[2:3], exec
	s_cbranch_execz .LBB6_41
	v_add_f32_e32 v31, v7, v31
	v_ashrrev_i32_e32 v153, 31, v152
	v_add_f32_e32 v30, v6, v30
	v_max_f32_e32 v38, 0, v31
	v_add_f32_e32 v31, v8, v32
	v_add_f32_e32 v32, v9, v33
	v_lshlrev_b64 v[36:37], 11, v[152:153]
	v_max_f32_e32 v30, 0, v30
	v_max_f32_e32 v31, 0, v31
	v_max_f32_e32 v32, 0, v32
	v_lshl_add_u64 v[36:37], v[34:35], 0, v[36:37]
	v_cvt_pk_f16_f32 v31, v31, v32
	v_cvt_pk_f16_f32 v30, v30, v38
	v_add_f32_e32 v27, v3, v27
	ds_write_b64 v199, v[30:31]
	v_add_f32_e32 v26, v2, v26
	v_max_f32_e32 v30, 0, v27
	v_add_f32_e32 v27, v4, v28
	v_add_f32_e32 v28, v5, v29
	v_max_f32_e32 v26, 0, v26
	v_max_f32_e32 v27, 0, v27
	v_max_f32_e32 v28, 0, v28
	v_cvt_pk_f16_f32 v27, v27, v28
	v_cvt_pk_f16_f32 v26, v26, v30
	ds_write_b64 v199, v[26:27] offset:32
	ds_read_b128 v[208:211], v202
	ds_bpermute_b32 v216, v203, v36
	ds_bpermute_b32 v217, v203, v37
	v_add_u32_e32 v222, 0, v205
	v_cmp_gt_u32_e64 s[38:39], s18, v222
.LBB6_41:
	s_or_b64 exec, exec, s[2:3]
	v_or_b32_e32 v26, 16, v170
	v_cmp_gt_u32_e32 vcc, s18, v26
	s_mov_b64 s[2:3], exec
	s_cbranch_execz .LBB6_43
	v_add_f32_e32 v23, v7, v23
	v_ashrrev_i32_e32 v151, 31, v150
	v_add_f32_e32 v22, v6, v22
	v_max_f32_e32 v28, 0, v23
	v_add_f32_e32 v23, v8, v24
	v_add_f32_e32 v24, v9, v25
	v_lshlrev_b64 v[26:27], 11, v[150:151]
	v_max_f32_e32 v22, 0, v22
	v_max_f32_e32 v23, 0, v23
	v_max_f32_e32 v24, 0, v24
	v_lshl_add_u64 v[26:27], v[34:35], 0, v[26:27]
	v_cvt_pk_f16_f32 v23, v23, v24
	v_cvt_pk_f16_f32 v22, v22, v28
	v_add_f32_e32 v19, v3, v19
	ds_write_b64 v199, v[22:23]
	v_add_f32_e32 v18, v2, v18
	v_max_f32_e32 v22, 0, v19
	v_add_f32_e32 v19, v4, v20
	v_add_f32_e32 v20, v5, v21
	v_max_f32_e32 v18, 0, v18
	v_max_f32_e32 v19, 0, v19
	v_max_f32_e32 v20, 0, v20
	v_cvt_pk_f16_f32 v19, v19, v20
	v_cvt_pk_f16_f32 v18, v18, v22
	ds_write_b64 v199, v[18:19] offset:32
	s_waitcnt lgkmcnt(2)
	v_lshl_add_u64 v[216:217], v[216:217], 0, v[220:221]
	s_mov_b64 s[42:43], exec
	s_and_b64 exec, s[42:43], s[38:39]
	global_store_dwordx4 v[216:217], v[208:211], off sc1
	s_mov_b64 exec, s[42:43]
	ds_read_b128 v[208:211], v202
	ds_bpermute_b32 v216, v203, v26
	ds_bpermute_b32 v217, v203, v27
	v_add_u32_e32 v222, 16, v205
	v_cmp_gt_u32_e64 s[38:39], s18, v222
.LBB6_43:
	s_or_b64 exec, exec, s[2:3]
	v_or_b32_e32 v18, 32, v170
	v_cmp_gt_u32_e32 vcc, s18, v18
	s_mov_b64 s[2:3], exec
	s_cbranch_execz .LBB6_45
	v_add_f32_e32 v7, v7, v15
	v_ashrrev_i32_e32 v149, 31, v148
	v_add_f32_e32 v6, v6, v14
	v_max_f32_e32 v14, 0, v7
	v_add_f32_e32 v7, v8, v16
	v_add_f32_e32 v8, v9, v17
	v_lshlrev_b64 v[18:19], 11, v[148:149]
	v_max_f32_e32 v6, 0, v6
	v_max_f32_e32 v7, 0, v7
	v_max_f32_e32 v8, 0, v8
	v_lshl_add_u64 v[18:19], v[34:35], 0, v[18:19]
	v_cvt_pk_f16_f32 v7, v7, v8
	v_cvt_pk_f16_f32 v6, v6, v14
	v_add_f32_e32 v3, v3, v11
	ds_write_b64 v199, v[6:7]
	v_add_f32_e32 v2, v2, v10
	v_max_f32_e32 v6, 0, v3
	v_add_f32_e32 v3, v4, v12
	v_add_f32_e32 v4, v5, v13
	v_max_f32_e32 v2, 0, v2
	v_max_f32_e32 v3, 0, v3
	v_max_f32_e32 v4, 0, v4
	v_cvt_pk_f16_f32 v3, v3, v4
	v_cvt_pk_f16_f32 v2, v2, v6
	ds_write_b64 v199, v[2:3] offset:32
	s_waitcnt lgkmcnt(2)
	v_lshl_add_u64 v[216:217], v[216:217], 0, v[220:221]
	s_mov_b64 s[42:43], exec
	s_and_b64 exec, s[42:43], s[38:39]
	global_store_dwordx4 v[216:217], v[208:211], off sc1
	s_mov_b64 exec, s[42:43]
	ds_read_b128 v[208:211], v202
	ds_bpermute_b32 v216, v203, v18
	ds_bpermute_b32 v217, v203, v19
	v_add_u32_e32 v222, 32, v205
	v_cmp_gt_u32_e64 s[38:39], s18, v222
	s_waitcnt lgkmcnt(0)
	v_lshl_add_u64 v[216:217], v[216:217], 0, v[220:221]
	s_mov_b64 s[42:43], exec
	s_and_b64 exec, s[42:43], s[38:39]
	global_store_dwordx4 v[216:217], v[208:211], off sc1
	s_mov_b64 exec, s[42:43]

.LBB7_4:
	s_andn2_b64 vcc, exec, s[6:7]
	s_cbranch_vccnz .LBB7_11
	s_cmpk_gt_i32 s4, 0x1fe
	s_cbranch_scc1 .LBB7_11
	s_load_dwordx2 s[2:3], s[0:1], 0x18
	s_ashr_i32 s5, s4, 31
	s_lshl_b64 s[6:7], s[4:5], 2
	s_waitcnt lgkmcnt(0)
	s_add_u32 s2, s2, s6
	s_addc_u32 s3, s3, s7
	s_load_dword s11, s[2:3], 0x0
	s_waitcnt lgkmcnt(0)
	s_cmp_lt_i32 s11, 0
	s_cbranch_scc1 .LBB7_11
	s_load_dwordx2 s[2:3], s[0:1], 0x10
	s_lshl_b32 s4, s4, 6
	s_ashr_i32 s5, s4, 31
	s_lshl_b64 s[8:9], s[4:5], 2
	v_lshrrev_b32_e32 v1, 4, v0
	s_load_dwordx4 s[4:7], s[0:1], 0x0
	s_waitcnt lgkmcnt(0)
	s_add_u32 s2, s2, s8
	s_addc_u32 s3, s3, s9
	v_lshlrev_b32_e32 v3, 2, v1
	global_load_dword v2, v3, s[2:3]
	global_load_dword v4, v3, s[2:3] offset:128
	s_load_dwordx2 s[12:13], s[0:1], 0x20
	s_load_dwordx2 s[8:9], s[0:1], 0x30
	v_and_b32_e32 v96, 15, v0
	v_mov_b32_e32 v25, 0
	v_lshlrev_b32_e32 v24, 4, v96
	s_and_b32 s1, s11, 0xff
	v_lshl_add_u64 v[6:7], s[4:5], 0, v[24:25]
	s_lshr_b32 s4, s11, 8
	s_lshl_b32 s0, s1, 21
	s_waitcnt lgkmcnt(0)
	s_add_u32 s12, s12, s0
	s_addc_u32 s13, s13, 0
	s_lshl_b32 s0, s10, 7
	v_or_b32_e32 v8, s0, v1
	v_ashrrev_i32_e32 v9, 31, v8
	v_lshlrev_b64 v[8:9], 11, v[8:9]
	v_lshl_add_u64 v[8:9], s[12:13], 0, v[8:9]
	s_mov_b32 s14, 0x10000
	v_lshl_add_u64 v[8:9], v[8:9], 0, v[24:25]
	v_add_co_u32_e32 v10, vcc, s14, v8
	s_mov_b32 s15, 0x20000
	s_nop 0
	v_addc_co_u32_e32 v11, vcc, 0, v9, vcc
	v_add_co_u32_e32 v12, vcc, s15, v8
	s_mov_b32 s16, 0x30000
	s_nop 0
	v_addc_co_u32_e32 v13, vcc, 0, v9, vcc
	v_add_co_u32_e32 v14, vcc, s16, v8
	global_load_dwordx4 v[32:35], v[8:9], off
	s_nop 0
	v_addc_co_u32_e32 v15, vcc, 0, v9, vcc
	global_load_dwordx4 v[36:39], v[10:11], off
	global_load_dwordx4 v[40:43], v[12:13], off
	global_load_dwordx4 v[44:47], v[14:15], off
	v_bfe_u32 v30, v0, 6, 2
	v_bfe_u32 v29, v0, 4, 2
	s_movk_i32 s5, 0xf0
	s_lshl_b32 s1, s1, 12
	v_lshlrev_b32_e32 v21, 8, v96
	v_lshlrev_b32_e32 v24, 7, v30
	s_waitcnt vmcnt(5)
	v_ashrrev_i32_e32 v3, 31, v2
	s_waitcnt vmcnt(4)
	v_ashrrev_i32_e32 v5, 31, v4
	v_lshlrev_b64 v[2:3], 11, v[2:3]
	v_lshlrev_b64 v[4:5], 11, v[4:5]
	v_lshl_add_u64 v[16:17], v[6:7], 0, v[2:3]
	v_lshl_add_u64 v[18:19], v[6:7], 0, v[4:5]
	global_load_dwordx4 v[48:51], v[16:17], off
	global_load_dwordx4 v[52:55], v[18:19], off
	global_load_dwordx4 v[56:59], v[16:17], off offset:256
	global_load_dwordx4 v[60:63], v[18:19], off offset:256
	global_load_dwordx4 v[64:67], v[8:9], off offset:256
	global_load_dwordx4 v[68:71], v[10:11], off offset:256
	global_load_dwordx4 v[72:75], v[12:13], off offset:256
	global_load_dwordx4 v[76:79], v[14:15], off offset:256
	v_lshrrev_b32_e32 v2, 8, v0
	v_xor_b32_e32 v0, v1, v0
	v_lshlrev_b32_e32 v3, 8, v1
	v_lshlrev_b32_e32 v0, 4, v0
	v_and_or_b32 v0, v0, s5, v3
	s_add_u32 s5, s8, s1
	s_addc_u32 s10, s9, 0
	s_ashr_i32 s1, s0, 31
	s_lshl_b64 s[8:9], s[0:1], 2
	s_add_u32 s8, s5, s8
	v_lshlrev_b32_e32 v4, 13, v30
	v_bitop3_b32 v1, v1, v96, 3 bitop3:0x6c
	s_addc_u32 s9, s10, s9
	v_lshl_or_b32 v27, v2, 5, v96
	v_add3_u32 v97, 0, v4, v21
	v_lshlrev_b32_e32 v100, 4, v1
	v_add_u32_e32 v20, 0, v0
	v_lshl_add_u64 v[0:1], s[8:9], 0, v[24:25]
	v_lshlrev_b32_e32 v24, 4, v29
	v_lshlrev_b32_e32 v28, 2, v27
	v_add_u32_e32 v31, v97, v100
	v_lshl_add_u64 v[22:23], v[0:1], 0, v[24:25]
	v_lshlrev_b32_e32 v80, 13, v2
	global_load_dword v26, v28, s[2:3] offset:64
	global_load_dwordx4 v[4:7], v[22:23], off
	global_load_dwordx4 v[0:3], v[22:23], off offset:64
	v_bitop3_b32 v23, v29, v96, 4 bitop3:0x36
	v_lshlrev_b32_e32 v101, 4, v23
	v_add3_u32 v22, 0, v80, v21
	v_add_u32_e32 v21, v22, v100
	v_add_u32_e32 v23, v22, v101
	v_bitop3_b32 v24, v29, v96, 8 bitop3:0x36
	v_lshlrev_b32_e32 v102, 4, v24
	v_add_u32_e32 v24, v22, v102
	v_add_u32_e32 v104, 0x8000, v97
	v_add_u32_e32 v116, 0x8000, v20
	s_lshl_b64 s[0:1], s[0:1], 1
	s_add_u32 s0, s6, s0
	s_addc_u32 s1, s7, s1
	v_cmp_gt_u32_e32 vcc, s4, v27
	s_waitcnt vmcnt(14)
	ds_write_b128 v20, v[32:35] offset:32768
	s_waitcnt vmcnt(13)
	ds_write_b128 v20, v[36:39] offset:40960
	s_waitcnt vmcnt(12)
	ds_write_b128 v20, v[40:43] offset:49152
	s_waitcnt vmcnt(11)
	ds_write_b128 v20, v[44:47] offset:57344
	s_waitcnt vmcnt(10)
	ds_write_b128 v20, v[48:51]
	s_waitcnt vmcnt(9)
	ds_write_b128 v20, v[52:55] offset:8192
	s_waitcnt lgkmcnt(0)
	s_barrier
	ds_read_b128 v[34:37], v31 offset:32768
	v_add_u32_e32 v32, v97, v101
	ds_read_b128 v[38:41], v31 offset:36864
	ds_read_b128 v[42:45], v21
	ds_read_b128 v[46:49], v21 offset:4096
	ds_read_b128 v[80:83], v32 offset:32768
	ds_read_b128 v[88:91], v23
	ds_read_b128 v[92:95], v32 offset:36864
	s_waitcnt lgkmcnt(4)
	v_mfma_f32_16x16x32_f16 v[50:53], v[34:37], v[42:45], 0
	v_bitop3_b32 v33, v29, v96, 12 bitop3:0x36
	v_lshlrev_b32_e32 v103, 4, v33
	v_add_u32_e32 v33, v97, v103
	v_mfma_f32_16x16x32_f16 v[42:45], v[38:41], v[42:45], 0
	v_add_u32_e32 v22, v22, v103
	s_waitcnt lgkmcnt(3)
	v_mfma_f32_16x16x32_f16 v[84:87], v[34:37], v[46:49], 0
	v_add_u32_e32 v35, v97, v102
	v_add_u32_e32 v34, v104, v100
	v_mfma_f32_16x16x32_f16 v[36:39], v[38:41], v[46:49], 0
	ds_read_b128 v[46:49], v23 offset:4096
	s_waitcnt lgkmcnt(2)
	v_mfma_f32_16x16x32_f16 v[50:53], v[80:83], v[88:91], v[50:53]
	s_waitcnt lgkmcnt(1)
	v_mfma_f32_16x16x32_f16 v[40:43], v[92:95], v[88:91], v[42:45]
	ds_read_b128 v[88:91], v35 offset:32768
	s_waitcnt lgkmcnt(1)
	v_mfma_f32_16x16x32_f16 v[80:83], v[80:83], v[46:49], v[84:87]
	s_nop 2
	ds_read_b128 v[84:87], v24
	ds_read_b128 v[96:99], v35 offset:36864
	v_mfma_f32_16x16x32_f16 v[36:39], v[92:95], v[46:49], v[36:39]
	ds_read_b128 v[44:47], v24 offset:4096
	s_waitcnt lgkmcnt(2)
	v_mfma_f32_16x16x32_f16 v[48:51], v[88:91], v[84:87], v[50:53]
	s_nop 2
	ds_read_b128 v[52:55], v22
	ds_read_b128 v[92:95], v22 offset:4096
	s_waitcnt vmcnt(8)
	ds_write_b128 v20, v[56:59] offset:16384
	s_waitcnt lgkmcnt(4)
	v_mfma_f32_16x16x32_f16 v[40:43], v[96:99], v[84:87], v[40:43]
	ds_read_b128 v[56:59], v33 offset:32768
	ds_read_b128 v[84:87], v33 offset:36864
	s_waitcnt vmcnt(7)
	ds_write_b128 v20, v[60:63] offset:24576
	s_waitcnt vmcnt(6)
	ds_write_b128 v116, v[64:67] offset:32768
	s_waitcnt vmcnt(5)
	ds_write_b128 v116, v[68:71] offset:40960
	s_waitcnt vmcnt(4)
	ds_write_b128 v116, v[72:75] offset:49152
	s_waitcnt lgkmcnt(9)
	v_mfma_f32_16x16x32_f16 v[60:63], v[88:91], v[44:47], v[80:83]
	s_waitcnt vmcnt(3)
	ds_write_b128 v116, v[76:79] offset:57344
	v_mfma_f32_16x16x32_f16 v[36:39], v[96:99], v[44:47], v[36:39]
	global_load_dwordx4 v[44:47], v[16:17], off offset:512
	global_load_dwordx4 v[64:67], v[18:19], off offset:512
	global_load_dwordx4 v[68:71], v[8:9], off offset:512
	global_load_dwordx4 v[72:75], v[10:11], off offset:512
	global_load_dwordx4 v[76:79], v[12:13], off offset:512
	global_load_dwordx4 v[80:83], v[14:15], off offset:512
	s_waitcnt lgkmcnt(0)
	v_mfma_f32_16x16x32_f16 v[48:51], v[56:59], v[52:55], v[48:51]
	s_barrier
	v_mfma_f32_16x16x32_f16 v[40:43], v[84:87], v[52:55], v[40:43]
	v_mfma_f32_16x16x32_f16 v[52:55], v[56:59], v[92:95], v[60:63]
	ds_read_b128 v[56:59], v34 offset:32768
	s_nop 1
	ds_read_b128 v[60:63], v34 offset:36864
	v_mfma_f32_16x16x32_f16 v[84:87], v[84:87], v[92:95], v[36:39]
	s_nop 2
	ds_read_b128 v[36:39], v21 offset:16384
	ds_read_b128 v[88:91], v21 offset:20480
	s_waitcnt lgkmcnt(1)
	v_mfma_f32_16x16x32_f16 v[48:51], v[56:59], v[36:39], v[48:51]
	v_mfma_f32_16x16x32_f16 v[38:41], v[60:63], v[36:39], v[40:43]
	v_add_u32_e32 v36, v104, v101
	v_add_u32_e32 v37, v104, v102
	s_waitcnt lgkmcnt(0)
	v_mfma_f32_16x16x32_f16 v[52:55], v[56:59], v[88:91], v[52:55]
	ds_read_b128 v[56:59], v36 offset:32768
	ds_read_b128 v[92:95], v36 offset:36864
	v_mfma_f32_16x16x32_f16 v[60:63], v[60:63], v[88:91], v[84:87]
	s_nop 2
	ds_read_b128 v[84:87], v23 offset:16384
	ds_read_b128 v[88:91], v23 offset:20480
	s_waitcnt lgkmcnt(1)
	v_mfma_f32_16x16x32_f16 v[48:51], v[56:59], v[84:87], v[48:51]
	v_mfma_f32_16x16x32_f16 v[38:41], v[92:95], v[84:87], v[38:41]
	s_waitcnt lgkmcnt(0)
	v_mfma_f32_16x16x32_f16 v[52:55], v[56:59], v[88:91], v[52:55]
	ds_read_b128 v[56:59], v37 offset:32768
	ds_read_b128 v[84:87], v37 offset:36864
	v_mfma_f32_16x16x32_f16 v[60:63], v[92:95], v[88:91], v[60:63]
	ds_read_b128 v[88:91], v24 offset:16384
	ds_read_b128 v[92:95], v24 offset:20480
	s_waitcnt lgkmcnt(1)
	v_mfma_f32_16x16x32_f16 v[40:43], v[84:87], v[88:91], v[38:41]
	s_nop 2
	v_add_u32_e32 v38, v104, v103
	v_mfma_f32_16x16x32_f16 v[48:51], v[56:59], v[88:91], v[48:51]
	s_waitcnt lgkmcnt(0)
	v_mfma_f32_16x16x32_f16 v[52:55], v[56:59], v[92:95], v[52:55]
	ds_read_b128 v[56:59], v38 offset:32768
	ds_read_b128 v[88:91], v38 offset:36864
	global_load_dwordx4 v[96:99], v[16:17], off offset:768
	v_mfma_f32_16x16x32_f16 v[60:63], v[84:87], v[92:95], v[60:63]
	ds_read_b128 v[84:87], v22 offset:16384
	ds_read_b128 v[92:95], v22 offset:20480
	global_load_dwordx4 v[100:103], v[18:19], off offset:768
	global_load_dwordx4 v[104:107], v[8:9], off offset:768
	global_load_dwordx4 v[108:111], v[10:11], off offset:768
	global_load_dwordx4 v[112:115], v[12:13], off offset:768
	s_waitcnt lgkmcnt(1)
	v_mfma_f32_16x16x32_f16 v[48:51], v[56:59], v[84:87], v[48:51]
	v_mfma_f32_16x16x32_f16 v[40:43], v[88:91], v[84:87], v[40:43]
	global_load_dwordx4 v[84:87], v[14:15], off offset:768
	s_waitcnt vmcnt(11)
	ds_write_b128 v20, v[44:47]
	s_waitcnt vmcnt(10)
	ds_write_b128 v20, v[64:67] offset:8192
	s_waitcnt vmcnt(9)
	ds_write_b128 v20, v[68:71] offset:32768
	s_waitcnt vmcnt(8)
	ds_write_b128 v20, v[72:75] offset:40960
	s_waitcnt vmcnt(7)
	ds_write_b128 v20, v[76:79] offset:49152
	s_waitcnt vmcnt(6)
	ds_write_b128 v20, v[80:83] offset:57344
	s_waitcnt lgkmcnt(0)
	s_barrier
	ds_read_b128 v[44:47], v31 offset:32768
	v_mfma_f32_16x16x32_f16 v[52:55], v[56:59], v[92:95], v[52:55]
	v_mfma_f32_16x16x32_f16 v[56:59], v[88:91], v[92:95], v[60:63]
	s_nop 2
	ds_read_b128 v[60:63], v31 offset:36864
	ds_read_b128 v[64:67], v21
	ds_read_b128 v[68:71], v21 offset:4096
	s_waitcnt lgkmcnt(1)
	v_mfma_f32_16x16x32_f16 v[48:51], v[44:47], v[64:67], v[48:51]
	v_mfma_f32_16x16x32_f16 v[40:43], v[60:63], v[64:67], v[40:43]
	s_waitcnt lgkmcnt(0)
	v_mfma_f32_16x16x32_f16 v[44:47], v[44:47], v[68:71], v[52:55]
	s_nop 2
	ds_read_b128 v[52:55], v32 offset:32768
	ds_read_b128 v[64:67], v32 offset:36864
	v_mfma_f32_16x16x32_f16 v[56:59], v[60:63], v[68:71], v[56:59]
	ds_read_b128 v[60:63], v23
	ds_read_b128 v[68:71], v23 offset:4096
	s_waitcnt lgkmcnt(1)
	v_mfma_f32_16x16x32_f16 v[48:51], v[52:55], v[60:63], v[48:51]
	v_mfma_f32_16x16x32_f16 v[40:43], v[64:67], v[60:63], v[40:43]
	s_waitcnt lgkmcnt(0)
	v_mfma_f32_16x16x32_f16 v[44:47], v[52:55], v[68:71], v[44:47]
	ds_read_b128 v[52:55], v35 offset:32768
	ds_read_b128 v[60:63], v35 offset:36864
	v_mfma_f32_16x16x32_f16 v[56:59], v[64:67], v[68:71], v[56:59]
	ds_read_b128 v[64:67], v24
	ds_read_b128 v[68:71], v24 offset:4096
	ds_read_b128 v[72:75], v22
	ds_read_b128 v[76:79], v22 offset:4096
	s_waitcnt vmcnt(5)
	ds_write_b128 v20, v[96:99] offset:16384
	s_waitcnt lgkmcnt(4)
	v_mfma_f32_16x16x32_f16 v[48:51], v[52:55], v[64:67], v[48:51]
	v_mfma_f32_16x16x32_f16 v[40:43], v[60:63], v[64:67], v[40:43]
	ds_read_b128 v[64:67], v33 offset:32768
	ds_read_b128 v[80:83], v33 offset:36864
	s_waitcnt vmcnt(4)
	ds_write_b128 v20, v[100:103] offset:24576
	s_waitcnt vmcnt(3)
	ds_write_b128 v116, v[104:107] offset:32768
	s_waitcnt vmcnt(2)
	ds_write_b128 v116, v[108:111] offset:40960
	s_waitcnt vmcnt(1)
	ds_write_b128 v116, v[112:115] offset:49152
	s_waitcnt lgkmcnt(9)
	v_mfma_f32_16x16x32_f16 v[44:47], v[52:55], v[68:71], v[44:47]
	s_waitcnt vmcnt(0)
	ds_write_b128 v116, v[84:87] offset:57344
	v_mfma_f32_16x16x32_f16 v[52:55], v[60:63], v[68:71], v[56:59]
	s_nop 2
	global_load_dwordx4 v[56:59], v[16:17], off offset:1024
	global_load_dwordx4 v[60:63], v[18:19], off offset:1024
	global_load_dwordx4 v[68:71], v[8:9], off offset:1024
	global_load_dwordx4 v[84:87], v[10:11], off offset:1024
	global_load_dwordx4 v[88:91], v[12:13], off offset:1024
	global_load_dwordx4 v[92:95], v[14:15], off offset:1024
	s_waitcnt lgkmcnt(0)
	v_mfma_f32_16x16x32_f16 v[48:51], v[64:67], v[72:75], v[48:51]
	s_barrier
	v_mfma_f32_16x16x32_f16 v[40:43], v[80:83], v[72:75], v[40:43]
	v_mfma_f32_16x16x32_f16 v[44:47], v[64:67], v[76:79], v[44:47]
	ds_read_b128 v[64:67], v34 offset:32768
	ds_read_b128 v[72:75], v34 offset:36864
	v_mfma_f32_16x16x32_f16 v[52:55], v[80:83], v[76:79], v[52:55]
	ds_read_b128 v[76:79], v21 offset:16384
	ds_read_b128 v[80:83], v21 offset:20480
	s_waitcnt lgkmcnt(1)
	v_mfma_f32_16x16x32_f16 v[48:51], v[64:67], v[76:79], v[48:51]
	v_mfma_f32_16x16x32_f16 v[40:43], v[72:75], v[76:79], v[40:43]
	s_waitcnt lgkmcnt(0)
	v_mfma_f32_16x16x32_f16 v[44:47], v[64:67], v[80:83], v[44:47]
	ds_read_b128 v[64:67], v36 offset:32768
	ds_read_b128 v[76:79], v36 offset:36864
	v_mfma_f32_16x16x32_f16 v[52:55], v[72:75], v[80:83], v[52:55]
	ds_read_b128 v[72:75], v23 offset:16384
	ds_read_b128 v[80:83], v23 offset:20480
	s_waitcnt lgkmcnt(1)
	v_mfma_f32_16x16x32_f16 v[48:51], v[64:67], v[72:75], v[48:51]
	v_mfma_f32_16x16x32_f16 v[40:43], v[76:79], v[72:75], v[40:43]
	s_waitcnt lgkmcnt(0)
	v_mfma_f32_16x16x32_f16 v[44:47], v[64:67], v[80:83], v[44:47]
	ds_read_b128 v[64:67], v37 offset:32768
	ds_read_b128 v[72:75], v37 offset:36864
	v_mfma_f32_16x16x32_f16 v[52:55], v[76:79], v[80:83], v[52:55]
	ds_read_b128 v[76:79], v24 offset:16384
	ds_read_b128 v[80:83], v24 offset:20480
	s_waitcnt lgkmcnt(1)
	v_mfma_f32_16x16x32_f16 v[48:51], v[64:67], v[76:79], v[48:51]
	v_mfma_f32_16x16x32_f16 v[40:43], v[72:75], v[76:79], v[40:43]
	s_waitcnt lgkmcnt(0)
	v_mfma_f32_16x16x32_f16 v[44:47], v[64:67], v[80:83], v[44:47]
	ds_read_b128 v[64:67], v38 offset:32768
	ds_read_b128 v[76:79], v22 offset:16384
	ds_read_b128 v[96:99], v38 offset:36864
	global_load_dwordx4 v[100:103], v[10:11], off offset:1280
	v_mfma_f32_16x16x32_f16 v[52:55], v[72:75], v[80:83], v[52:55]
	global_load_dwordx4 v[72:75], v[8:9], off offset:1280
	ds_read_b128 v[80:83], v22 offset:20480
	global_load_dwordx4 v[104:107], v[12:13], off offset:1280
	global_load_dwordx4 v[108:111], v[14:15], off offset:1280
	s_waitcnt lgkmcnt(2)
	v_mfma_f32_16x16x32_f16 v[48:51], v[64:67], v[76:79], v[48:51]
	s_waitcnt lgkmcnt(1)
	v_mfma_f32_16x16x32_f16 v[40:43], v[96:99], v[76:79], v[40:43]
	global_load_dwordx4 v[76:79], v[16:17], off offset:1280
	global_load_dwordx4 v[112:115], v[18:19], off offset:1280
	s_waitcnt vmcnt(11)
	ds_write_b128 v20, v[56:59]
	s_waitcnt vmcnt(10)
	ds_write_b128 v20, v[60:63] offset:8192
	s_waitcnt vmcnt(9)
	ds_write_b128 v20, v[68:71] offset:32768
	s_waitcnt vmcnt(8)
	ds_write_b128 v20, v[84:87] offset:40960
	s_waitcnt vmcnt(7)
	ds_write_b128 v20, v[88:91] offset:49152
	s_waitcnt vmcnt(6)
	ds_write_b128 v20, v[92:95] offset:57344
	s_waitcnt lgkmcnt(0)
	s_barrier
	ds_read_b128 v[56:59], v31 offset:32768
	v_mfma_f32_16x16x32_f16 v[44:47], v[64:67], v[80:83], v[44:47]
	ds_read_b128 v[60:63], v31 offset:36864
	ds_read_b128 v[64:67], v21
	ds_read_b128 v[68:71], v21 offset:4096
	v_mfma_f32_16x16x32_f16 v[52:55], v[96:99], v[80:83], v[52:55]
	s_waitcnt lgkmcnt(1)
	v_mfma_f32_16x16x32_f16 v[48:51], v[56:59], v[64:67], v[48:51]
	v_mfma_f32_16x16x32_f16 v[40:43], v[60:63], v[64:67], v[40:43]
	s_waitcnt lgkmcnt(0)
	v_mfma_f32_16x16x32_f16 v[44:47], v[56:59], v[68:71], v[44:47]
	ds_read_b128 v[56:59], v32 offset:32768
	ds_read_b128 v[64:67], v32 offset:36864
	v_mfma_f32_16x16x32_f16 v[52:55], v[60:63], v[68:71], v[52:55]
	ds_read_b128 v[60:63], v23
	ds_read_b128 v[68:71], v23 offset:4096
	s_waitcnt lgkmcnt(1)
	v_mfma_f32_16x16x32_f16 v[48:51], v[56:59], v[60:63], v[48:51]
	v_mfma_f32_16x16x32_f16 v[40:43], v[64:67], v[60:63], v[40:43]
	s_waitcnt lgkmcnt(0)
	v_mfma_f32_16x16x32_f16 v[44:47], v[56:59], v[68:71], v[44:47]
	ds_read_b128 v[56:59], v35 offset:32768
	ds_read_b128 v[60:63], v35 offset:36864
	v_mfma_f32_16x16x32_f16 v[52:55], v[64:67], v[68:71], v[52:55]
	ds_read_b128 v[64:67], v24
	ds_read_b128 v[68:71], v24 offset:4096
	s_waitcnt vmcnt(4)
	ds_write_b128 v116, v[72:75] offset:32768
	s_waitcnt lgkmcnt(2)
	v_mfma_f32_16x16x32_f16 v[48:51], v[56:59], v[64:67], v[48:51]
	v_mfma_f32_16x16x32_f16 v[40:43], v[60:63], v[64:67], v[40:43]
	ds_read_b128 v[64:67], v33 offset:32768
	s_waitcnt lgkmcnt(2)
	v_mfma_f32_16x16x32_f16 v[44:47], v[56:59], v[68:71], v[44:47]
	ds_read_b128 v[56:59], v22
	ds_read_b128 v[72:75], v33 offset:36864
	ds_write_b128 v116, v[100:103] offset:40960
	s_waitcnt vmcnt(3)
	ds_write_b128 v116, v[104:107] offset:49152
	v_mfma_f32_16x16x32_f16 v[52:55], v[60:63], v[68:71], v[52:55]
	ds_read_b128 v[60:63], v22 offset:4096
	s_waitcnt vmcnt(2)
	ds_write_b128 v116, v[108:111] offset:57344
	s_waitcnt vmcnt(1)
	ds_write_b128 v20, v[76:79] offset:16384
	s_waitcnt vmcnt(0)
	ds_write_b128 v20, v[112:115] offset:24576
	s_waitcnt lgkmcnt(7)
	v_mfma_f32_16x16x32_f16 v[48:51], v[64:67], v[56:59], v[48:51]
	s_waitcnt lgkmcnt(6)
	v_mfma_f32_16x16x32_f16 v[40:43], v[72:75], v[56:59], v[40:43]
	global_load_dwordx4 v[56:59], v[16:17], off offset:1536
	global_load_dwordx4 v[68:71], v[18:19], off offset:1536
	global_load_dwordx4 v[76:79], v[8:9], off offset:1536
	global_load_dwordx4 v[80:83], v[10:11], off offset:1536
	s_waitcnt lgkmcnt(3)
	v_mfma_f32_16x16x32_f16 v[44:47], v[64:67], v[60:63], v[44:47]
	global_load_dwordx4 v[64:67], v[12:13], off offset:1536
	global_load_dwordx4 v[84:87], v[14:15], off offset:1536
	s_waitcnt lgkmcnt(0)
	s_barrier
	ds_read_b128 v[88:91], v34 offset:32768
	v_mfma_f32_16x16x32_f16 v[52:55], v[72:75], v[60:63], v[52:55]
	ds_read_b128 v[60:63], v34 offset:36864
	ds_read_b128 v[72:75], v21 offset:16384
	ds_read_b128 v[92:95], v21 offset:20480
	s_waitcnt lgkmcnt(1)
	v_mfma_f32_16x16x32_f16 v[48:51], v[88:91], v[72:75], v[48:51]
	v_mfma_f32_16x16x32_f16 v[40:43], v[60:63], v[72:75], v[40:43]
	ds_read_b128 v[72:75], v36 offset:32768
	s_waitcnt lgkmcnt(1)
	v_mfma_f32_16x16x32_f16 v[44:47], v[88:91], v[92:95], v[44:47]
	v_mfma_f32_16x16x32_f16 v[52:55], v[60:63], v[92:95], v[52:55]
	ds_read_b128 v[60:63], v36 offset:36864
	ds_read_b128 v[88:91], v23 offset:16384
	ds_read_b128 v[92:95], v23 offset:20480
	s_waitcnt lgkmcnt(1)
	v_mfma_f32_16x16x32_f16 v[48:51], v[72:75], v[88:91], v[48:51]
	v_mfma_f32_16x16x32_f16 v[40:43], v[60:63], v[88:91], v[40:43]
	s_waitcnt lgkmcnt(0)
	v_mfma_f32_16x16x32_f16 v[44:47], v[72:75], v[92:95], v[44:47]
	ds_read_b128 v[72:75], v37 offset:32768
	ds_read_b128 v[88:91], v37 offset:36864
	v_mfma_f32_16x16x32_f16 v[52:55], v[60:63], v[92:95], v[52:55]
	ds_read_b128 v[60:63], v24 offset:16384
	ds_read_b128 v[92:95], v24 offset:20480
	s_waitcnt lgkmcnt(1)
	v_mfma_f32_16x16x32_f16 v[48:51], v[72:75], v[60:63], v[48:51]
	v_mfma_f32_16x16x32_f16 v[40:43], v[88:91], v[60:63], v[40:43]
	s_waitcnt lgkmcnt(0)
	v_mfma_f32_16x16x32_f16 v[44:47], v[72:75], v[92:95], v[44:47]
	ds_read_b128 v[60:63], v38 offset:32768
	ds_read_b128 v[72:75], v38 offset:36864
	v_mfma_f32_16x16x32_f16 v[52:55], v[88:91], v[92:95], v[52:55]
	ds_read_b128 v[88:91], v22 offset:16384
	ds_read_b128 v[92:95], v22 offset:20480
	global_load_dwordx4 v[96:99], v[16:17], off offset:1792
	global_load_dwordx4 v[100:103], v[18:19], off offset:1792
	s_waitcnt lgkmcnt(1)
	v_mfma_f32_16x16x32_f16 v[48:51], v[60:63], v[88:91], v[48:51]
	v_mfma_f32_16x16x32_f16 v[16:19], v[72:75], v[88:91], v[40:43]
	s_nop 2
	global_load_dwordx4 v[40:43], v[8:9], off offset:1792
	global_load_dwordx4 v[88:91], v[10:11], off offset:1792
	global_load_dwordx4 v[104:107], v[12:13], off offset:1792
	global_load_dwordx4 v[108:111], v[14:15], off offset:1792
	s_waitcnt vmcnt(11)
	ds_write_b128 v20, v[56:59]
	s_waitcnt vmcnt(10)
	ds_write_b128 v20, v[68:71] offset:8192
	s_waitcnt vmcnt(9)
	ds_write_b128 v20, v[76:79] offset:32768
	s_waitcnt vmcnt(8)
	ds_write_b128 v20, v[80:83] offset:40960
	s_waitcnt vmcnt(7)
	ds_write_b128 v20, v[64:67] offset:49152
	s_waitcnt vmcnt(6)
	ds_write_b128 v20, v[84:87] offset:57344
	s_waitcnt lgkmcnt(0)
	s_barrier
	ds_read_b128 v[12:15], v31 offset:32768
	v_mfma_f32_16x16x32_f16 v[8:11], v[60:63], v[92:95], v[44:47]
	v_mfma_f32_16x16x32_f16 v[44:47], v[72:75], v[92:95], v[52:55]
	s_nop 2
	ds_read_b128 v[52:55], v31 offset:36864
	ds_read_b128 v[56:59], v21
	ds_read_b128 v[60:63], v21 offset:4096
	s_waitcnt lgkmcnt(1)
	v_mfma_f32_16x16x32_f16 v[48:51], v[12:15], v[56:59], v[48:51]
	v_mfma_f32_16x16x32_f16 v[16:19], v[52:55], v[56:59], v[16:19]
	s_waitcnt lgkmcnt(0)
	v_mfma_f32_16x16x32_f16 v[8:11], v[12:15], v[60:63], v[8:11]
	ds_read_b128 v[12:15], v32 offset:32768
	ds_read_b128 v[56:59], v32 offset:36864
	v_mfma_f32_16x16x32_f16 v[44:47], v[52:55], v[60:63], v[44:47]
	ds_read_b128 v[52:55], v23
	ds_read_b128 v[60:63], v23 offset:4096
	s_waitcnt lgkmcnt(1)
	v_mfma_f32_16x16x32_f16 v[48:51], v[12:15], v[52:55], v[48:51]
	v_mfma_f32_16x16x32_f16 v[16:19], v[56:59], v[52:55], v[16:19]
	s_waitcnt lgkmcnt(0)
	v_mfma_f32_16x16x32_f16 v[8:11], v[12:15], v[60:63], v[8:11]
	ds_read_b128 v[12:15], v35 offset:32768
	ds_read_b128 v[52:55], v35 offset:36864
	v_mfma_f32_16x16x32_f16 v[44:47], v[56:59], v[60:63], v[44:47]
	ds_read_b128 v[56:59], v24
	ds_read_b128 v[60:63], v24 offset:4096
	s_waitcnt lgkmcnt(1)
	v_mfma_f32_16x16x32_f16 v[48:51], v[12:15], v[56:59], v[48:51]
	s_waitcnt lgkmcnt(0)
	v_mfma_f32_16x16x32_f16 v[8:11], v[12:15], v[60:63], v[8:11]
	ds_read_b128 v[12:15], v33 offset:32768
	v_mfma_f32_16x16x32_f16 v[16:19], v[52:55], v[56:59], v[16:19]
	v_mfma_f32_16x16x32_f16 v[44:47], v[52:55], v[60:63], v[44:47]
	ds_read_b128 v[52:55], v33 offset:36864
	ds_read_b128 v[56:59], v22
	ds_read_b128 v[60:63], v22 offset:4096
	s_waitcnt vmcnt(5)
	ds_write_b128 v20, v[96:99] offset:16384
	s_waitcnt vmcnt(4)
	ds_write_b128 v20, v[100:103] offset:24576
	s_waitcnt lgkmcnt(3)
	v_mfma_f32_16x16x32_f16 v[48:51], v[12:15], v[56:59], v[48:51]
	s_waitcnt lgkmcnt(2)
	v_mfma_f32_16x16x32_f16 v[8:11], v[12:15], v[60:63], v[8:11]
	v_add_u32_e32 v12, 0x10000, v20
	s_waitcnt vmcnt(3)
	ds_write_b128 v12, v[40:43]
	s_waitcnt vmcnt(2)
	ds_write_b128 v12, v[88:91] offset:8192
	s_waitcnt vmcnt(1)
	ds_write_b128 v12, v[104:107] offset:16384
	s_waitcnt vmcnt(0)
	ds_write_b128 v12, v[108:111] offset:24576
	s_waitcnt lgkmcnt(0)
	s_barrier
	ds_read_b128 v[12:15], v34 offset:32768
	v_mfma_f32_16x16x32_f16 v[16:19], v[52:55], v[56:59], v[16:19]
	v_mfma_f32_16x16x32_f16 v[40:43], v[52:55], v[60:63], v[44:47]
	ds_read_b128 v[32:35], v34 offset:36864
	s_nop 1
	ds_read_b128 v[44:47], v21 offset:16384
	ds_read_b128 v[52:55], v21 offset:20480
	s_waitcnt lgkmcnt(1)
	v_mfma_f32_16x16x32_f16 v[48:51], v[12:15], v[44:47], v[48:51]
	s_waitcnt lgkmcnt(0)
	v_mfma_f32_16x16x32_f16 v[8:11], v[12:15], v[52:55], v[8:11]
	ds_read_b128 v[12:15], v36 offset:32768
	v_mfma_f32_16x16x32_f16 v[16:19], v[32:35], v[44:47], v[16:19]
	v_mfma_f32_16x16x32_f16 v[32:35], v[32:35], v[52:55], v[40:43]
	s_nop 2
	ds_read_b128 v[40:43], v36 offset:36864
	ds_read_b128 v[44:47], v23 offset:16384
	ds_read_b128 v[52:55], v23 offset:20480
	s_waitcnt lgkmcnt(1)
	v_mfma_f32_16x16x32_f16 v[48:51], v[12:15], v[44:47], v[48:51]
	s_waitcnt lgkmcnt(0)
	v_mfma_f32_16x16x32_f16 v[8:11], v[12:15], v[52:55], v[8:11]
	ds_read_b128 v[12:15], v37 offset:32768
	v_mfma_f32_16x16x32_f16 v[16:19], v[40:43], v[44:47], v[16:19]
	v_mfma_f32_16x16x32_f16 v[32:35], v[40:43], v[52:55], v[32:35]
	ds_read_b128 v[40:43], v37 offset:36864
	ds_read_b128 v[44:47], v24 offset:16384
	ds_read_b128 v[52:55], v24 offset:20480
	v_lshlrev_b32_e32 v24, 6, v30
	s_waitcnt lgkmcnt(1)
	v_mfma_f32_16x16x32_f16 v[48:51], v[12:15], v[44:47], v[48:51]
	s_waitcnt lgkmcnt(0)
	v_mfma_f32_16x16x32_f16 v[8:11], v[12:15], v[52:55], v[8:11]
	ds_read_b128 v[12:15], v38 offset:32768
	v_mfma_f32_16x16x32_f16 v[16:19], v[40:43], v[44:47], v[16:19]
	v_mfma_f32_16x16x32_f16 v[32:35], v[40:43], v[52:55], v[32:35]
	ds_read_b128 v[36:39], v38 offset:36864
	ds_read_b128 v[40:43], v22 offset:16384
	ds_read_b128 v[44:47], v22 offset:20480
	s_waitcnt lgkmcnt(1)
	v_mfma_f32_16x16x32_f16 v[20:23], v[12:15], v[40:43], v[48:51]
	s_waitcnt lgkmcnt(0)
	v_mfma_f32_16x16x32_f16 v[12:15], v[12:15], v[44:47], v[8:11]
	s_nop 2
	v_lshl_add_u64 v[8:9], s[0:1], 0, v[24:25]
	v_lshlrev_b32_e32 v24, 3, v29
	v_mfma_f32_16x16x32_f16 v[16:19], v[36:39], v[40:43], v[16:19]
	v_lshl_add_u64 v[30:31], v[8:9], 0, v[24:25]
	v_mfma_f32_16x16x32_f16 v[8:11], v[36:39], v[44:47], v[32:35]
	v_mbcnt_lo_u32_b32 v196, -1, 0
	v_mbcnt_hi_u32_b32 v196, -1, v196
	v_and_b32_e32 v197, 15, v196
	v_lshrrev_b32_e32 v198, 4, v196
	v_lshrrev_b32_e32 v222, 10, v116
	s_nop 0
	v_readfirstlane_b32 s36, v222
	s_nop 3
	s_and_b32 s36, s36, 7
	s_mulk_i32 s36, 0x500
	s_add_u32 s36, s36, 0x8000
	v_mul_u32_u24_e32 v199, 0x50, v197
	v_lshl_add_u32 v199, v198, 3, v199
	v_add_u32_e32 v199, s36, v199
	v_lshrrev_b32_e32 v200, 2, v196
	v_and_b32_e32 v201, 3, v196
	v_mul_u32_u24_e32 v202, 0x50, v200
	v_lshl_add_u32 v202, v201, 4, v202
	v_add_u32_e32 v202, s36, v202
	v_lshlrev_b32_e32 v203, 2, v200
	v_add_u32_e32 v204, 32, v203
	v_lshlrev_b32_e32 v220, 4, v201
	v_mov_b32_e32 v221, 0
	v_sub_u32_e32 v205, v27, v197
	v_add_u32_e32 v205, v205, v200
	s_mov_b64 s[0:1], exec
	s_cbranch_execz .LBB7_9
	v_mov_b32_e32 v29, v25
	v_lshl_add_u64 v[24:25], s[2:3], 0, v[28:29]
	global_load_dword v24, v[24:25], off
	s_nop 0
	v_add_f32_e32 v16, v0, v16
	v_add_f32_e32 v17, v1, v17
	v_add_f32_e32 v18, v2, v18
	v_add_f32_e32 v19, v3, v19
	v_add_f32_e32 v20, v4, v20
	v_add_f32_e32 v21, v5, v21
	v_max_f32_e32 v25, 0, v16
	v_max_f32_e32 v28, 0, v17
	v_max_f32_e32 v18, 0, v18
	v_max_f32_e32 v19, 0, v19
	v_add_f32_e32 v22, v6, v22
	v_add_f32_e32 v23, v7, v23
	v_max_f32_e32 v20, 0, v20
	v_max_f32_e32 v21, 0, v21
	v_cvt_pk_f16_f32 v19, v18, v19
	v_cvt_pk_f16_f32 v18, v25, v28
	v_max_f32_e32 v22, 0, v22
	v_max_f32_e32 v23, 0, v23
	v_cvt_pk_f16_f32 v16, v20, v21
	v_cvt_pk_f16_f32 v17, v22, v23
	s_waitcnt vmcnt(0)
	v_ashrrev_i32_e32 v25, 31, v24
	v_lshlrev_b64 v[20:21], 11, v[24:25]
	v_lshl_add_u64 v[20:21], v[30:31], 0, v[20:21]
	ds_write_b64 v199, v[16:17]
	ds_write_b64 v199, v[18:19] offset:32
	ds_read_b128 v[208:211], v202
	ds_bpermute_b32 v216, v203, v20
	ds_bpermute_b32 v217, v203, v21
	v_add_u32_e32 v222, 0, v205
	v_cmp_gt_u32_e64 s[38:39], s4, v222
.LBB7_9:
	s_or_b64 exec, exec, s[0:1]
	s_nop 2
	v_or_b32_e32 v16, 16, v27
	v_cmp_gt_u32_e32 vcc, s4, v16
	s_mov_b64 s[0:1], exec
	s_cbranch_execz .LBB7_11
	v_add_f32_e32 v5, v5, v13
	v_ashrrev_i32_e32 v27, 31, v26
	v_add_f32_e32 v4, v4, v12
	v_max_f32_e32 v12, 0, v5
	v_add_f32_e32 v5, v6, v14
	v_add_f32_e32 v6, v7, v15
	v_lshlrev_b64 v[16:17], 11, v[26:27]
	v_max_f32_e32 v4, 0, v4
	v_max_f32_e32 v5, 0, v5
	v_max_f32_e32 v6, 0, v6
	v_lshl_add_u64 v[16:17], v[30:31], 0, v[16:17]
	v_cvt_pk_f16_f32 v5, v5, v6
	v_cvt_pk_f16_f32 v4, v4, v12
	v_add_f32_e32 v1, v1, v9
	ds_write_b64 v199, v[4:5]
	v_add_f32_e32 v0, v0, v8
	v_max_f32_e32 v4, 0, v1
	v_add_f32_e32 v1, v2, v10
	v_add_f32_e32 v2, v3, v11
	v_max_f32_e32 v0, 0, v0
	v_max_f32_e32 v1, 0, v1
	v_max_f32_e32 v2, 0, v2
	v_cvt_pk_f16_f32 v1, v1, v2
	v_cvt_pk_f16_f32 v0, v0, v4
	ds_write_b64 v199, v[0:1] offset:32
	s_waitcnt lgkmcnt(2)
	v_lshl_add_u64 v[216:217], v[216:217], 0, v[220:221]
	s_mov_b64 s[42:43], exec
	s_and_b64 exec, s[42:43], s[38:39]
	global_store_dwordx4 v[216:217], v[208:211], off sc1
	s_mov_b64 exec, s[42:43]
	ds_read_b128 v[208:211], v202
	ds_bpermute_b32 v216, v203, v16
	ds_bpermute_b32 v217, v203, v17
	v_add_u32_e32 v222, 16, v205
	v_cmp_gt_u32_e64 s[38:39], s4, v222
	s_waitcnt lgkmcnt(0)
	v_lshl_add_u64 v[216:217], v[216:217], 0, v[220:221]
	s_mov_b64 s[42:43], exec
	s_and_b64 exec, s[42:43], s[38:39]
	global_store_dwordx4 v[216:217], v[208:211], off sc1
	s_mov_b64 exec, s[42:43]
